# all s_setprio toggles removed from the GEMM K-loops (both wave halves at priority 0)
# baseline (speedup 1.0000x reference)
; #define PG8_STAGE(bufoff, gbase, voff) do { _Pragma("unroll") for (int _i = 0; _i < 2; ++_i) \
;         __builtin_amdgcn_global_load_lds((const unsigned*)((const char*)(gbase) + (voff)[_i]), (PG8_LAS unsigned*)(lds + (bufoff) + ldsw + _i * 8192), 16, 0, 0); } while (0)
; #define PG8_WAIT_V(n) asm volatile("s_waitcnt vmcnt(" #n ")" ::: "memory")
; #define PG8_WAIT_L(n) asm volatile("s_waitcnt lgkmcnt(" #n ")" ::: "memory")
; #define PG8_BAR __builtin_amdgcn_s_barrier()
; #define PG8_SCHED __builtin_amdgcn_sched_barrier(0)
; template <class Epi, class Sched, bool ALIGN_EPI = false, bool SP2 = false, bool FP8 = false, bool PEEL = false>
; __device__ __forceinline__ void gemm_phase(PG8_LAS unsigned char* lds, const Gemm g, const Sched& S, const Epi& E, const int wid) {
;     ...
;             PG8_LDB(B0, 0, 0); PG8_LDB(B1, 0, 1); PG8_SCHED; PG8_LDA(At, 0, 0); PG8_STAGE(PG8_SA(1, 1), a1 + hstep, voffA);
;             PG8_WAIT_V(8); PG8_WAIT_L(0); PG8_BAR; PG8_MMAZ(0, 0, At, B0); PG8_MMAZ(0, 1, At, B1); PG8_BAR; PG8_SCHED;
;             PG8_LDA(At, 0, 1); PG8_STAGE(PG8_SB(0, 0), b2, voffB); PG8_STAGE(PG8_SB(0, 1), b2 + hstep, voffB); PG8_STAGE(PG8_SA(0, 0), a2, voffA);
;             PG8_WAIT_V(8); PG8_WAIT_L(0); PG8_BAR; PG8_MMAZ(1, 0, At, B0); PG8_MMAZ(1, 1, At, B1); PG8_BAR; PG8_SCHED;
.LBB0_236:
	s_ashr_i32 s23, s22, 31
	s_lshl_b64 s[24:25], s[22:23], 19
	s_add_u32 s24, s34, s24
	ds_read_b128 v[0:3], v153
	ds_read_b128 v[4:7], v153 offset:1024
	ds_read_b128 v[8:11], v153 offset:2048
	ds_read_b128 v[12:15], v153 offset:3072
	ds_read_b128 v[16:19], v154
	ds_read_b128 v[20:23], v154 offset:1024
	ds_read_b128 v[24:27], v154 offset:2048
	ds_read_b128 v[28:31], v154 offset:3072
	s_addc_u32 s25, s35, s25
	s_ashr_i32 s21, s20, 31
	s_lshl_b64 s[26:27], s[20:21], 19
	s_add_u32 s26, s42, s26
	s_addc_u32 s27, s43, s27
	s_and_b64 s[40:41], s[10:11], exec
	s_cselect_b32 s13, s25, s37
	s_cselect_b32 s21, s24, s36
	s_cselect_b32 s23, s27, s31
	s_cselect_b32 s60, s26, s30
	s_add_u32 s40, s36, 0x40080
	s_addc_u32 s41, s37, 0
	s_add_i32 s61, s44, 0xc000
	v_lshl_add_u64 v[64:65], s[40:41], 0, v[128:129]
	s_mov_b32 m0, s61
	s_add_i32 s62, s44, 0xe000
	ds_read_b128 v[32:35], v155
	ds_read_b128 v[36:39], v155 offset:1024
	ds_read_b128 v[40:43], v155 offset:2048
	ds_read_b128 v[44:47], v155 offset:3072
	ds_read_b128 v[48:51], v155 offset:4096
	ds_read_b128 v[52:55], v155 offset:5120
	ds_read_b128 v[56:59], v155 offset:6144
	ds_read_b128 v[60:63], v155 offset:7168
	global_load_lds_dwordx4 v[64:65], off
	v_lshl_add_u64 v[64:65], s[40:41], 0, v[132:133]
	s_mov_b32 m0, s62
	s_nop 0
	global_load_lds_dwordx4 v[64:65], off
	s_waitcnt vmcnt(8)
	s_waitcnt lgkmcnt(0)
	s_barrier
	s_waitcnt lgkmcnt(0)
	v_mfma_f32_16x16x32_bf16 v[88:91], v[0:3], v[56:59], 0
	v_mfma_f32_16x16x32_bf16 v[64:67], v[0:3], v[32:35], 0
	v_mfma_f32_16x16x32_bf16 v[68:71], v[8:11], v[32:35], 0
	v_mfma_f32_16x16x32_bf16 v[72:75], v[0:3], v[40:43], 0
	v_mfma_f32_16x16x32_bf16 v[76:79], v[8:11], v[40:43], 0
	v_mfma_f32_16x16x32_bf16 v[80:83], v[0:3], v[48:51], 0
	v_mfma_f32_16x16x32_bf16 v[84:87], v[8:11], v[48:51], 0
	v_mfma_f32_16x16x32_bf16 v[96:99], v[4:7], v[60:63], v[88:91]
	v_mfma_f32_16x16x32_bf16 v[88:91], v[8:11], v[56:59], 0
	v_mfma_f32_16x16x32_bf16 v[64:67], v[4:7], v[36:39], v[64:67]
	v_mfma_f32_16x16x32_bf16 v[68:71], v[12:15], v[36:39], v[68:71]
	v_mfma_f32_16x16x32_bf16 v[72:75], v[4:7], v[44:47], v[72:75]
	v_mfma_f32_16x16x32_bf16 v[76:79], v[12:15], v[44:47], v[76:79]
	v_mfma_f32_16x16x32_bf16 v[80:83], v[4:7], v[52:55], v[80:83]
	v_mfma_f32_16x16x32_bf16 v[84:87], v[12:15], v[52:55], v[84:87]
	v_mfma_f32_16x16x32_bf16 v[100:103], v[12:15], v[60:63], v[88:91]
	v_mfma_f32_16x16x32_bf16 v[88:91], v[16:19], v[32:35], 0
	v_mfma_f32_16x16x32_bf16 v[32:35], v[24:27], v[32:35], 0
	v_mfma_f32_16x16x32_bf16 v[112:115], v[20:23], v[36:39], v[88:91]
	v_mfma_f32_16x16x32_bf16 v[32:35], v[28:31], v[36:39], v[32:35]
	v_mfma_f32_16x16x32_bf16 v[36:39], v[16:19], v[40:43], 0
	v_mfma_f32_16x16x32_bf16 v[40:43], v[24:27], v[40:43], 0
	v_mfma_f32_16x16x32_bf16 v[36:39], v[20:23], v[44:47], v[36:39]
	v_mfma_f32_16x16x32_bf16 v[40:43], v[28:31], v[44:47], v[40:43]
	v_mfma_f32_16x16x32_bf16 v[44:47], v[16:19], v[48:51], 0
	v_mfma_f32_16x16x32_bf16 v[48:51], v[24:27], v[48:51], 0
	v_mfma_f32_16x16x32_bf16 v[44:47], v[20:23], v[52:55], v[44:47]
	v_mfma_f32_16x16x32_bf16 v[48:51], v[28:31], v[52:55], v[48:51]
	v_mfma_f32_16x16x32_bf16 v[52:55], v[16:19], v[56:59], 0
	v_mfma_f32_16x16x32_bf16 v[56:59], v[24:27], v[56:59], 0
	v_mfma_f32_16x16x32_bf16 v[52:55], v[20:23], v[60:63], v[52:55]
	v_mfma_f32_16x16x32_bf16 v[56:59], v[28:31], v[60:63], v[56:59]
	s_barrier
	s_add_i32 s63, s56, s3
	v_lshl_add_u64 v[250:251], s[30:31], 0, v[130:131]
	s_add_i32 s64, s63, 0x2000
	v_lshl_add_u64 v[144:145], v[250:251], 0, s[16:17]
	s_mov_b32 m0, s63
	v_lshl_add_u64 v[252:253], s[30:31], 0, v[134:135]
	s_add_u32 s40, s30, 0x40100
	ds_read_b128 v[60:63], v155 offset:16384
	ds_read_b128 v[88:91], v155 offset:17408
	ds_read_b128 v[92:95], v155 offset:18432
	ds_read_b128 v[104:107], v155 offset:19456
	ds_read_b128 v[108:111], v155 offset:20480
	ds_read_b128 v[116:119], v155 offset:21504
	ds_read_b128 v[120:123], v155 offset:22528
	ds_read_b128 v[124:127], v155 offset:23552
	global_load_lds_dwordx4 v[144:145], off
	v_lshl_add_u64 v[144:145], v[252:253], 0, s[16:17]
	s_mov_b32 m0, s64
	s_addc_u32 s41, s31, 0
	s_add_i32 s65, s57, s3
	global_load_lds_dwordx4 v[144:145], off
	v_lshl_add_u64 v[144:145], s[40:41], 0, v[130:131]
	s_mov_b32 m0, s65
	s_add_i32 s66, s65, 0x2000
	global_load_lds_dwordx4 v[144:145], off
	v_lshl_add_u64 v[144:145], s[40:41], 0, v[134:135]
	s_mov_b32 m0, s66
	v_lshl_add_u64 v[140:141], s[36:37], 0, v[128:129]
	global_load_lds_dwordx4 v[144:145], off
	v_lshl_add_u64 v[144:145], v[140:141], 0, s[16:17]
	s_mov_b32 m0, s44
	v_lshl_add_u64 v[142:143], s[36:37], 0, v[132:133]
	global_load_lds_dwordx4 v[144:145], off
	v_lshl_add_u64 v[144:145], v[142:143], 0, s[16:17]
	s_mov_b32 m0, s45
	s_nop 0
	global_load_lds_dwordx4 v[144:145], off
	s_waitcnt vmcnt(8)
	s_waitcnt lgkmcnt(0)
	s_barrier
; #define PG8_STAGE(bufoff, gbase, voff) do { _Pragma("unroll") for (int _i = 0; _i < 2; ++_i) \
;         __builtin_amdgcn_global_load_lds((const unsigned*)((const char*)(gbase) + (voff)[_i]), (PG8_LAS unsigned*)(lds + (bufoff) + ldsw + _i * 8192), 16, 0, 0); } while (0)
; #define PG8_WAIT_V(n) asm volatile("s_waitcnt vmcnt(" #n ")" ::: "memory")
; #define PG8_WAIT_L(n) asm volatile("s_waitcnt lgkmcnt(" #n ")" ::: "memory")
; #define PG8_BAR __builtin_amdgcn_s_barrier()
; #define PG8_SCHED __builtin_amdgcn_sched_barrier(0)
; template <class Epi, class Sched, bool ALIGN_EPI = false, bool SP2 = false, bool FP8 = false, bool PEEL = false>
; __device__ __forceinline__ void gemm_phase(PG8_LAS unsigned char* lds, const Gemm g, const Sched& S, const Epi& E, const int wid) {
;     ...
;             PG8_WAIT_V(8); PG8_WAIT_L(0); PG8_BAR; PG8_MMAZ(1, 0, At, B0); PG8_MMAZ(1, 1, At, B1); PG8_BAR; PG8_SCHED;
;             PG8_LDB(B0, 1, 0); PG8_LDB(B1, 1, 1); PG8_SCHED; PG8_LDA(At, 1, 0); PG8_STAGE(PG8_SA(0, 1), a2 + hstep, voffA);
;             PG8_WAIT_V(8); PG8_WAIT_L(0); PG8_BAR; PG8_MMA(0, 0, At, B0); PG8_MMA(0, 1, At, B1); PG8_BAR; PG8_SCHED;
	s_waitcnt lgkmcnt(0)
	v_mfma_f32_16x16x32_bf16 v[144:147], v[0:3], v[60:63], 0
	v_mfma_f32_16x16x32_bf16 v[162:165], v[0:3], v[92:95], 0
	v_mfma_f32_16x16x32_bf16 v[170:173], v[0:3], v[108:111], 0
	v_mfma_f32_16x16x32_bf16 v[0:3], v[0:3], v[120:123], 0
	v_mfma_f32_16x16x32_bf16 v[146:149], v[4:7], v[88:91], v[144:147]
	v_mfma_f32_16x16x32_bf16 v[162:165], v[4:7], v[104:107], v[162:165]
	v_mfma_f32_16x16x32_bf16 v[170:173], v[4:7], v[116:119], v[170:173]
	v_mfma_f32_16x16x32_bf16 v[0:3], v[4:7], v[124:127], v[0:3]
	v_mfma_f32_16x16x32_bf16 v[4:7], v[8:11], v[120:123], 0
	v_mfma_f32_16x16x32_bf16 v[158:161], v[8:11], v[60:63], 0
	v_mfma_f32_16x16x32_bf16 v[166:169], v[8:11], v[92:95], 0
	v_mfma_f32_16x16x32_bf16 v[174:177], v[8:11], v[108:111], 0
	v_mfma_f32_16x16x32_bf16 v[4:7], v[12:15], v[124:127], v[4:7]
	v_mfma_f32_16x16x32_bf16 v[158:161], v[12:15], v[88:91], v[158:161]
	v_mfma_f32_16x16x32_bf16 v[166:169], v[12:15], v[104:107], v[166:169]
	v_mfma_f32_16x16x32_bf16 v[174:177], v[12:15], v[116:119], v[174:177]
	v_mfma_f32_16x16x32_bf16 v[8:11], v[16:19], v[60:63], 0
	v_mfma_f32_16x16x32_bf16 v[178:181], v[20:23], v[88:91], v[8:11]
	v_mfma_f32_16x16x32_bf16 v[8:11], v[24:27], v[60:63], 0
	v_mfma_f32_16x16x32_bf16 v[182:185], v[28:31], v[88:91], v[8:11]
	v_mfma_f32_16x16x32_bf16 v[8:11], v[16:19], v[92:95], 0
	v_mfma_f32_16x16x32_bf16 v[186:189], v[20:23], v[104:107], v[8:11]
	v_mfma_f32_16x16x32_bf16 v[8:11], v[24:27], v[92:95], 0
	v_mfma_f32_16x16x32_bf16 v[190:193], v[28:31], v[104:107], v[8:11]
	v_mfma_f32_16x16x32_bf16 v[8:11], v[16:19], v[108:111], 0
	v_mfma_f32_16x16x32_bf16 v[194:197], v[20:23], v[116:119], v[8:11]
	v_mfma_f32_16x16x32_bf16 v[8:11], v[24:27], v[108:111], 0
	v_mfma_f32_16x16x32_bf16 v[198:201], v[28:31], v[116:119], v[8:11]
	v_mfma_f32_16x16x32_bf16 v[8:11], v[16:19], v[120:123], 0
	v_mfma_f32_16x16x32_bf16 v[202:205], v[20:23], v[124:127], v[8:11]
	v_mfma_f32_16x16x32_bf16 v[8:11], v[24:27], v[120:123], 0
	v_mfma_f32_16x16x32_bf16 v[206:209], v[28:31], v[124:127], v[8:11]
	s_barrier
	s_add_i32 s67, 0, 0x18000
	s_add_i32 s84, 0, 0x1c000
	v_add_u32_e32 v144, s67, v151
	v_add_u32_e32 v145, s84, v151
	s_nop 0
	ds_read_b128 v[8:11], v144
	ds_read_b128 v[12:15], v144 offset:1024
	ds_read_b128 v[16:19], v144 offset:2048
	ds_read_b128 v[20:23], v144 offset:3072
	ds_read_b128 v[210:213], v145
	ds_read_b128 v[214:217], v145 offset:1024
	ds_read_b128 v[218:221], v145 offset:2048
	ds_read_b128 v[222:225], v145 offset:3072
	s_add_u32 s40, s36, 0x40100
	s_addc_u32 s41, s37, 0
	s_mov_b32 m0, s46
	v_lshl_add_u64 v[88:89], s[40:41], 0, v[128:129]
	ds_read_b128 v[24:27], v155 offset:32768
	ds_read_b128 v[28:31], v155 offset:33792
	ds_read_b128 v[60:63], v155 offset:34816
	ds_read_b128 v[226:229], v155 offset:35840
	ds_read_b128 v[230:233], v155 offset:36864
	ds_read_b128 v[234:237], v155 offset:37888
	ds_read_b128 v[238:241], v155 offset:38912
	ds_read_b128 v[242:245], v155 offset:39936
	global_load_lds_dwordx4 v[88:89], off
	v_lshl_add_u64 v[88:89], s[40:41], 0, v[132:133]
	s_mov_b32 m0, s47
	s_nop 0
	global_load_lds_dwordx4 v[88:89], off
	s_waitcnt vmcnt(8)
	s_waitcnt lgkmcnt(0)
	s_barrier
	s_waitcnt lgkmcnt(0)
	v_mfma_f32_16x16x32_bf16 v[64:67], v[8:11], v[24:27], v[64:67]
	v_mfma_f32_16x16x32_bf16 v[124:127], v[12:15], v[28:31], v[64:67]
	v_mfma_f32_16x16x32_bf16 v[64:67], v[16:19], v[24:27], v[68:71]
	v_mfma_f32_16x16x32_bf16 v[120:123], v[20:23], v[28:31], v[64:67]
	v_mfma_f32_16x16x32_bf16 v[64:67], v[8:11], v[60:63], v[72:75]
	v_mfma_f32_16x16x32_bf16 v[108:111], v[12:15], v[226:229], v[64:67]
	v_mfma_f32_16x16x32_bf16 v[64:67], v[16:19], v[60:63], v[76:79]
	v_mfma_f32_16x16x32_bf16 v[104:107], v[20:23], v[226:229], v[64:67]
	v_mfma_f32_16x16x32_bf16 v[64:67], v[8:11], v[230:233], v[80:83]
	v_mfma_f32_16x16x32_bf16 v[92:95], v[12:15], v[234:237], v[64:67]
	v_mfma_f32_16x16x32_bf16 v[64:67], v[16:19], v[230:233], v[84:87]
	v_mfma_f32_16x16x32_bf16 v[88:91], v[20:23], v[234:237], v[64:67]
	v_mfma_f32_16x16x32_bf16 v[64:67], v[8:11], v[238:241], v[96:99]
	v_mfma_f32_16x16x32_bf16 v[76:79], v[12:15], v[242:245], v[64:67]
	v_mfma_f32_16x16x32_bf16 v[64:67], v[16:19], v[238:241], v[100:103]
	v_mfma_f32_16x16x32_bf16 v[72:75], v[20:23], v[242:245], v[64:67]
	v_mfma_f32_16x16x32_bf16 v[64:67], v[210:213], v[24:27], v[112:115]
	v_mfma_f32_16x16x32_bf16 v[24:27], v[218:221], v[24:27], v[32:35]
	v_mfma_f32_16x16x32_bf16 v[112:115], v[222:225], v[28:31], v[24:27]
	v_mfma_f32_16x16x32_bf16 v[24:27], v[210:213], v[60:63], v[36:39]
	v_mfma_f32_16x16x32_bf16 v[100:103], v[214:217], v[226:229], v[24:27]
	v_mfma_f32_16x16x32_bf16 v[24:27], v[218:221], v[60:63], v[40:43]
	v_mfma_f32_16x16x32_bf16 v[96:99], v[222:225], v[226:229], v[24:27]
	v_mfma_f32_16x16x32_bf16 v[24:27], v[210:213], v[230:233], v[44:47]
	v_mfma_f32_16x16x32_bf16 v[84:87], v[214:217], v[234:237], v[24:27]
	v_mfma_f32_16x16x32_bf16 v[24:27], v[218:221], v[230:233], v[48:51]
	v_mfma_f32_16x16x32_bf16 v[80:83], v[222:225], v[234:237], v[24:27]
	v_mfma_f32_16x16x32_bf16 v[24:27], v[210:213], v[238:241], v[52:55]
	v_mfma_f32_16x16x32_bf16 v[68:71], v[214:217], v[242:245], v[24:27]
	v_mfma_f32_16x16x32_bf16 v[24:27], v[218:221], v[238:241], v[56:59]
	v_mfma_f32_16x16x32_bf16 v[116:119], v[214:217], v[28:31], v[64:67]
	v_mfma_f32_16x16x32_bf16 v[64:67], v[222:225], v[242:245], v[24:27]
	s_barrier
; #define PG8_STAGE(bufoff, gbase, voff) do { _Pragma("unroll") for (int _i = 0; _i < 2; ++_i) \
;         __builtin_amdgcn_global_load_lds((const unsigned*)((const char*)(gbase) + (voff)[_i]), (PG8_LAS unsigned*)(lds + (bufoff) + ldsw + _i * 8192), 16, 0, 0); } while (0)
; #define PG8_WAIT_V(n) asm volatile("s_waitcnt vmcnt(" #n ")" ::: "memory")
; #define PG8_WAIT_L(n) asm volatile("s_waitcnt lgkmcnt(" #n ")" ::: "memory")
; #define PG8_BAR __builtin_amdgcn_s_barrier()
; #define PG8_SCHED __builtin_amdgcn_sched_barrier(0)
; template <class Epi, class Sched, bool ALIGN_EPI = false, bool SP2 = false, bool FP8 = false, bool PEEL = false>
; __device__ __forceinline__ void gemm_phase(PG8_LAS unsigned char* lds, const Gemm g, const Sched& S, const Epi& E, const int wid) {
;     ...
;             PG8_LDA(At, 1, 1); PG8_STAGE(PG8_SB(1, 0), b3, voffB); PG8_STAGE(PG8_SB(1, 1), b3 + hstep, voffB); PG8_STAGE(PG8_SA(1, 0), a3, voffA);
;             PG8_WAIT_V(8); PG8_WAIT_L(0); PG8_BAR; PG8_MMA(1, 0, At, B0); PG8_MMA(1, 1, At, B1); PG8_BAR; PG8_SCHED;
;         }
;     ...
;             const char* a1 = cA + (size_t)(t + 1) * kstep;
;             const char* a2 = last ? nA : cA + (size_t)(t + 2) * kstep; const char* b2 = last ? nB : cB + (size_t)(t + 2) * kstep;
;             const char* a3 = a2 + kstep; const char* b3 = b2 + kstep;
;             if (last && has_next) S.a_ready(nxt);
;             PG8_LDB(B0, 0, 0); PG8_LDB(B1, 0, 1); PG8_SCHED; PG8_LDA(At, 0, 0); PG8_STAGE(PG8_SA(1, 1), a1 + hstep, voffA);
	s_add_i32 s67, s67, s3
	s_add_i32 s75, s67, 0x2000
	s_nop 1
	v_lshl_add_u64 v[24:25], v[250:251], 0, s[18:19]
	s_mov_b32 m0, s67
	s_add_u32 s40, s30, 0x40180
	ds_read_b128 v[32:35], v155 offset:49152
	ds_read_b128 v[36:39], v155 offset:50176
	ds_read_b128 v[226:229], v155 offset:51200
	ds_read_b128 v[230:233], v155 offset:52224
	ds_read_b128 v[234:237], v155 offset:53248
	ds_read_b128 v[238:241], v155 offset:54272
	ds_read_b128 v[242:245], v155 offset:55296
	ds_read_b128 v[246:249], v155 offset:56320
	global_load_lds_dwordx4 v[24:25], off
	v_lshl_add_u64 v[24:25], v[252:253], 0, s[18:19]
	s_mov_b32 m0, s75
	s_addc_u32 s41, s31, 0
	s_add_i32 s84, s84, s3
	global_load_lds_dwordx4 v[24:25], off
	v_lshl_add_u64 v[24:25], s[40:41], 0, v[130:131]
	s_mov_b32 m0, s84
	s_add_i32 s85, s84, 0x2000
	global_load_lds_dwordx4 v[24:25], off
	v_lshl_add_u64 v[24:25], s[40:41], 0, v[134:135]
	s_mov_b32 m0, s85
	s_nop 0
	global_load_lds_dwordx4 v[24:25], off
	v_lshl_add_u64 v[24:25], v[140:141], 0, s[18:19]
	s_mov_b32 m0, s54
	s_nop 0
	global_load_lds_dwordx4 v[24:25], off
	v_lshl_add_u64 v[24:25], v[142:143], 0, s[18:19]
	s_mov_b32 m0, s55
	s_nop 0
	global_load_lds_dwordx4 v[24:25], off
	s_waitcnt vmcnt(8)
	s_waitcnt lgkmcnt(0)
	s_barrier
	s_waitcnt lgkmcnt(0)
	v_mfma_f32_16x16x32_bf16 v[24:27], v[8:11], v[32:35], v[146:149]
	v_mfma_f32_16x16x32_bf16 v[60:63], v[12:15], v[36:39], v[24:27]
	v_mfma_f32_16x16x32_bf16 v[24:27], v[16:19], v[32:35], v[158:161]
	v_mfma_f32_16x16x32_bf16 v[56:59], v[20:23], v[36:39], v[24:27]
	v_mfma_f32_16x16x32_bf16 v[24:27], v[8:11], v[226:229], v[162:165]
	v_mfma_f32_16x16x32_bf16 v[44:47], v[12:15], v[230:233], v[24:27]
	v_mfma_f32_16x16x32_bf16 v[24:27], v[16:19], v[226:229], v[166:169]
	v_mfma_f32_16x16x32_bf16 v[40:43], v[20:23], v[230:233], v[24:27]
	v_mfma_f32_16x16x32_bf16 v[24:27], v[8:11], v[234:237], v[170:173]
	v_mfma_f32_16x16x32_bf16 v[0:3], v[8:11], v[242:245], v[0:3]
	v_mfma_f32_16x16x32_bf16 v[28:31], v[12:15], v[238:241], v[24:27]
	v_mfma_f32_16x16x32_bf16 v[24:27], v[16:19], v[234:237], v[174:177]
	v_mfma_f32_16x16x32_bf16 v[12:15], v[12:15], v[246:249], v[0:3]
	v_mfma_f32_16x16x32_bf16 v[0:3], v[16:19], v[242:245], v[4:7]
	v_mfma_f32_16x16x32_bf16 v[24:27], v[20:23], v[238:241], v[24:27]
	v_mfma_f32_16x16x32_bf16 v[8:11], v[20:23], v[246:249], v[0:3]
	v_mfma_f32_16x16x32_bf16 v[0:3], v[210:213], v[32:35], v[178:181]
	v_mfma_f32_16x16x32_bf16 v[52:55], v[214:217], v[36:39], v[0:3]
	v_mfma_f32_16x16x32_bf16 v[0:3], v[218:221], v[32:35], v[182:185]
	v_mfma_f32_16x16x32_bf16 v[48:51], v[222:225], v[36:39], v[0:3]
	v_mfma_f32_16x16x32_bf16 v[0:3], v[210:213], v[226:229], v[186:189]
	v_mfma_f32_16x16x32_bf16 v[36:39], v[214:217], v[230:233], v[0:3]
	v_mfma_f32_16x16x32_bf16 v[0:3], v[218:221], v[226:229], v[190:193]
	v_mfma_f32_16x16x32_bf16 v[32:35], v[222:225], v[230:233], v[0:3]
	v_mfma_f32_16x16x32_bf16 v[0:3], v[210:213], v[234:237], v[194:197]
	v_mfma_f32_16x16x32_bf16 v[20:23], v[214:217], v[238:241], v[0:3]
	v_mfma_f32_16x16x32_bf16 v[0:3], v[218:221], v[234:237], v[198:201]
	v_mfma_f32_16x16x32_bf16 v[16:19], v[222:225], v[238:241], v[0:3]
	v_mfma_f32_16x16x32_bf16 v[0:3], v[210:213], v[242:245], v[202:205]
	v_mfma_f32_16x16x32_bf16 v[4:7], v[214:217], v[246:249], v[0:3]
	v_mfma_f32_16x16x32_bf16 v[0:3], v[218:221], v[242:245], v[206:209]
	v_mfma_f32_16x16x32_bf16 v[0:3], v[222:225], v[246:249], v[0:3]
	s_barrier
	s_add_u32 s36, s36, 0x40180
	s_addc_u32 s37, s37, 0
	s_add_u32 s88, s30, 0x200
	s_addc_u32 s89, s31, 0
	s_mov_b32 s90, 0
.LBB0_237:
	ds_read_b128 v[146:149], v153
	ds_read_b128 v[158:161], v153 offset:1024
	ds_read_b128 v[162:165], v153 offset:2048
	ds_read_b128 v[166:169], v153 offset:3072
	ds_read_b128 v[170:173], v154
	ds_read_b128 v[174:177], v154 offset:1024
	ds_read_b128 v[178:181], v154 offset:2048
	ds_read_b128 v[182:185], v154 offset:3072
	s_add_u32 s30, s36, 0xfffc0080
	s_addc_u32 s31, s37, -1
	s_cmp_eq_u32 s90, 12
	s_cselect_b32 s41, s13, s31
	s_cselect_b32 s40, s21, s30
	s_cselect_b32 s31, s23, s89
	s_cselect_b32 s30, s60, s88
	s_mov_b32 m0, s61
	v_lshl_add_u64 v[140:141], s[36:37], 0, v[136:137]
	ds_read_b128 v[186:189], v155
	ds_read_b128 v[190:193], v155 offset:1024
	ds_read_b128 v[194:197], v155 offset:2048
	ds_read_b128 v[198:201], v155 offset:3072
	ds_read_b128 v[202:205], v155 offset:4096
	ds_read_b128 v[206:209], v155 offset:5120
	ds_read_b128 v[210:213], v155 offset:6144
	ds_read_b128 v[214:217], v155 offset:7168
	global_load_lds_dwordx4 v[140:141], off
	v_lshl_add_u64 v[140:141], s[36:37], 0, v[138:139]
	s_mov_b32 m0, s62
	s_nop 0
	global_load_lds_dwordx4 v[140:141], off
	s_waitcnt vmcnt(8)
	s_waitcnt lgkmcnt(0)
	s_barrier
; #define PG8_STAGE(bufoff, gbase, voff) do { _Pragma("unroll") for (int _i = 0; _i < 2; ++_i) \
;         __builtin_amdgcn_global_load_lds((const unsigned*)((const char*)(gbase) + (voff)[_i]), (PG8_LAS unsigned*)(lds + (bufoff) + ldsw + _i * 8192), 16, 0, 0); } while (0)
; #define PG8_WAIT_V(n) asm volatile("s_waitcnt vmcnt(" #n ")" ::: "memory")
; #define PG8_WAIT_L(n) asm volatile("s_waitcnt lgkmcnt(" #n ")" ::: "memory")
; #define PG8_BAR __builtin_amdgcn_s_barrier()
; #define PG8_SCHED __builtin_amdgcn_sched_barrier(0)
; template <class Epi, class Sched, bool ALIGN_EPI = false, bool SP2 = false, bool FP8 = false, bool PEEL = false>
; __device__ __forceinline__ void gemm_phase(PG8_LAS unsigned char* lds, const Gemm g, const Sched& S, const Epi& E, const int wid) {
;     ...
;             PG8_WAIT_V(8); PG8_WAIT_L(0); PG8_BAR; PG8_MMA(0, 0, At, B0); PG8_MMA(0, 1, At, B1); PG8_BAR; PG8_SCHED;
;             PG8_LDA(At, 0, 1); PG8_STAGE(PG8_SB(0, 0), b2, voffB); PG8_STAGE(PG8_SB(0, 1), b2 + hstep, voffB); PG8_STAGE(PG8_SA(0, 0), a2, voffA);
;             PG8_WAIT_V(8); PG8_WAIT_L(0); PG8_BAR; PG8_MMA(1, 0, At, B0); PG8_MMA(1, 1, At, B1); PG8_BAR; PG8_SCHED;
;             PG8_LDB(B0, 1, 0); PG8_LDB(B1, 1, 1); PG8_SCHED; PG8_LDA(At, 1, 0); PG8_STAGE(PG8_SA(0, 1), a2 + hstep, voffA);
;             PG8_WAIT_V(8); PG8_WAIT_L(0); PG8_BAR; PG8_MMA(0, 0, At, B0); PG8_MMA(0, 1, At, B1); PG8_BAR; PG8_SCHED;
	s_waitcnt lgkmcnt(0)
	v_mfma_f32_16x16x32_bf16 v[124:127], v[146:149], v[186:189], v[124:127]
	v_mfma_f32_16x16x32_bf16 v[120:123], v[162:165], v[186:189], v[120:123]
	v_mfma_f32_16x16x32_bf16 v[108:111], v[146:149], v[194:197], v[108:111]
	v_mfma_f32_16x16x32_bf16 v[104:107], v[162:165], v[194:197], v[104:107]
	v_mfma_f32_16x16x32_bf16 v[92:95], v[146:149], v[202:205], v[92:95]
	v_mfma_f32_16x16x32_bf16 v[88:91], v[162:165], v[202:205], v[88:91]
	v_mfma_f32_16x16x32_bf16 v[76:79], v[146:149], v[210:213], v[76:79]
	v_mfma_f32_16x16x32_bf16 v[72:75], v[162:165], v[210:213], v[72:75]
	v_mfma_f32_16x16x32_bf16 v[124:127], v[158:161], v[190:193], v[124:127]
	v_mfma_f32_16x16x32_bf16 v[120:123], v[166:169], v[190:193], v[120:123]
	v_mfma_f32_16x16x32_bf16 v[108:111], v[158:161], v[198:201], v[108:111]
	v_mfma_f32_16x16x32_bf16 v[104:107], v[166:169], v[198:201], v[104:107]
	v_mfma_f32_16x16x32_bf16 v[92:95], v[158:161], v[206:209], v[92:95]
	v_mfma_f32_16x16x32_bf16 v[88:91], v[166:169], v[206:209], v[88:91]
	v_mfma_f32_16x16x32_bf16 v[76:79], v[158:161], v[214:217], v[76:79]
	v_mfma_f32_16x16x32_bf16 v[72:75], v[166:169], v[214:217], v[72:75]
	v_mfma_f32_16x16x32_bf16 v[116:119], v[170:173], v[186:189], v[116:119]
	v_mfma_f32_16x16x32_bf16 v[112:115], v[178:181], v[186:189], v[112:115]
	v_mfma_f32_16x16x32_bf16 v[100:103], v[170:173], v[194:197], v[100:103]
	v_mfma_f32_16x16x32_bf16 v[96:99], v[178:181], v[194:197], v[96:99]
	v_mfma_f32_16x16x32_bf16 v[84:87], v[170:173], v[202:205], v[84:87]
	v_mfma_f32_16x16x32_bf16 v[80:83], v[178:181], v[202:205], v[80:83]
	v_mfma_f32_16x16x32_bf16 v[68:71], v[170:173], v[210:213], v[68:71]
	v_mfma_f32_16x16x32_bf16 v[64:67], v[178:181], v[210:213], v[64:67]
	v_mfma_f32_16x16x32_bf16 v[116:119], v[174:177], v[190:193], v[116:119]
	v_mfma_f32_16x16x32_bf16 v[112:115], v[182:185], v[190:193], v[112:115]
	v_mfma_f32_16x16x32_bf16 v[100:103], v[174:177], v[198:201], v[100:103]
	v_mfma_f32_16x16x32_bf16 v[96:99], v[182:185], v[198:201], v[96:99]
	v_mfma_f32_16x16x32_bf16 v[84:87], v[174:177], v[206:209], v[84:87]
	v_mfma_f32_16x16x32_bf16 v[80:83], v[182:185], v[206:209], v[80:83]
	v_mfma_f32_16x16x32_bf16 v[68:71], v[174:177], v[214:217], v[68:71]
	v_mfma_f32_16x16x32_bf16 v[64:67], v[182:185], v[214:217], v[64:67]
	s_barrier
	s_mov_b32 m0, s63
	v_lshl_add_u64 v[140:141], s[30:31], 0, v[130:131]
	s_add_u32 s92, s30, 0x40000
	ds_read_b128 v[186:189], v155 offset:16384
	ds_read_b128 v[190:193], v155 offset:17408
	ds_read_b128 v[194:197], v155 offset:18432
	ds_read_b128 v[198:201], v155 offset:19456
	ds_read_b128 v[202:205], v155 offset:20480
	ds_read_b128 v[206:209], v155 offset:21504
	ds_read_b128 v[210:213], v155 offset:22528
	ds_read_b128 v[214:217], v155 offset:23552
	global_load_lds_dwordx4 v[140:141], off
	v_lshl_add_u64 v[142:143], s[30:31], 0, v[134:135]
	s_mov_b32 m0, s64
	s_addc_u32 s93, s31, 0
	global_load_lds_dwordx4 v[142:143], off
	v_lshl_add_u64 v[218:219], s[92:93], 0, v[130:131]
	s_mov_b32 m0, s65
	v_lshl_add_u64 v[220:221], s[40:41], 0, v[132:133]
	global_load_lds_dwordx4 v[218:219], off
	v_lshl_add_u64 v[218:219], s[92:93], 0, v[134:135]
	s_mov_b32 m0, s66
	s_nop 0
	global_load_lds_dwordx4 v[218:219], off
	v_lshl_add_u64 v[218:219], s[40:41], 0, v[128:129]
	s_mov_b32 m0, s44
	s_nop 0
	global_load_lds_dwordx4 v[218:219], off
	s_mov_b32 m0, s45
	s_nop 0
	global_load_lds_dwordx4 v[220:221], off
	s_waitcnt vmcnt(8)
	s_waitcnt lgkmcnt(0)
	s_barrier
	s_waitcnt lgkmcnt(0)
	v_mfma_f32_16x16x32_bf16 v[60:63], v[146:149], v[186:189], v[60:63]
	v_mfma_f32_16x16x32_bf16 v[56:59], v[162:165], v[186:189], v[56:59]
	v_mfma_f32_16x16x32_bf16 v[44:47], v[146:149], v[194:197], v[44:47]
	v_mfma_f32_16x16x32_bf16 v[40:43], v[162:165], v[194:197], v[40:43]
	v_mfma_f32_16x16x32_bf16 v[28:31], v[146:149], v[202:205], v[28:31]
	v_mfma_f32_16x16x32_bf16 v[24:27], v[162:165], v[202:205], v[24:27]
	v_mfma_f32_16x16x32_bf16 v[12:15], v[146:149], v[210:213], v[12:15]
	v_mfma_f32_16x16x32_bf16 v[8:11], v[162:165], v[210:213], v[8:11]
	v_mfma_f32_16x16x32_bf16 v[60:63], v[158:161], v[190:193], v[60:63]
	v_mfma_f32_16x16x32_bf16 v[56:59], v[166:169], v[190:193], v[56:59]
	v_mfma_f32_16x16x32_bf16 v[44:47], v[158:161], v[198:201], v[44:47]
	v_mfma_f32_16x16x32_bf16 v[40:43], v[166:169], v[198:201], v[40:43]
	v_mfma_f32_16x16x32_bf16 v[28:31], v[158:161], v[206:209], v[28:31]
	v_mfma_f32_16x16x32_bf16 v[24:27], v[166:169], v[206:209], v[24:27]
	v_mfma_f32_16x16x32_bf16 v[12:15], v[158:161], v[214:217], v[12:15]
	v_mfma_f32_16x16x32_bf16 v[8:11], v[166:169], v[214:217], v[8:11]
	v_mfma_f32_16x16x32_bf16 v[52:55], v[170:173], v[186:189], v[52:55]
	v_mfma_f32_16x16x32_bf16 v[48:51], v[178:181], v[186:189], v[48:51]
	v_mfma_f32_16x16x32_bf16 v[36:39], v[170:173], v[194:197], v[36:39]
	v_mfma_f32_16x16x32_bf16 v[32:35], v[178:181], v[194:197], v[32:35]
	v_mfma_f32_16x16x32_bf16 v[20:23], v[170:173], v[202:205], v[20:23]
	v_mfma_f32_16x16x32_bf16 v[16:19], v[178:181], v[202:205], v[16:19]
	v_mfma_f32_16x16x32_bf16 v[4:7], v[170:173], v[210:213], v[4:7]
	v_mfma_f32_16x16x32_bf16 v[0:3], v[178:181], v[210:213], v[0:3]
	v_mfma_f32_16x16x32_bf16 v[52:55], v[174:177], v[190:193], v[52:55]
	v_mfma_f32_16x16x32_bf16 v[48:51], v[182:185], v[190:193], v[48:51]
	v_mfma_f32_16x16x32_bf16 v[36:39], v[174:177], v[198:201], v[36:39]
	v_mfma_f32_16x16x32_bf16 v[32:35], v[182:185], v[198:201], v[32:35]
	v_mfma_f32_16x16x32_bf16 v[20:23], v[174:177], v[206:209], v[20:23]
	v_mfma_f32_16x16x32_bf16 v[16:19], v[182:185], v[206:209], v[16:19]
	v_mfma_f32_16x16x32_bf16 v[4:7], v[174:177], v[214:217], v[4:7]
	v_mfma_f32_16x16x32_bf16 v[0:3], v[182:185], v[214:217], v[0:3]
	s_barrier
; #define PG8_STAGE(bufoff, gbase, voff) do { _Pragma("unroll") for (int _i = 0; _i < 2; ++_i) \
;         __builtin_amdgcn_global_load_lds((const unsigned*)((const char*)(gbase) + (voff)[_i]), (PG8_LAS unsigned*)(lds + (bufoff) + ldsw + _i * 8192), 16, 0, 0); } while (0)
; #define PG8_WAIT_V(n) asm volatile("s_waitcnt vmcnt(" #n ")" ::: "memory")
; #define PG8_WAIT_L(n) asm volatile("s_waitcnt lgkmcnt(" #n ")" ::: "memory")
; #define PG8_BAR __builtin_amdgcn_s_barrier()
; #define PG8_SCHED __builtin_amdgcn_sched_barrier(0)
; template <class Epi, class Sched, bool ALIGN_EPI = false, bool SP2 = false, bool FP8 = false, bool PEEL = false>
; __device__ __forceinline__ void gemm_phase(PG8_LAS unsigned char* lds, const Gemm g, const Sched& S, const Epi& E, const int wid) {
;     ...
;             PG8_LDB(B0, 1, 0); PG8_LDB(B1, 1, 1); PG8_SCHED; PG8_LDA(At, 1, 0); PG8_STAGE(PG8_SA(0, 1), a2 + hstep, voffA);
;             PG8_WAIT_V(8); PG8_WAIT_L(0); PG8_BAR; PG8_MMA(0, 0, At, B0); PG8_MMA(0, 1, At, B1); PG8_BAR; PG8_SCHED;
;             PG8_LDA(At, 1, 1); PG8_STAGE(PG8_SB(1, 0), b3, voffB); PG8_STAGE(PG8_SB(1, 1), b3 + hstep, voffB); PG8_STAGE(PG8_SA(1, 0), a3, voffA);
;             PG8_WAIT_V(8); PG8_WAIT_L(0); PG8_BAR; PG8_MMA(1, 0, At, B0); PG8_MMA(1, 1, At, B1); PG8_BAR; PG8_SCHED;
;         }
	ds_read_b128 v[146:149], v144
	ds_read_b128 v[158:161], v144 offset:1024
	ds_read_b128 v[162:165], v144 offset:2048
	ds_read_b128 v[166:169], v144 offset:3072
	ds_read_b128 v[170:173], v145
	ds_read_b128 v[174:177], v145 offset:1024
	ds_read_b128 v[178:181], v145 offset:2048
	ds_read_b128 v[182:185], v145 offset:3072
	s_add_u32 s40, s40, 0x40000
	s_addc_u32 s41, s41, 0
	s_mov_b32 m0, s46
	v_lshl_add_u64 v[222:223], s[40:41], 0, v[128:129]
	ds_read_b128 v[186:189], v155 offset:32768
	ds_read_b128 v[190:193], v155 offset:33792
	ds_read_b128 v[194:197], v155 offset:34816
	ds_read_b128 v[198:201], v155 offset:35840
	ds_read_b128 v[202:205], v155 offset:36864
	ds_read_b128 v[206:209], v155 offset:37888
	ds_read_b128 v[210:213], v155 offset:38912
	ds_read_b128 v[214:217], v155 offset:39936
	global_load_lds_dwordx4 v[222:223], off
	v_lshl_add_u64 v[222:223], s[40:41], 0, v[132:133]
	s_mov_b32 m0, s47
	s_nop 0
	global_load_lds_dwordx4 v[222:223], off
	s_waitcnt vmcnt(8)
	s_waitcnt lgkmcnt(0)
	s_barrier
	s_waitcnt lgkmcnt(0)
	v_mfma_f32_16x16x32_bf16 v[124:127], v[146:149], v[186:189], v[124:127]
	v_mfma_f32_16x16x32_bf16 v[120:123], v[162:165], v[186:189], v[120:123]
	v_mfma_f32_16x16x32_bf16 v[108:111], v[146:149], v[194:197], v[108:111]
	v_mfma_f32_16x16x32_bf16 v[104:107], v[162:165], v[194:197], v[104:107]
	v_mfma_f32_16x16x32_bf16 v[92:95], v[146:149], v[202:205], v[92:95]
	v_mfma_f32_16x16x32_bf16 v[88:91], v[162:165], v[202:205], v[88:91]
	v_mfma_f32_16x16x32_bf16 v[76:79], v[146:149], v[210:213], v[76:79]
	v_mfma_f32_16x16x32_bf16 v[72:75], v[162:165], v[210:213], v[72:75]
	v_mfma_f32_16x16x32_bf16 v[124:127], v[158:161], v[190:193], v[124:127]
	v_mfma_f32_16x16x32_bf16 v[120:123], v[166:169], v[190:193], v[120:123]
	v_mfma_f32_16x16x32_bf16 v[108:111], v[158:161], v[198:201], v[108:111]
	v_mfma_f32_16x16x32_bf16 v[104:107], v[166:169], v[198:201], v[104:107]
	v_mfma_f32_16x16x32_bf16 v[92:95], v[158:161], v[206:209], v[92:95]
	v_mfma_f32_16x16x32_bf16 v[88:91], v[166:169], v[206:209], v[88:91]
	v_mfma_f32_16x16x32_bf16 v[76:79], v[158:161], v[214:217], v[76:79]
	v_mfma_f32_16x16x32_bf16 v[72:75], v[166:169], v[214:217], v[72:75]
	v_mfma_f32_16x16x32_bf16 v[116:119], v[170:173], v[186:189], v[116:119]
	v_mfma_f32_16x16x32_bf16 v[112:115], v[178:181], v[186:189], v[112:115]
	v_mfma_f32_16x16x32_bf16 v[100:103], v[170:173], v[194:197], v[100:103]
	v_mfma_f32_16x16x32_bf16 v[96:99], v[178:181], v[194:197], v[96:99]
	v_mfma_f32_16x16x32_bf16 v[84:87], v[170:173], v[202:205], v[84:87]
	v_mfma_f32_16x16x32_bf16 v[80:83], v[178:181], v[202:205], v[80:83]
	v_mfma_f32_16x16x32_bf16 v[68:71], v[170:173], v[210:213], v[68:71]
	v_mfma_f32_16x16x32_bf16 v[64:67], v[178:181], v[210:213], v[64:67]
	v_mfma_f32_16x16x32_bf16 v[116:119], v[174:177], v[190:193], v[116:119]
	v_mfma_f32_16x16x32_bf16 v[112:115], v[182:185], v[190:193], v[112:115]
	v_mfma_f32_16x16x32_bf16 v[100:103], v[174:177], v[198:201], v[100:103]
	v_mfma_f32_16x16x32_bf16 v[96:99], v[182:185], v[198:201], v[96:99]
	v_mfma_f32_16x16x32_bf16 v[84:87], v[174:177], v[206:209], v[84:87]
	v_mfma_f32_16x16x32_bf16 v[80:83], v[182:185], v[206:209], v[80:83]
	v_mfma_f32_16x16x32_bf16 v[68:71], v[174:177], v[214:217], v[68:71]
	v_mfma_f32_16x16x32_bf16 v[64:67], v[182:185], v[214:217], v[64:67]
	s_barrier
	s_mov_b32 m0, s67
	v_lshl_add_u64 v[140:141], v[140:141], 0, s[14:15]
	s_add_u32 s30, s30, 0x40080
	ds_read_b128 v[186:189], v155 offset:49152
	ds_read_b128 v[190:193], v155 offset:50176
	ds_read_b128 v[194:197], v155 offset:51200
	ds_read_b128 v[198:201], v155 offset:52224
	ds_read_b128 v[202:205], v155 offset:53248
	ds_read_b128 v[206:209], v155 offset:54272
	ds_read_b128 v[210:213], v155 offset:55296
	ds_read_b128 v[214:217], v155 offset:56320
	global_load_lds_dwordx4 v[140:141], off
	v_lshl_add_u64 v[140:141], v[142:143], 0, s[14:15]
	s_mov_b32 m0, s75
	s_addc_u32 s31, s31, 0
	global_load_lds_dwordx4 v[140:141], off
	v_lshl_add_u64 v[140:141], s[30:31], 0, v[130:131]
	s_mov_b32 m0, s84
	s_nop 0
	global_load_lds_dwordx4 v[140:141], off
	v_lshl_add_u64 v[140:141], s[30:31], 0, v[134:135]
	s_mov_b32 m0, s85
	s_nop 0
	global_load_lds_dwordx4 v[140:141], off
	v_lshl_add_u64 v[140:141], v[218:219], 0, s[14:15]
	s_mov_b32 m0, s54
	s_nop 0
	global_load_lds_dwordx4 v[140:141], off
	v_lshl_add_u64 v[140:141], v[220:221], 0, s[14:15]
	s_mov_b32 m0, s55
	s_nop 0
	global_load_lds_dwordx4 v[140:141], off
	s_waitcnt vmcnt(8)
	s_waitcnt lgkmcnt(0)
	s_barrier
	s_waitcnt lgkmcnt(0)
	v_mfma_f32_16x16x32_bf16 v[60:63], v[146:149], v[186:189], v[60:63]
	v_mfma_f32_16x16x32_bf16 v[56:59], v[162:165], v[186:189], v[56:59]
	v_mfma_f32_16x16x32_bf16 v[44:47], v[146:149], v[194:197], v[44:47]
	v_mfma_f32_16x16x32_bf16 v[40:43], v[162:165], v[194:197], v[40:43]
	v_mfma_f32_16x16x32_bf16 v[28:31], v[146:149], v[202:205], v[28:31]
	v_mfma_f32_16x16x32_bf16 v[24:27], v[162:165], v[202:205], v[24:27]
	v_mfma_f32_16x16x32_bf16 v[12:15], v[146:149], v[210:213], v[12:15]
	v_mfma_f32_16x16x32_bf16 v[8:11], v[162:165], v[210:213], v[8:11]
	v_mfma_f32_16x16x32_bf16 v[60:63], v[158:161], v[190:193], v[60:63]
	v_mfma_f32_16x16x32_bf16 v[56:59], v[166:169], v[190:193], v[56:59]
	v_mfma_f32_16x16x32_bf16 v[44:47], v[158:161], v[198:201], v[44:47]
	v_mfma_f32_16x16x32_bf16 v[40:43], v[166:169], v[198:201], v[40:43]
	v_mfma_f32_16x16x32_bf16 v[28:31], v[158:161], v[206:209], v[28:31]
	v_mfma_f32_16x16x32_bf16 v[24:27], v[166:169], v[206:209], v[24:27]
	v_mfma_f32_16x16x32_bf16 v[12:15], v[158:161], v[214:217], v[12:15]
	v_mfma_f32_16x16x32_bf16 v[8:11], v[166:169], v[214:217], v[8:11]
	v_mfma_f32_16x16x32_bf16 v[52:55], v[170:173], v[186:189], v[52:55]
	v_mfma_f32_16x16x32_bf16 v[48:51], v[178:181], v[186:189], v[48:51]
	v_mfma_f32_16x16x32_bf16 v[36:39], v[170:173], v[194:197], v[36:39]
	v_mfma_f32_16x16x32_bf16 v[32:35], v[178:181], v[194:197], v[32:35]
	v_mfma_f32_16x16x32_bf16 v[20:23], v[170:173], v[202:205], v[20:23]
	v_mfma_f32_16x16x32_bf16 v[16:19], v[178:181], v[202:205], v[16:19]
	v_mfma_f32_16x16x32_bf16 v[4:7], v[170:173], v[210:213], v[4:7]
	v_mfma_f32_16x16x32_bf16 v[0:3], v[178:181], v[210:213], v[0:3]
	v_mfma_f32_16x16x32_bf16 v[52:55], v[174:177], v[190:193], v[52:55]
	v_mfma_f32_16x16x32_bf16 v[48:51], v[182:185], v[190:193], v[48:51]
	v_mfma_f32_16x16x32_bf16 v[36:39], v[174:177], v[198:201], v[36:39]
	v_mfma_f32_16x16x32_bf16 v[32:35], v[182:185], v[198:201], v[32:35]
	v_mfma_f32_16x16x32_bf16 v[20:23], v[174:177], v[206:209], v[20:23]
	v_mfma_f32_16x16x32_bf16 v[16:19], v[182:185], v[206:209], v[16:19]
	v_mfma_f32_16x16x32_bf16 v[4:7], v[174:177], v[214:217], v[4:7]
	v_mfma_f32_16x16x32_bf16 v[0:3], v[182:185], v[214:217], v[0:3]
	s_barrier
	s_add_i32 s90, s90, 2
	s_add_u32 s36, s36, 0x100
	s_addc_u32 s37, s37, 0
	s_add_u32 s88, s88, 0x100
	s_addc_u32 s89, s89, 0
	s_cmp_gt_u32 s90, 13
	s_cbranch_scc0 .LBB0_237
	s_and_b64 vcc, exec, s[6:7]
	s_cbranch_vccz .LBB0_240
	s_barrier

; #define PG8_STAGE(bufoff, gbase, voff) do { _Pragma("unroll") for (int _i = 0; _i < 2; ++_i) \
;         __builtin_amdgcn_global_load_lds((const unsigned*)((const char*)(gbase) + (voff)[_i]), (PG8_LAS unsigned*)(lds + (bufoff) + ldsw + _i * 8192), 16, 0, 0); } while (0)
; #define PG8_WAIT_V(n) asm volatile("s_waitcnt vmcnt(" #n ")" ::: "memory")
; #define PG8_WAIT_L(n) asm volatile("s_waitcnt lgkmcnt(" #n ")" ::: "memory")
; #define PG8_BAR __builtin_amdgcn_s_barrier()
; #define PG8_SCHED __builtin_amdgcn_sched_barrier(0)
; template <class Epi, class Sched, bool ALIGN_EPI = false, bool SP2 = false, bool FP8 = false, bool PEEL = false>
; __device__ __forceinline__ void gemm_phase(PG8_LAS unsigned char* lds, const Gemm g, const Sched& S, const Epi& E, const int wid) {
;     ...
;         for (int t = 0; t < nt; t += 2) {
;             const bool last = (t == nt - 2);
;             const char* a1 = cA + (size_t)(t + 1) * kstep;
;             const char* a2 = last ? nA : cA + (size_t)(t + 2) * kstep; const char* b2 = last ? nB : cB + (size_t)(t + 2) * kstep;
;             const char* a3 = a2 + kstep; const char* b3 = b2 + kstep;
;             if (last && has_next) S.a_ready(nxt);
;             PG8_LDB(B0, 0, 0); PG8_LDB(B1, 0, 1); PG8_SCHED; PG8_LDA(At, 0, 0); PG8_STAGE(PG8_SA(1, 1), a1 + hstep, voffA);
;             PG8_WAIT_V(8); PG8_WAIT_L(0); PG8_BAR; PG8_MMA(0, 0, At, B0); PG8_MMA(0, 1, At, B1); PG8_BAR; PG8_SCHED;
;             PG8_LDA(At, 0, 1); PG8_STAGE(PG8_SB(0, 0), b2, voffB); PG8_STAGE(PG8_SB(0, 1), b2 + hstep, voffB); PG8_STAGE(PG8_SA(0, 0), a2, voffA);
.LBB0_659:
	v_add_u32_e32 v162, s50, v148
	v_add_u32_e32 v178, s51, v148
	s_add_u32 s26, s6, s24
	ds_read_b128 v[150:153], v162
	ds_read_b128 v[154:157], v162 offset:1024
	ds_read_b128 v[158:161], v162 offset:2048
	ds_read_b128 v[162:165], v162 offset:3072
	ds_read_b128 v[166:169], v178
	ds_read_b128 v[170:173], v178 offset:1024
	ds_read_b128 v[174:177], v178 offset:2048
	ds_read_b128 v[178:181], v178 offset:3072
	s_addc_u32 s27, s7, s25
	s_add_u32 s26, s26, 0x100
	s_addc_u32 s27, s27, 0
	s_add_u32 s59, s54, s24
	s_addc_u32 s60, s55, s25
	s_cmpk_eq_i32 s24, 0x700
	s_cselect_b32 s31, s17, s27
	s_cselect_b32 s30, s56, s26
	s_cselect_b32 s27, s15, s60
	s_cselect_b32 s26, s57, s59
	v_lshl_add_u64 v[218:219], v[144:145], 0, s[24:25]
	s_add_i32 m0, s43, 0xc000
	ds_read_b128 v[182:185], v149
	ds_read_b128 v[190:193], v149 offset:1024
	ds_read_b128 v[194:197], v149 offset:2048
	ds_read_b128 v[198:201], v149 offset:3072
	ds_read_b128 v[202:205], v149 offset:4096
	ds_read_b128 v[206:209], v149 offset:5120
	ds_read_b128 v[210:213], v149 offset:6144
	ds_read_b128 v[214:217], v149 offset:7168
	global_load_lds_dwordx4 v[218:219], off
	v_lshl_add_u64 v[218:219], v[146:147], 0, s[24:25]
	s_add_i32 m0, s43, 0xe000
	s_nop 0
	global_load_lds_dwordx4 v[218:219], off
	s_waitcnt vmcnt(8)
	s_waitcnt lgkmcnt(0)
	s_barrier
	s_waitcnt lgkmcnt(0)
	v_mfma_f32_16x16x32_bf16 v[124:127], v[150:153], v[182:185], v[124:127]
	v_mfma_f32_16x16x32_bf16 v[120:123], v[158:161], v[182:185], v[120:123]
	v_mfma_f32_16x16x32_bf16 v[112:115], v[150:153], v[194:197], v[112:115]
	v_mfma_f32_16x16x32_bf16 v[108:111], v[158:161], v[194:197], v[108:111]
	v_mfma_f32_16x16x32_bf16 v[100:103], v[150:153], v[202:205], v[100:103]
	v_mfma_f32_16x16x32_bf16 v[92:95], v[158:161], v[202:205], v[92:95]
	v_mfma_f32_16x16x32_bf16 v[84:87], v[150:153], v[210:213], v[84:87]
	v_mfma_f32_16x16x32_bf16 v[76:79], v[158:161], v[210:213], v[76:79]
	v_mfma_f32_16x16x32_bf16 v[124:127], v[154:157], v[190:193], v[124:127]
	v_mfma_f32_16x16x32_bf16 v[120:123], v[162:165], v[190:193], v[120:123]
	v_mfma_f32_16x16x32_bf16 v[112:115], v[154:157], v[198:201], v[112:115]
	v_mfma_f32_16x16x32_bf16 v[108:111], v[162:165], v[198:201], v[108:111]
	v_mfma_f32_16x16x32_bf16 v[100:103], v[154:157], v[206:209], v[100:103]
	v_mfma_f32_16x16x32_bf16 v[92:95], v[162:165], v[206:209], v[92:95]
	v_mfma_f32_16x16x32_bf16 v[84:87], v[154:157], v[214:217], v[84:87]
	v_mfma_f32_16x16x32_bf16 v[76:79], v[162:165], v[214:217], v[76:79]
	v_mfma_f32_16x16x32_bf16 v[116:119], v[166:169], v[182:185], v[116:119]
	v_mfma_f32_16x16x32_bf16 v[104:107], v[174:177], v[182:185], v[104:107]
	v_mfma_f32_16x16x32_bf16 v[96:99], v[166:169], v[194:197], v[96:99]
	v_mfma_f32_16x16x32_bf16 v[88:91], v[174:177], v[194:197], v[88:91]
	v_mfma_f32_16x16x32_bf16 v[80:83], v[166:169], v[202:205], v[80:83]
	v_mfma_f32_16x16x32_bf16 v[72:75], v[174:177], v[202:205], v[72:75]
	v_mfma_f32_16x16x32_bf16 v[68:71], v[166:169], v[210:213], v[68:71]
	v_mfma_f32_16x16x32_bf16 v[64:67], v[174:177], v[210:213], v[64:67]
	v_mfma_f32_16x16x32_bf16 v[116:119], v[170:173], v[190:193], v[116:119]
	v_mfma_f32_16x16x32_bf16 v[104:107], v[178:181], v[190:193], v[104:107]
	v_mfma_f32_16x16x32_bf16 v[96:99], v[170:173], v[198:201], v[96:99]
	v_mfma_f32_16x16x32_bf16 v[88:91], v[178:181], v[198:201], v[88:91]
	v_mfma_f32_16x16x32_bf16 v[80:83], v[170:173], v[206:209], v[80:83]
	v_mfma_f32_16x16x32_bf16 v[72:75], v[178:181], v[206:209], v[72:75]
	v_mfma_f32_16x16x32_bf16 v[68:71], v[170:173], v[214:217], v[68:71]
	v_mfma_f32_16x16x32_bf16 v[64:67], v[178:181], v[214:217], v[64:67]
	s_barrier
	s_add_i32 s59, s50, s41
	v_lshl_add_u64 v[218:219], s[26:27], 0, v[132:133]
	s_mov_b32 m0, s59
	ds_read_b128 v[182:185], v149 offset:16384
	ds_read_b128 v[190:193], v149 offset:17408
	ds_read_b128 v[194:197], v149 offset:18432
	ds_read_b128 v[198:201], v149 offset:19456
	ds_read_b128 v[202:205], v149 offset:20480
	ds_read_b128 v[206:209], v149 offset:21504
	ds_read_b128 v[210:213], v149 offset:22528
	ds_read_b128 v[214:217], v149 offset:23552
	global_load_lds_dwordx4 v[218:219], off
	s_add_i32 m0, s59, 0x2000
	s_add_u32 s60, s26, 0x40000
	v_lshl_add_u64 v[220:221], s[26:27], 0, v[128:129]
	s_addc_u32 s61, s27, 0
	s_add_i32 s59, s51, s41
	global_load_lds_dwordx4 v[220:221], off
	v_lshl_add_u64 v[222:223], s[60:61], 0, v[132:133]
	s_mov_b32 m0, s59
	v_lshl_add_u64 v[224:225], s[30:31], 0, v[130:131]
	global_load_lds_dwordx4 v[222:223], off
	v_lshl_add_u64 v[222:223], s[60:61], 0, v[128:129]
	s_add_i32 m0, s59, 0x2000
	s_nop 0
	global_load_lds_dwordx4 v[222:223], off
	v_lshl_add_u64 v[222:223], s[30:31], 0, v[134:135]
	s_mov_b32 m0, s43
	s_nop 0
	global_load_lds_dwordx4 v[222:223], off
	s_mov_b32 m0, s44
	s_nop 0
	global_load_lds_dwordx4 v[224:225], off
	s_waitcnt vmcnt(8)
	s_waitcnt lgkmcnt(0)
	s_barrier
; #define PG8_STAGE(bufoff, gbase, voff) do { _Pragma("unroll") for (int _i = 0; _i < 2; ++_i) \
;         __builtin_amdgcn_global_load_lds((const unsigned*)((const char*)(gbase) + (voff)[_i]), (PG8_LAS unsigned*)(lds + (bufoff) + ldsw + _i * 8192), 16, 0, 0); } while (0)
; #define PG8_WAIT_V(n) asm volatile("s_waitcnt vmcnt(" #n ")" ::: "memory")
; #define PG8_WAIT_L(n) asm volatile("s_waitcnt lgkmcnt(" #n ")" ::: "memory")
; #define PG8_BAR __builtin_amdgcn_s_barrier()
; #define PG8_SCHED __builtin_amdgcn_sched_barrier(0)
; template <class Epi, class Sched, bool ALIGN_EPI = false, bool SP2 = false, bool FP8 = false, bool PEEL = false>
; __device__ __forceinline__ void gemm_phase(PG8_LAS unsigned char* lds, const Gemm g, const Sched& S, const Epi& E, const int wid) {
;     ...
;             PG8_WAIT_V(8); PG8_WAIT_L(0); PG8_BAR; PG8_MMA(1, 0, At, B0); PG8_MMA(1, 1, At, B1); PG8_BAR; PG8_SCHED;
;             PG8_LDB(B0, 1, 0); PG8_LDB(B1, 1, 1); PG8_SCHED; PG8_LDA(At, 1, 0); PG8_STAGE(PG8_SA(0, 1), a2 + hstep, voffA);
;             PG8_WAIT_V(8); PG8_WAIT_L(0); PG8_BAR; PG8_MMA(0, 0, At, B0); PG8_MMA(0, 1, At, B1); PG8_BAR; PG8_SCHED;
	s_waitcnt lgkmcnt(0)
	v_mfma_f32_16x16x32_bf16 v[60:63], v[150:153], v[182:185], v[60:63]
	v_mfma_f32_16x16x32_bf16 v[56:59], v[158:161], v[182:185], v[56:59]
	v_mfma_f32_16x16x32_bf16 v[52:55], v[150:153], v[194:197], v[52:55]
	v_mfma_f32_16x16x32_bf16 v[44:47], v[158:161], v[194:197], v[44:47]
	v_mfma_f32_16x16x32_bf16 v[36:39], v[150:153], v[202:205], v[36:39]
	v_mfma_f32_16x16x32_bf16 v[28:31], v[158:161], v[202:205], v[28:31]
	v_mfma_f32_16x16x32_bf16 v[20:23], v[150:153], v[210:213], v[20:23]
	v_mfma_f32_16x16x32_bf16 v[12:15], v[158:161], v[210:213], v[12:15]
	v_mfma_f32_16x16x32_bf16 v[60:63], v[154:157], v[190:193], v[60:63]
	v_mfma_f32_16x16x32_bf16 v[56:59], v[162:165], v[190:193], v[56:59]
	v_mfma_f32_16x16x32_bf16 v[52:55], v[154:157], v[198:201], v[52:55]
	v_mfma_f32_16x16x32_bf16 v[44:47], v[162:165], v[198:201], v[44:47]
	v_mfma_f32_16x16x32_bf16 v[36:39], v[154:157], v[206:209], v[36:39]
	v_mfma_f32_16x16x32_bf16 v[28:31], v[162:165], v[206:209], v[28:31]
	v_mfma_f32_16x16x32_bf16 v[20:23], v[154:157], v[214:217], v[20:23]
	v_mfma_f32_16x16x32_bf16 v[12:15], v[162:165], v[214:217], v[12:15]
	v_mfma_f32_16x16x32_bf16 v[48:51], v[166:169], v[182:185], v[48:51]
	v_mfma_f32_16x16x32_bf16 v[40:43], v[174:177], v[182:185], v[40:43]
	v_mfma_f32_16x16x32_bf16 v[32:35], v[166:169], v[194:197], v[32:35]
	v_mfma_f32_16x16x32_bf16 v[24:27], v[174:177], v[194:197], v[24:27]
	v_mfma_f32_16x16x32_bf16 v[16:19], v[166:169], v[202:205], v[16:19]
	v_mfma_f32_16x16x32_bf16 v[8:11], v[174:177], v[202:205], v[8:11]
	v_mfma_f32_16x16x32_bf16 v[4:7], v[166:169], v[210:213], v[4:7]
	v_mfma_f32_16x16x32_bf16 v[0:3], v[174:177], v[210:213], v[0:3]
	v_mfma_f32_16x16x32_bf16 v[48:51], v[170:173], v[190:193], v[48:51]
	v_mfma_f32_16x16x32_bf16 v[40:43], v[178:181], v[190:193], v[40:43]
	v_mfma_f32_16x16x32_bf16 v[32:35], v[170:173], v[198:201], v[32:35]
	v_mfma_f32_16x16x32_bf16 v[24:27], v[178:181], v[198:201], v[24:27]
	v_mfma_f32_16x16x32_bf16 v[16:19], v[170:173], v[206:209], v[16:19]
	v_mfma_f32_16x16x32_bf16 v[8:11], v[178:181], v[206:209], v[8:11]
	v_mfma_f32_16x16x32_bf16 v[4:7], v[170:173], v[214:217], v[4:7]
	v_mfma_f32_16x16x32_bf16 v[0:3], v[178:181], v[214:217], v[0:3]
	s_barrier
	s_add_i32 s59, 0, 0x18000
	s_add_i32 s60, 0, 0x1c000
	v_add_u32_e32 v162, s59, v148
	v_add_u32_e32 v178, s60, v148
	ds_read_b128 v[150:153], v162
	ds_read_b128 v[154:157], v162 offset:1024
	ds_read_b128 v[158:161], v162 offset:2048
	ds_read_b128 v[162:165], v162 offset:3072
	ds_read_b128 v[166:169], v178
	ds_read_b128 v[170:173], v178 offset:1024
	ds_read_b128 v[174:177], v178 offset:2048
	ds_read_b128 v[178:181], v178 offset:3072
	s_add_u32 s30, s30, 0x40000
	s_addc_u32 s31, s31, 0
	s_mov_b32 m0, s45
	v_lshl_add_u64 v[226:227], s[30:31], 0, v[134:135]
	ds_read_b128 v[182:185], v149 offset:32768
	ds_read_b128 v[190:193], v149 offset:33792
	ds_read_b128 v[194:197], v149 offset:34816
	ds_read_b128 v[198:201], v149 offset:35840
	ds_read_b128 v[202:205], v149 offset:36864
	ds_read_b128 v[206:209], v149 offset:37888
	ds_read_b128 v[210:213], v149 offset:38912
	ds_read_b128 v[214:217], v149 offset:39936
	global_load_lds_dwordx4 v[226:227], off
	v_lshl_add_u64 v[226:227], s[30:31], 0, v[130:131]
	s_mov_b32 m0, s46
	s_nop 0
	global_load_lds_dwordx4 v[226:227], off
	s_waitcnt vmcnt(8)
	s_waitcnt lgkmcnt(0)
	s_barrier
	s_waitcnt lgkmcnt(0)
	v_mfma_f32_16x16x32_bf16 v[124:127], v[150:153], v[182:185], v[124:127]
	v_mfma_f32_16x16x32_bf16 v[120:123], v[158:161], v[182:185], v[120:123]
	v_mfma_f32_16x16x32_bf16 v[112:115], v[150:153], v[194:197], v[112:115]
	v_mfma_f32_16x16x32_bf16 v[108:111], v[158:161], v[194:197], v[108:111]
	v_mfma_f32_16x16x32_bf16 v[100:103], v[150:153], v[202:205], v[100:103]
	v_mfma_f32_16x16x32_bf16 v[92:95], v[158:161], v[202:205], v[92:95]
	v_mfma_f32_16x16x32_bf16 v[84:87], v[150:153], v[210:213], v[84:87]
	v_mfma_f32_16x16x32_bf16 v[76:79], v[158:161], v[210:213], v[76:79]
	v_mfma_f32_16x16x32_bf16 v[124:127], v[154:157], v[190:193], v[124:127]
	v_mfma_f32_16x16x32_bf16 v[120:123], v[162:165], v[190:193], v[120:123]
	v_mfma_f32_16x16x32_bf16 v[112:115], v[154:157], v[198:201], v[112:115]
	v_mfma_f32_16x16x32_bf16 v[108:111], v[162:165], v[198:201], v[108:111]
	v_mfma_f32_16x16x32_bf16 v[100:103], v[154:157], v[206:209], v[100:103]
	v_mfma_f32_16x16x32_bf16 v[92:95], v[162:165], v[206:209], v[92:95]
	v_mfma_f32_16x16x32_bf16 v[84:87], v[154:157], v[214:217], v[84:87]
	v_mfma_f32_16x16x32_bf16 v[76:79], v[162:165], v[214:217], v[76:79]
	v_mfma_f32_16x16x32_bf16 v[116:119], v[166:169], v[182:185], v[116:119]
	v_mfma_f32_16x16x32_bf16 v[104:107], v[174:177], v[182:185], v[104:107]
	v_mfma_f32_16x16x32_bf16 v[96:99], v[166:169], v[194:197], v[96:99]
	v_mfma_f32_16x16x32_bf16 v[88:91], v[174:177], v[194:197], v[88:91]
	v_mfma_f32_16x16x32_bf16 v[80:83], v[166:169], v[202:205], v[80:83]
	v_mfma_f32_16x16x32_bf16 v[72:75], v[174:177], v[202:205], v[72:75]
	v_mfma_f32_16x16x32_bf16 v[68:71], v[166:169], v[210:213], v[68:71]
	v_mfma_f32_16x16x32_bf16 v[64:67], v[174:177], v[210:213], v[64:67]
	v_mfma_f32_16x16x32_bf16 v[116:119], v[170:173], v[190:193], v[116:119]
	v_mfma_f32_16x16x32_bf16 v[104:107], v[178:181], v[190:193], v[104:107]
	v_mfma_f32_16x16x32_bf16 v[96:99], v[170:173], v[198:201], v[96:99]
	v_mfma_f32_16x16x32_bf16 v[88:91], v[178:181], v[198:201], v[88:91]
	v_mfma_f32_16x16x32_bf16 v[80:83], v[170:173], v[206:209], v[80:83]
	v_mfma_f32_16x16x32_bf16 v[72:75], v[178:181], v[206:209], v[72:75]
	v_mfma_f32_16x16x32_bf16 v[68:71], v[170:173], v[214:217], v[68:71]
	v_mfma_f32_16x16x32_bf16 v[64:67], v[178:181], v[214:217], v[64:67]
	s_barrier
; #define PG8_STAGE(bufoff, gbase, voff) do { _Pragma("unroll") for (int _i = 0; _i < 2; ++_i) \
;         __builtin_amdgcn_global_load_lds((const unsigned*)((const char*)(gbase) + (voff)[_i]), (PG8_LAS unsigned*)(lds + (bufoff) + ldsw + _i * 8192), 16, 0, 0); } while (0)
; #define PG8_WAIT_V(n) asm volatile("s_waitcnt vmcnt(" #n ")" ::: "memory")
; #define PG8_WAIT_L(n) asm volatile("s_waitcnt lgkmcnt(" #n ")" ::: "memory")
; #define PG8_BAR __builtin_amdgcn_s_barrier()
; #define PG8_SCHED __builtin_amdgcn_sched_barrier(0)
; template <class Epi, class Sched, bool ALIGN_EPI = false, bool SP2 = false, bool FP8 = false, bool PEEL = false>
; __device__ __forceinline__ void gemm_phase(PG8_LAS unsigned char* lds, const Gemm g, const Sched& S, const Epi& E, const int wid) {
;     ...
;             PG8_LDA(At, 1, 1); PG8_STAGE(PG8_SB(1, 0), b3, voffB); PG8_STAGE(PG8_SB(1, 1), b3 + hstep, voffB); PG8_STAGE(PG8_SA(1, 0), a3, voffA);
;             PG8_WAIT_V(8); PG8_WAIT_L(0); PG8_BAR; PG8_MMA(1, 0, At, B0); PG8_MMA(1, 1, At, B1); PG8_BAR; PG8_SCHED;
;     ...
;         for (int a = 0; a < 2; ++a)
; #pragma unroll
;             for (int b = 0; b < 2; ++b)
; #pragma unroll
;                 for (int m = 0; m < 4; ++m)
; #pragma unroll
;                     for (int n = 0; n < 2; ++n) acc[a][b][m][n] = (f32x4){0.f, 0.f, 0.f, 0.f};
	s_add_i32 s30, s59, s41
	v_lshl_add_u64 v[218:219], v[218:219], 0, s[12:13]
	s_mov_b32 m0, s30
	ds_read_b128 v[182:185], v149 offset:49152
	ds_read_b128 v[190:193], v149 offset:50176
	ds_read_b128 v[194:197], v149 offset:51200
	ds_read_b128 v[198:201], v149 offset:52224
	ds_read_b128 v[202:205], v149 offset:53248
	ds_read_b128 v[206:209], v149 offset:54272
	ds_read_b128 v[210:213], v149 offset:55296
	ds_read_b128 v[214:217], v149 offset:56320
	global_load_lds_dwordx4 v[218:219], off
	s_add_i32 m0, s30, 0x2000
	s_add_u32 s26, s26, 0x40080
	v_lshl_add_u64 v[218:219], v[220:221], 0, s[12:13]
	s_addc_u32 s27, s27, 0
	s_add_i32 s30, s60, s41
	global_load_lds_dwordx4 v[218:219], off
	v_lshl_add_u64 v[218:219], s[26:27], 0, v[132:133]
	s_mov_b32 m0, s30
	s_nop 0
	global_load_lds_dwordx4 v[218:219], off
	v_lshl_add_u64 v[218:219], s[26:27], 0, v[128:129]
	s_add_i32 m0, s30, 0x2000
	s_nop 0
	global_load_lds_dwordx4 v[218:219], off
	v_lshl_add_u64 v[218:219], v[222:223], 0, s[12:13]
	s_mov_b32 m0, s47
	s_nop 0
	global_load_lds_dwordx4 v[218:219], off
	v_lshl_add_u64 v[218:219], v[224:225], 0, s[12:13]
	s_mov_b32 m0, s48
	s_nop 0
	global_load_lds_dwordx4 v[218:219], off
	s_waitcnt vmcnt(8)
	s_waitcnt lgkmcnt(0)
	s_barrier
	s_waitcnt lgkmcnt(0)
	v_mfma_f32_16x16x32_bf16 v[60:63], v[150:153], v[182:185], v[60:63]
	v_mfma_f32_16x16x32_bf16 v[56:59], v[158:161], v[182:185], v[56:59]
	v_mfma_f32_16x16x32_bf16 v[52:55], v[150:153], v[194:197], v[52:55]
	v_mfma_f32_16x16x32_bf16 v[44:47], v[158:161], v[194:197], v[44:47]
	v_mfma_f32_16x16x32_bf16 v[36:39], v[150:153], v[202:205], v[36:39]
	v_mfma_f32_16x16x32_bf16 v[28:31], v[158:161], v[202:205], v[28:31]
	v_mfma_f32_16x16x32_bf16 v[20:23], v[150:153], v[210:213], v[20:23]
	v_mfma_f32_16x16x32_bf16 v[12:15], v[158:161], v[210:213], v[12:15]
	v_mfma_f32_16x16x32_bf16 v[60:63], v[154:157], v[190:193], v[60:63]
	v_mfma_f32_16x16x32_bf16 v[56:59], v[162:165], v[190:193], v[56:59]
	v_mfma_f32_16x16x32_bf16 v[52:55], v[154:157], v[198:201], v[52:55]
	v_mfma_f32_16x16x32_bf16 v[44:47], v[162:165], v[198:201], v[44:47]
	v_mfma_f32_16x16x32_bf16 v[36:39], v[154:157], v[206:209], v[36:39]
	v_mfma_f32_16x16x32_bf16 v[28:31], v[162:165], v[206:209], v[28:31]
	v_mfma_f32_16x16x32_bf16 v[20:23], v[154:157], v[214:217], v[20:23]
	v_mfma_f32_16x16x32_bf16 v[12:15], v[162:165], v[214:217], v[12:15]
	v_mfma_f32_16x16x32_bf16 v[48:51], v[166:169], v[182:185], v[48:51]
	v_mfma_f32_16x16x32_bf16 v[40:43], v[174:177], v[182:185], v[40:43]
	v_mfma_f32_16x16x32_bf16 v[32:35], v[166:169], v[194:197], v[32:35]
	v_mfma_f32_16x16x32_bf16 v[24:27], v[174:177], v[194:197], v[24:27]
	v_mfma_f32_16x16x32_bf16 v[16:19], v[166:169], v[202:205], v[16:19]
	v_mfma_f32_16x16x32_bf16 v[8:11], v[174:177], v[202:205], v[8:11]
	v_mfma_f32_16x16x32_bf16 v[4:7], v[166:169], v[210:213], v[4:7]
	v_mfma_f32_16x16x32_bf16 v[0:3], v[174:177], v[210:213], v[0:3]
	v_mfma_f32_16x16x32_bf16 v[48:51], v[170:173], v[190:193], v[48:51]
	v_mfma_f32_16x16x32_bf16 v[40:43], v[178:181], v[190:193], v[40:43]
	v_mfma_f32_16x16x32_bf16 v[32:35], v[170:173], v[198:201], v[32:35]
	v_mfma_f32_16x16x32_bf16 v[24:27], v[178:181], v[198:201], v[24:27]
	v_mfma_f32_16x16x32_bf16 v[16:19], v[170:173], v[206:209], v[16:19]
	v_mfma_f32_16x16x32_bf16 v[8:11], v[178:181], v[206:209], v[8:11]
	v_mfma_f32_16x16x32_bf16 v[4:7], v[170:173], v[214:217], v[4:7]
	v_mfma_f32_16x16x32_bf16 v[0:3], v[178:181], v[214:217], v[0:3]
	s_barrier
	s_add_i32 s58, s58, 2
	s_add_u32 s24, s24, 0x100
	s_addc_u32 s25, s25, 0
	s_cmp_gt_u32 s58, 13
	s_cbranch_scc0 .LBB0_659
	s_add_u32 s24, s54, 0xffffff00
	s_addc_u32 s25, s55, -1
	s_andn2_b64 vcc, exec, s[10:11]
	s_cbranch_vccnz .LBB0_662
	v_mov_b32_e32 v0, 0
	s_mov_b32 s4, s14
	s_mov_b32 s3, s52
	s_mov_b64 s[6:7], s[22:23]
	s_mov_b32 s49, s53
	v_mov_b32_e32 v1, v0
	v_mov_b32_e32 v2, v0
	v_mov_b32_e32 v3, v0
	v_mov_b32_e32 v4, v0
	v_mov_b32_e32 v5, v0
	v_mov_b32_e32 v6, v0
	v_mov_b32_e32 v7, v0
	v_mov_b32_e32 v8, v0
	v_mov_b32_e32 v9, v0
	v_mov_b32_e32 v10, v0
	v_mov_b32_e32 v11, v0
	v_mov_b32_e32 v16, v0
	v_mov_b32_e32 v17, v0
	v_mov_b32_e32 v18, v0
	v_mov_b32_e32 v19, v0
	v_mov_b32_e32 v24, v0
	v_mov_b32_e32 v25, v0
	v_mov_b32_e32 v26, v0
	v_mov_b32_e32 v27, v0
	v_mov_b32_e32 v32, v0
	v_mov_b32_e32 v33, v0
	v_mov_b32_e32 v34, v0
	v_mov_b32_e32 v35, v0
	v_mov_b32_e32 v40, v0
	v_mov_b32_e32 v41, v0
	v_mov_b32_e32 v42, v0
	v_mov_b32_e32 v43, v0
	v_mov_b32_e32 v48, v0
	v_mov_b32_e32 v49, v0
	v_mov_b32_e32 v50, v0
	v_mov_b32_e32 v51, v0
	v_mov_b32_e32 v12, v0
	v_mov_b32_e32 v13, v0
	v_mov_b32_e32 v14, v0
	v_mov_b32_e32 v15, v0
	v_mov_b32_e32 v20, v0
	v_mov_b32_e32 v21, v0
	v_mov_b32_e32 v22, v0
	v_mov_b32_e32 v23, v0
	v_mov_b32_e32 v28, v0
	v_mov_b32_e32 v29, v0
	v_mov_b32_e32 v30, v0
	v_mov_b32_e32 v31, v0
	v_mov_b32_e32 v36, v0
	v_mov_b32_e32 v37, v0
	v_mov_b32_e32 v38, v0
	v_mov_b32_e32 v39, v0
	v_mov_b32_e32 v44, v0
	v_mov_b32_e32 v45, v0
	v_mov_b32_e32 v46, v0
	v_mov_b32_e32 v47, v0
	v_mov_b32_e32 v52, v0
	v_mov_b32_e32 v53, v0
	v_mov_b32_e32 v54, v0
	v_mov_b32_e32 v55, v0
	v_mov_b32_e32 v56, v0
	v_mov_b32_e32 v57, v0
	v_mov_b32_e32 v58, v0
	v_mov_b32_e32 v59, v0
	v_mov_b32_e32 v60, v0
	v_mov_b32_e32 v61, v0
	v_mov_b32_e32 v62, v0
	v_mov_b32_e32 v63, v0
	v_mov_b32_e32 v64, v0
	v_mov_b32_e32 v65, v0
	v_mov_b32_e32 v66, v0
	v_mov_b32_e32 v67, v0
	v_mov_b32_e32 v68, v0
	v_mov_b32_e32 v69, v0
	v_mov_b32_e32 v70, v0
	v_mov_b32_e32 v71, v0
	v_mov_b32_e32 v72, v0
	v_mov_b32_e32 v73, v0
	v_mov_b32_e32 v74, v0
	v_mov_b32_e32 v75, v0
	v_mov_b32_e32 v80, v0
	v_mov_b32_e32 v81, v0
	v_mov_b32_e32 v82, v0
	v_mov_b32_e32 v83, v0
	v_mov_b32_e32 v88, v0
	v_mov_b32_e32 v89, v0
	v_mov_b32_e32 v90, v0
	v_mov_b32_e32 v91, v0
	v_mov_b32_e32 v96, v0
	v_mov_b32_e32 v97, v0
	v_mov_b32_e32 v98, v0
	v_mov_b32_e32 v99, v0
	v_mov_b32_e32 v104, v0
	v_mov_b32_e32 v105, v0
	v_mov_b32_e32 v106, v0
	v_mov_b32_e32 v107, v0
	v_mov_b32_e32 v116, v0
	v_mov_b32_e32 v117, v0
	v_mov_b32_e32 v118, v0
	v_mov_b32_e32 v119, v0
	v_mov_b32_e32 v76, v0
	v_mov_b32_e32 v77, v0
	v_mov_b32_e32 v78, v0
	v_mov_b32_e32 v79, v0
	v_mov_b32_e32 v84, v0
	v_mov_b32_e32 v85, v0
	v_mov_b32_e32 v86, v0
	v_mov_b32_e32 v87, v0
	v_mov_b32_e32 v92, v0
	v_mov_b32_e32 v93, v0
	v_mov_b32_e32 v94, v0
	v_mov_b32_e32 v95, v0
	v_mov_b32_e32 v100, v0
	v_mov_b32_e32 v101, v0
	v_mov_b32_e32 v102, v0
	v_mov_b32_e32 v103, v0
	v_mov_b32_e32 v108, v0
	v_mov_b32_e32 v109, v0
	v_mov_b32_e32 v110, v0
	v_mov_b32_e32 v111, v0
	v_mov_b32_e32 v112, v0
	v_mov_b32_e32 v113, v0
	v_mov_b32_e32 v114, v0
	v_mov_b32_e32 v115, v0
	v_mov_b32_e32 v120, v0
	v_mov_b32_e32 v121, v0
	v_mov_b32_e32 v122, v0
	v_mov_b32_e32 v123, v0
	v_mov_b32_e32 v124, v0
	v_mov_b32_e32 v125, v0
	v_mov_b32_e32 v126, v0
	v_mov_b32_e32 v127, v0
	s_andn2_b64 vcc, exec, s[8:9]
	s_cbranch_vccnz .LBB0_663
	s_branch .LBB0_664

; #define PG8_STAGE(bufoff, gbase, voff) do { _Pragma("unroll") for (int _i = 0; _i < 2; ++_i) \
;         __builtin_amdgcn_global_load_lds((const unsigned*)((const char*)(gbase) + (voff)[_i]), (PG8_LAS unsigned*)(lds + (bufoff) + ldsw + _i * 8192), 16, 0, 0); } while (0)
; #define PG8_WAIT_V(n) asm volatile("s_waitcnt vmcnt(" #n ")" ::: "memory")
; #define PG8_WAIT_L(n) asm volatile("s_waitcnt lgkmcnt(" #n ")" ::: "memory")
; #define PG8_BAR __builtin_amdgcn_s_barrier()
; #define PG8_SCHED __builtin_amdgcn_sched_barrier(0)
; template <class Epi, class Sched, bool ALIGN_EPI = false, bool SP2 = false, bool FP8 = false, bool PEEL = false>
; __device__ __forceinline__ void gemm_phase(PG8_LAS unsigned char* lds, const Gemm g, const Sched& S, const Epi& E, const int wid) {
;     ...
;         {
;             const int t = 0;
;             const bool last = (t == nt - 2);
;             const char* a1 = cA + (size_t)(t + 1) * kstep;
;             const char* a2 = last ? nA : cA + (size_t)(t + 2) * kstep; const char* b2 = last ? nB : cB + (size_t)(t + 2) * kstep;
;             const char* a3 = a2 + kstep; const char* b3 = b2 + kstep;
;             if (last && has_next) S.a_ready(nxt);
;             PG8_LDB(B0, 0, 0); PG8_LDB(B1, 0, 1); PG8_SCHED; PG8_LDA(At, 0, 0); PG8_STAGE(PG8_SA(1, 1), a1 + hstep, voffA);
;             PG8_WAIT_V(8); PG8_WAIT_L(0); PG8_BAR; PG8_MMAZ(0, 0, At, B0); PG8_MMAZ(0, 1, At, B1); PG8_BAR; PG8_SCHED;
;             PG8_LDA(At, 0, 1); PG8_STAGE(PG8_SB(0, 0), b2, voffB); PG8_STAGE(PG8_SB(0, 1), b2 + hstep, voffB); PG8_STAGE(PG8_SA(0, 0), a2, voffA);
;             PG8_WAIT_V(8); PG8_WAIT_L(0); PG8_BAR; PG8_MMAZ(1, 0, At, B0); PG8_MMAZ(1, 1, At, B1); PG8_BAR; PG8_SCHED;
;             PG8_LDB(B0, 1, 0); PG8_LDB(B1, 1, 1); PG8_SCHED; PG8_LDA(At, 1, 0); PG8_STAGE(PG8_SA(0, 1), a2 + hstep, voffA);
;             PG8_WAIT_V(8); PG8_WAIT_L(0); PG8_BAR; PG8_MMA(0, 0, At, B0); PG8_MMA(0, 1, At, B1); PG8_BAR; PG8_SCHED;
.LBB0_866:
	s_ashr_i32 s27, s26, 31
	s_lshl_b64 s[30:31], s[26:27], 18
	v_add_u32_e32 v188, s56, v185
	v_add_u32_e32 v189, s57, v185
	s_add_u32 s30, s38, s30
	ds_read_b128 v[16:19], v188
	ds_read_b128 v[20:23], v188 offset:1024
	ds_read_b128 v[24:27], v188 offset:2048
	ds_read_b128 v[28:31], v188 offset:3072
	ds_read_b128 v[0:3], v189
	ds_read_b128 v[4:7], v189 offset:1024
	ds_read_b128 v[8:11], v189 offset:2048
	ds_read_b128 v[12:15], v189 offset:3072
	s_addc_u32 s31, s39, s31
	s_ashr_i32 s25, s24, 31
	s_lshl_b64 s[36:37], s[24:25], 18
	s_add_u32 s36, s3, s36
	s_addc_u32 s37, s17, s37
	s_and_b64 s[48:49], s[8:9], exec
	s_cselect_b32 s25, s31, s47
	s_cselect_b32 s27, s30, s46
	s_cselect_b32 s63, s37, s45
	s_cselect_b32 s64, s36, s44
	s_add_u32 s48, s46, 0x20080
	s_addc_u32 s49, s47, 0
	s_mov_b32 m0, s59
	v_lshl_add_u64 v[214:215], s[48:49], 0, v[166:167]
	s_add_i32 s65, s42, 0xe000
	ds_read_b128 v[176:179], v187
	ds_read_b128 v[180:183], v187 offset:1024
	ds_read_b128 v[190:193], v187 offset:2048
	ds_read_b128 v[194:197], v187 offset:3072
	ds_read_b128 v[198:201], v187 offset:4096
	ds_read_b128 v[202:205], v187 offset:5120
	ds_read_b128 v[206:209], v187 offset:6144
	ds_read_b128 v[210:213], v187 offset:7168
	global_load_lds_dwordx4 v[214:215], off
	v_lshl_add_u64 v[214:215], s[48:49], 0, v[162:163]
	s_mov_b32 m0, s65
	s_nop 0
	global_load_lds_dwordx4 v[214:215], off
	s_waitcnt vmcnt(8)
	s_waitcnt lgkmcnt(0)
	s_barrier
	s_waitcnt lgkmcnt(0)
	v_mfma_f32_16x16x128_f8f6f4 v[156:159], v[16:23], v[176:183], 0
	v_mfma_f32_16x16x128_f8f6f4 v[152:155], v[24:31], v[176:183], 0
	v_mfma_f32_16x16x128_f8f6f4 v[148:151], v[16:23], v[190:197], 0
	v_mfma_f32_16x16x128_f8f6f4 v[144:147], v[24:31], v[190:197], 0
	v_mfma_f32_16x16x128_f8f6f4 v[140:143], v[16:23], v[198:205], 0
	v_mfma_f32_16x16x128_f8f6f4 v[136:139], v[24:31], v[198:205], 0
	v_mfma_f32_16x16x128_f8f6f4 v[132:135], v[16:23], v[206:213], 0
	v_mfma_f32_16x16x128_f8f6f4 v[128:131], v[24:31], v[206:213], 0
	v_mfma_f32_16x16x128_f8f6f4 v[124:127], v[0:7], v[176:183], 0
	v_mfma_f32_16x16x128_f8f6f4 v[120:123], v[8:15], v[176:183], 0
	v_mfma_f32_16x16x128_f8f6f4 v[116:119], v[0:7], v[190:197], 0
	v_mfma_f32_16x16x128_f8f6f4 v[112:115], v[8:15], v[190:197], 0
	v_mfma_f32_16x16x128_f8f6f4 v[108:111], v[0:7], v[198:205], 0
	v_mfma_f32_16x16x128_f8f6f4 v[104:107], v[8:15], v[198:205], 0
	v_mfma_f32_16x16x128_f8f6f4 v[100:103], v[0:7], v[206:213], 0
	v_mfma_f32_16x16x128_f8f6f4 v[96:99], v[8:15], v[206:213], 0
	s_barrier
	v_lshl_add_u64 v[176:177], s[44:45], 0, v[164:165]
	s_add_i32 s66, s56, s23
	v_lshl_add_u64 v[178:179], v[176:177], 0, s[12:13]
	s_mov_b32 m0, s66
	s_add_i32 s67, s66, 0x2000
	ds_read_b128 v[190:193], v187 offset:16384
	ds_read_b128 v[194:197], v187 offset:17408
	ds_read_b128 v[198:201], v187 offset:18432
	ds_read_b128 v[202:205], v187 offset:19456
	ds_read_b128 v[206:209], v187 offset:20480
	ds_read_b128 v[210:213], v187 offset:21504
	ds_read_b128 v[214:217], v187 offset:22528
	ds_read_b128 v[218:221], v187 offset:23552
	global_load_lds_dwordx4 v[178:179], off
	v_lshl_add_u64 v[178:179], s[44:45], 0, v[160:161]
	s_add_u32 s48, s44, 0x20100
	v_lshl_add_u64 v[180:181], v[178:179], 0, s[12:13]
	s_mov_b32 m0, s67
	s_addc_u32 s49, s45, 0
	s_add_i32 s75, s57, s23
	global_load_lds_dwordx4 v[180:181], off
	v_lshl_add_u64 v[180:181], s[48:49], 0, v[164:165]
	s_mov_b32 m0, s75
	s_add_i32 s84, s75, 0x2000
	global_load_lds_dwordx4 v[180:181], off
	v_lshl_add_u64 v[180:181], s[48:49], 0, v[160:161]
	s_mov_b32 m0, s84
	s_nop 0
	global_load_lds_dwordx4 v[180:181], off
	v_lshl_add_u64 v[180:181], s[46:47], 0, v[166:167]
	v_lshl_add_u64 v[182:183], v[180:181], 0, s[12:13]
	s_mov_b32 m0, s42
	s_nop 0
	global_load_lds_dwordx4 v[182:183], off
	v_lshl_add_u64 v[182:183], s[46:47], 0, v[162:163]
	v_lshl_add_u64 v[222:223], v[182:183], 0, s[12:13]
	s_mov_b32 m0, s43
	s_nop 0
	global_load_lds_dwordx4 v[222:223], off
	s_waitcnt vmcnt(8)
	s_waitcnt lgkmcnt(0)
	s_barrier
	s_waitcnt lgkmcnt(0)
	v_mfma_f32_16x16x128_f8f6f4 v[92:95], v[16:23], v[190:197], 0
	v_mfma_f32_16x16x128_f8f6f4 v[88:91], v[24:31], v[190:197], 0
	v_mfma_f32_16x16x128_f8f6f4 v[84:87], v[16:23], v[198:205], 0
	v_mfma_f32_16x16x128_f8f6f4 v[80:83], v[24:31], v[198:205], 0
	v_mfma_f32_16x16x128_f8f6f4 v[76:79], v[16:23], v[206:213], 0
	v_mfma_f32_16x16x128_f8f6f4 v[72:75], v[24:31], v[206:213], 0
	v_mfma_f32_16x16x128_f8f6f4 v[68:71], v[16:23], v[214:221], 0
	v_mfma_f32_16x16x128_f8f6f4 v[64:67], v[24:31], v[214:221], 0
	v_mfma_f32_16x16x128_f8f6f4 v[60:63], v[0:7], v[190:197], 0
	v_mfma_f32_16x16x128_f8f6f4 v[56:59], v[8:15], v[190:197], 0
	v_mfma_f32_16x16x128_f8f6f4 v[52:55], v[0:7], v[198:205], 0
	v_mfma_f32_16x16x128_f8f6f4 v[48:51], v[8:15], v[198:205], 0
	v_mfma_f32_16x16x128_f8f6f4 v[44:47], v[0:7], v[206:213], 0
	v_mfma_f32_16x16x128_f8f6f4 v[40:43], v[8:15], v[206:213], 0
	v_mfma_f32_16x16x128_f8f6f4 v[36:39], v[0:7], v[214:221], 0
	v_mfma_f32_16x16x128_f8f6f4 v[32:35], v[8:15], v[214:221], 0
	s_barrier
	s_add_i32 s85, 0, 0x18000
	s_add_i32 s87, 0, 0x1c000
	v_add_u32_e32 v190, s85, v185
	v_add_u32_e32 v191, s87, v185
	ds_read_b128 v[16:19], v190
	ds_read_b128 v[20:23], v190 offset:1024
	ds_read_b128 v[24:27], v190 offset:2048
	ds_read_b128 v[28:31], v190 offset:3072
	ds_read_b128 v[0:3], v191
	ds_read_b128 v[4:7], v191 offset:1024
	ds_read_b128 v[8:11], v191 offset:2048
	ds_read_b128 v[12:15], v191 offset:3072
	s_add_u32 s48, s46, 0x20100
	s_addc_u32 s49, s47, 0
	s_mov_b32 m0, s50
	v_lshl_add_u64 v[224:225], s[48:49], 0, v[166:167]
	ds_read_b128 v[192:195], v187 offset:32768
	ds_read_b128 v[196:199], v187 offset:33792
	ds_read_b128 v[200:203], v187 offset:34816
	ds_read_b128 v[204:207], v187 offset:35840
	ds_read_b128 v[208:211], v187 offset:36864
	ds_read_b128 v[212:215], v187 offset:37888
	ds_read_b128 v[216:219], v187 offset:38912
	ds_read_b128 v[220:223], v187 offset:39936
	global_load_lds_dwordx4 v[224:225], off
	v_lshl_add_u64 v[224:225], s[48:49], 0, v[162:163]
	s_mov_b32 m0, s51
	s_nop 0
	global_load_lds_dwordx4 v[224:225], off
	s_waitcnt vmcnt(8)
	s_waitcnt lgkmcnt(0)
	s_barrier
; #define PG8_STAGE(bufoff, gbase, voff) do { _Pragma("unroll") for (int _i = 0; _i < 2; ++_i) \
;         __builtin_amdgcn_global_load_lds((const unsigned*)((const char*)(gbase) + (voff)[_i]), (PG8_LAS unsigned*)(lds + (bufoff) + ldsw + _i * 8192), 16, 0, 0); } while (0)
; #define PG8_WAIT_V(n) asm volatile("s_waitcnt vmcnt(" #n ")" ::: "memory")
; #define PG8_WAIT_L(n) asm volatile("s_waitcnt lgkmcnt(" #n ")" ::: "memory")
; #define PG8_BAR __builtin_amdgcn_s_barrier()
; #define PG8_SCHED __builtin_amdgcn_sched_barrier(0)
; template <class Epi, class Sched, bool ALIGN_EPI = false, bool SP2 = false, bool FP8 = false, bool PEEL = false>
; __device__ __forceinline__ void gemm_phase(PG8_LAS unsigned char* lds, const Gemm g, const Sched& S, const Epi& E, const int wid) {
;     ...
;             PG8_LDA(At, 1, 1); PG8_STAGE(PG8_SB(1, 0), b3, voffB); PG8_STAGE(PG8_SB(1, 1), b3 + hstep, voffB); PG8_STAGE(PG8_SA(1, 0), a3, voffA);
;             PG8_WAIT_V(8); PG8_WAIT_L(0); PG8_BAR; PG8_MMA(1, 0, At, B0); PG8_MMA(1, 1, At, B1); PG8_BAR; PG8_SCHED;
;         }
; #pragma unroll 1
;         for (int t = 2; t < nt; t += 2) {
;             const bool last = (t == nt - 2);
;             const char* a1 = cA + (size_t)(t + 1) * kstep;
;             const char* a2 = last ? nA : cA + (size_t)(t + 2) * kstep; const char* b2 = last ? nB : cB + (size_t)(t + 2) * kstep;
;             const char* a3 = a2 + kstep; const char* b3 = b2 + kstep;
;             if (last && has_next) S.a_ready(nxt);
;             PG8_LDB(B0, 0, 0); PG8_LDB(B1, 0, 1); PG8_SCHED; PG8_LDA(At, 0, 0); PG8_STAGE(PG8_SA(1, 1), a1 + hstep, voffA);
;             PG8_WAIT_V(8); PG8_WAIT_L(0); PG8_BAR; PG8_MMA(0, 0, At, B0); PG8_MMA(0, 1, At, B1); PG8_BAR; PG8_SCHED;
;             PG8_LDA(At, 0, 1); PG8_STAGE(PG8_SB(0, 0), b2, voffB); PG8_STAGE(PG8_SB(0, 1), b2 + hstep, voffB); PG8_STAGE(PG8_SA(0, 0), a2, voffA);
	s_waitcnt lgkmcnt(0)
	v_mfma_f32_16x16x128_f8f6f4 v[156:159], v[16:23], v[192:199], v[156:159]
	v_mfma_f32_16x16x128_f8f6f4 v[152:155], v[24:31], v[192:199], v[152:155]
	v_mfma_f32_16x16x128_f8f6f4 v[148:151], v[16:23], v[200:207], v[148:151]
	v_mfma_f32_16x16x128_f8f6f4 v[144:147], v[24:31], v[200:207], v[144:147]
	v_mfma_f32_16x16x128_f8f6f4 v[140:143], v[16:23], v[208:215], v[140:143]
	v_mfma_f32_16x16x128_f8f6f4 v[136:139], v[24:31], v[208:215], v[136:139]
	v_mfma_f32_16x16x128_f8f6f4 v[132:135], v[16:23], v[216:223], v[132:135]
	v_mfma_f32_16x16x128_f8f6f4 v[128:131], v[24:31], v[216:223], v[128:131]
	v_mfma_f32_16x16x128_f8f6f4 v[124:127], v[0:7], v[192:199], v[124:127]
	v_mfma_f32_16x16x128_f8f6f4 v[120:123], v[8:15], v[192:199], v[120:123]
	v_mfma_f32_16x16x128_f8f6f4 v[116:119], v[0:7], v[200:207], v[116:119]
	v_mfma_f32_16x16x128_f8f6f4 v[112:115], v[8:15], v[200:207], v[112:115]
	v_mfma_f32_16x16x128_f8f6f4 v[108:111], v[0:7], v[208:215], v[108:111]
	v_mfma_f32_16x16x128_f8f6f4 v[104:107], v[8:15], v[208:215], v[104:107]
	v_mfma_f32_16x16x128_f8f6f4 v[100:103], v[0:7], v[216:223], v[100:103]
	v_mfma_f32_16x16x128_f8f6f4 v[96:99], v[8:15], v[216:223], v[96:99]
	s_barrier
	s_add_i32 s85, s85, s23
	s_add_i32 s86, s85, 0x2000
	v_lshl_add_u64 v[176:177], v[176:177], 0, s[14:15]
	s_mov_b32 m0, s85
	s_add_u32 s48, s44, 0x20180
	ds_read_b128 v[192:195], v187 offset:49152
	ds_read_b128 v[196:199], v187 offset:50176
	ds_read_b128 v[200:203], v187 offset:51200
	ds_read_b128 v[204:207], v187 offset:52224
	ds_read_b128 v[208:211], v187 offset:53248
	ds_read_b128 v[212:215], v187 offset:54272
	ds_read_b128 v[216:219], v187 offset:55296
	ds_read_b128 v[220:223], v187 offset:56320
	global_load_lds_dwordx4 v[176:177], off
	v_lshl_add_u64 v[176:177], v[178:179], 0, s[14:15]
	s_mov_b32 m0, s86
	s_addc_u32 s49, s45, 0
	s_add_i32 s87, s87, s23
	global_load_lds_dwordx4 v[176:177], off
	v_lshl_add_u64 v[176:177], s[48:49], 0, v[164:165]
	s_mov_b32 m0, s87
	s_add_i32 s88, s87, 0x2000
	global_load_lds_dwordx4 v[176:177], off
	v_lshl_add_u64 v[176:177], s[48:49], 0, v[160:161]
	s_mov_b32 m0, s88
	s_nop 0
	global_load_lds_dwordx4 v[176:177], off
	v_lshl_add_u64 v[176:177], v[180:181], 0, s[14:15]
	s_mov_b32 m0, s54
	s_nop 0
	global_load_lds_dwordx4 v[176:177], off
	v_lshl_add_u64 v[176:177], v[182:183], 0, s[14:15]
	s_mov_b32 m0, s55
	s_nop 0
	global_load_lds_dwordx4 v[176:177], off
	s_waitcnt vmcnt(8)
	s_waitcnt lgkmcnt(0)
	s_barrier
	s_waitcnt lgkmcnt(0)
	v_mfma_f32_16x16x128_f8f6f4 v[92:95], v[16:23], v[192:199], v[92:95]
	v_mfma_f32_16x16x128_f8f6f4 v[88:91], v[24:31], v[192:199], v[88:91]
	v_mfma_f32_16x16x128_f8f6f4 v[84:87], v[16:23], v[200:207], v[84:87]
	v_mfma_f32_16x16x128_f8f6f4 v[80:83], v[24:31], v[200:207], v[80:83]
	v_mfma_f32_16x16x128_f8f6f4 v[76:79], v[16:23], v[208:215], v[76:79]
	v_mfma_f32_16x16x128_f8f6f4 v[72:75], v[24:31], v[208:215], v[72:75]
	v_mfma_f32_16x16x128_f8f6f4 v[68:71], v[16:23], v[216:223], v[68:71]
	v_mfma_f32_16x16x128_f8f6f4 v[64:67], v[24:31], v[216:223], v[64:67]
	v_mfma_f32_16x16x128_f8f6f4 v[60:63], v[0:7], v[192:199], v[60:63]
	v_mfma_f32_16x16x128_f8f6f4 v[56:59], v[8:15], v[192:199], v[56:59]
	v_mfma_f32_16x16x128_f8f6f4 v[52:55], v[0:7], v[200:207], v[52:55]
	v_mfma_f32_16x16x128_f8f6f4 v[48:51], v[8:15], v[200:207], v[48:51]
	v_mfma_f32_16x16x128_f8f6f4 v[44:47], v[0:7], v[208:215], v[44:47]
	v_mfma_f32_16x16x128_f8f6f4 v[40:43], v[8:15], v[208:215], v[40:43]
	v_mfma_f32_16x16x128_f8f6f4 v[36:39], v[0:7], v[216:223], v[36:39]
	v_mfma_f32_16x16x128_f8f6f4 v[32:35], v[8:15], v[216:223], v[32:35]
	s_barrier
	s_add_u32 s46, s46, 0x20180
	s_addc_u32 s47, s47, 0
	s_add_u32 s89, s44, 0x200
	s_addc_u32 s90, s45, 0
	s_mov_b32 s91, 0
.LBB0_867:
	ds_read_b128 v[0:3], v188
	ds_read_b128 v[4:7], v188 offset:1024
	ds_read_b128 v[16:19], v188 offset:2048
	ds_read_b128 v[20:23], v188 offset:3072
	ds_read_b128 v[24:27], v189
	ds_read_b128 v[28:31], v189 offset:1024
	ds_read_b128 v[176:179], v189 offset:2048
	ds_read_b128 v[180:183], v189 offset:3072
	s_add_u32 s44, s46, 0xfffe0080
	s_addc_u32 s45, s47, -1
	s_cmp_eq_u32 s91, 4
	s_cselect_b32 s49, s25, s45
	s_cselect_b32 s48, s27, s44
	s_cselect_b32 s45, s63, s90
	s_cselect_b32 s44, s64, s89
	s_mov_b32 m0, s59
	v_lshl_add_u64 v[216:217], s[46:47], 0, v[168:169]
	ds_read_b128 v[8:11], v187
	ds_read_b128 v[12:15], v187 offset:1024
	ds_read_b128 v[192:195], v187 offset:2048
	ds_read_b128 v[196:199], v187 offset:3072
	ds_read_b128 v[200:203], v187 offset:4096
	ds_read_b128 v[204:207], v187 offset:5120
	ds_read_b128 v[208:211], v187 offset:6144
	ds_read_b128 v[212:215], v187 offset:7168
	global_load_lds_dwordx4 v[216:217], off
	v_lshl_add_u64 v[216:217], s[46:47], 0, v[170:171]
	s_mov_b32 m0, s65
	s_nop 0
	global_load_lds_dwordx4 v[216:217], off
	s_waitcnt vmcnt(8)
	s_waitcnt lgkmcnt(0)
	s_barrier
	s_waitcnt lgkmcnt(0)
	v_mfma_f32_16x16x128_f8f6f4 v[156:159], v[0:7], v[8:15], v[156:159]
	v_mfma_f32_16x16x128_f8f6f4 v[152:155], v[16:23], v[8:15], v[152:155]
	v_mfma_f32_16x16x128_f8f6f4 v[148:151], v[0:7], v[192:199], v[148:151]
	v_mfma_f32_16x16x128_f8f6f4 v[144:147], v[16:23], v[192:199], v[144:147]
	v_mfma_f32_16x16x128_f8f6f4 v[140:143], v[0:7], v[200:207], v[140:143]
	v_mfma_f32_16x16x128_f8f6f4 v[136:139], v[16:23], v[200:207], v[136:139]
	v_mfma_f32_16x16x128_f8f6f4 v[132:135], v[0:7], v[208:215], v[132:135]
	v_mfma_f32_16x16x128_f8f6f4 v[128:131], v[16:23], v[208:215], v[128:131]
	v_mfma_f32_16x16x128_f8f6f4 v[124:127], v[24:31], v[8:15], v[124:127]
	v_mfma_f32_16x16x128_f8f6f4 v[120:123], v[176:183], v[8:15], v[120:123]
	v_mfma_f32_16x16x128_f8f6f4 v[116:119], v[24:31], v[192:199], v[116:119]
	v_mfma_f32_16x16x128_f8f6f4 v[112:115], v[176:183], v[192:199], v[112:115]
	v_mfma_f32_16x16x128_f8f6f4 v[108:111], v[24:31], v[200:207], v[108:111]
	v_mfma_f32_16x16x128_f8f6f4 v[104:107], v[176:183], v[200:207], v[104:107]
	v_mfma_f32_16x16x128_f8f6f4 v[100:103], v[24:31], v[208:215], v[100:103]
	v_mfma_f32_16x16x128_f8f6f4 v[96:99], v[176:183], v[208:215], v[96:99]
	s_barrier
; #define PG8_STAGE(bufoff, gbase, voff) do { _Pragma("unroll") for (int _i = 0; _i < 2; ++_i) \
;         __builtin_amdgcn_global_load_lds((const unsigned*)((const char*)(gbase) + (voff)[_i]), (PG8_LAS unsigned*)(lds + (bufoff) + ldsw + _i * 8192), 16, 0, 0); } while (0)
; #define PG8_WAIT_V(n) asm volatile("s_waitcnt vmcnt(" #n ")" ::: "memory")
; #define PG8_WAIT_L(n) asm volatile("s_waitcnt lgkmcnt(" #n ")" ::: "memory")
; #define PG8_BAR __builtin_amdgcn_s_barrier()
; #define PG8_SCHED __builtin_amdgcn_sched_barrier(0)
; template <class Epi, class Sched, bool ALIGN_EPI = false, bool SP2 = false, bool FP8 = false, bool PEEL = false>
; __device__ __forceinline__ void gemm_phase(PG8_LAS unsigned char* lds, const Gemm g, const Sched& S, const Epi& E, const int wid) {
;     ...
;             PG8_LDA(At, 0, 1); PG8_STAGE(PG8_SB(0, 0), b2, voffB); PG8_STAGE(PG8_SB(0, 1), b2 + hstep, voffB); PG8_STAGE(PG8_SA(0, 0), a2, voffA);
;             PG8_WAIT_V(8); PG8_WAIT_L(0); PG8_BAR; PG8_MMA(1, 0, At, B0); PG8_MMA(1, 1, At, B1); PG8_BAR; PG8_SCHED;
;             PG8_LDB(B0, 1, 0); PG8_LDB(B1, 1, 1); PG8_SCHED; PG8_LDA(At, 1, 0); PG8_STAGE(PG8_SA(0, 1), a2 + hstep, voffA);
;             PG8_WAIT_V(8); PG8_WAIT_L(0); PG8_BAR; PG8_MMA(0, 0, At, B0); PG8_MMA(0, 1, At, B1); PG8_BAR; PG8_SCHED;
;             PG8_LDA(At, 1, 1); PG8_STAGE(PG8_SB(1, 0), b3, voffB); PG8_STAGE(PG8_SB(1, 1), b3 + hstep, voffB); PG8_STAGE(PG8_SA(1, 0), a3, voffA);
;             PG8_WAIT_V(8); PG8_WAIT_L(0); PG8_BAR; PG8_MMA(1, 0, At, B0); PG8_MMA(1, 1, At, B1); PG8_BAR; PG8_SCHED;
;         }
	s_mov_b32 m0, s66
	v_lshl_add_u64 v[8:9], s[44:45], 0, v[164:165]
	s_add_u32 s92, s44, 0x20000
	ds_read_b128 v[192:195], v187 offset:16384
	ds_read_b128 v[196:199], v187 offset:17408
	ds_read_b128 v[200:203], v187 offset:18432
	ds_read_b128 v[204:207], v187 offset:19456
	ds_read_b128 v[208:211], v187 offset:20480
	ds_read_b128 v[212:215], v187 offset:21504
	ds_read_b128 v[216:219], v187 offset:22528
	ds_read_b128 v[220:223], v187 offset:23552
	global_load_lds_dwordx4 v[8:9], off
	v_lshl_add_u64 v[10:11], s[44:45], 0, v[160:161]
	s_mov_b32 m0, s67
	s_addc_u32 s93, s45, 0
	global_load_lds_dwordx4 v[10:11], off
	v_lshl_add_u64 v[12:13], s[92:93], 0, v[164:165]
	s_mov_b32 m0, s75
	v_lshl_add_u64 v[14:15], s[48:49], 0, v[162:163]
	global_load_lds_dwordx4 v[12:13], off
	v_lshl_add_u64 v[12:13], s[92:93], 0, v[160:161]
	s_mov_b32 m0, s84
	s_nop 0
	global_load_lds_dwordx4 v[12:13], off
	v_lshl_add_u64 v[12:13], s[48:49], 0, v[166:167]
	s_mov_b32 m0, s42
	s_nop 0
	global_load_lds_dwordx4 v[12:13], off
	s_mov_b32 m0, s43
	s_nop 0
	global_load_lds_dwordx4 v[14:15], off
	s_waitcnt vmcnt(8)
	s_waitcnt lgkmcnt(0)
	s_barrier
	s_waitcnt lgkmcnt(0)
	v_mfma_f32_16x16x128_f8f6f4 v[92:95], v[0:7], v[192:199], v[92:95]
	v_mfma_f32_16x16x128_f8f6f4 v[88:91], v[16:23], v[192:199], v[88:91]
	v_mfma_f32_16x16x128_f8f6f4 v[84:87], v[0:7], v[200:207], v[84:87]
	v_mfma_f32_16x16x128_f8f6f4 v[80:83], v[16:23], v[200:207], v[80:83]
	v_mfma_f32_16x16x128_f8f6f4 v[76:79], v[0:7], v[208:215], v[76:79]
	v_mfma_f32_16x16x128_f8f6f4 v[72:75], v[16:23], v[208:215], v[72:75]
	v_mfma_f32_16x16x128_f8f6f4 v[68:71], v[0:7], v[216:223], v[68:71]
	v_mfma_f32_16x16x128_f8f6f4 v[64:67], v[16:23], v[216:223], v[64:67]
	v_mfma_f32_16x16x128_f8f6f4 v[60:63], v[24:31], v[192:199], v[60:63]
	v_mfma_f32_16x16x128_f8f6f4 v[56:59], v[176:183], v[192:199], v[56:59]
	v_mfma_f32_16x16x128_f8f6f4 v[52:55], v[24:31], v[200:207], v[52:55]
	v_mfma_f32_16x16x128_f8f6f4 v[48:51], v[176:183], v[200:207], v[48:51]
	v_mfma_f32_16x16x128_f8f6f4 v[44:47], v[24:31], v[208:215], v[44:47]
	v_mfma_f32_16x16x128_f8f6f4 v[40:43], v[176:183], v[208:215], v[40:43]
	v_mfma_f32_16x16x128_f8f6f4 v[36:39], v[24:31], v[216:223], v[36:39]
	v_mfma_f32_16x16x128_f8f6f4 v[32:35], v[176:183], v[216:223], v[32:35]
	s_barrier
	ds_read_b128 v[16:19], v190
	ds_read_b128 v[20:23], v190 offset:1024
	ds_read_b128 v[24:27], v190 offset:2048
	ds_read_b128 v[28:31], v190 offset:3072
	ds_read_b128 v[0:3], v191
	ds_read_b128 v[4:7], v191 offset:1024
	ds_read_b128 v[176:179], v191 offset:2048
	ds_read_b128 v[180:183], v191 offset:3072
	s_add_u32 s48, s48, 0x20000
	s_addc_u32 s49, s49, 0
	s_mov_b32 m0, s50
	v_lshl_add_u64 v[224:225], s[48:49], 0, v[166:167]
	ds_read_b128 v[192:195], v187 offset:32768
	ds_read_b128 v[196:199], v187 offset:33792
	ds_read_b128 v[200:203], v187 offset:34816
	ds_read_b128 v[204:207], v187 offset:35840
	ds_read_b128 v[208:211], v187 offset:36864
	ds_read_b128 v[212:215], v187 offset:37888
	ds_read_b128 v[216:219], v187 offset:38912
	ds_read_b128 v[220:223], v187 offset:39936
	global_load_lds_dwordx4 v[224:225], off
	v_lshl_add_u64 v[224:225], s[48:49], 0, v[162:163]
	s_mov_b32 m0, s51
	s_nop 0
	global_load_lds_dwordx4 v[224:225], off
	s_waitcnt vmcnt(8)
	s_waitcnt lgkmcnt(0)
	s_barrier
	s_waitcnt lgkmcnt(0)
	v_mfma_f32_16x16x128_f8f6f4 v[156:159], v[16:23], v[192:199], v[156:159]
	v_mfma_f32_16x16x128_f8f6f4 v[152:155], v[24:31], v[192:199], v[152:155]
	v_mfma_f32_16x16x128_f8f6f4 v[148:151], v[16:23], v[200:207], v[148:151]
	v_mfma_f32_16x16x128_f8f6f4 v[144:147], v[24:31], v[200:207], v[144:147]
	v_mfma_f32_16x16x128_f8f6f4 v[140:143], v[16:23], v[208:215], v[140:143]
	v_mfma_f32_16x16x128_f8f6f4 v[136:139], v[24:31], v[208:215], v[136:139]
	v_mfma_f32_16x16x128_f8f6f4 v[132:135], v[16:23], v[216:223], v[132:135]
	v_mfma_f32_16x16x128_f8f6f4 v[128:131], v[24:31], v[216:223], v[128:131]
	v_mfma_f32_16x16x128_f8f6f4 v[124:127], v[0:7], v[192:199], v[124:127]
	v_mfma_f32_16x16x128_f8f6f4 v[120:123], v[176:183], v[192:199], v[120:123]
	v_mfma_f32_16x16x128_f8f6f4 v[116:119], v[0:7], v[200:207], v[116:119]
	v_mfma_f32_16x16x128_f8f6f4 v[112:115], v[176:183], v[200:207], v[112:115]
	v_mfma_f32_16x16x128_f8f6f4 v[108:111], v[0:7], v[208:215], v[108:111]
	v_mfma_f32_16x16x128_f8f6f4 v[104:107], v[176:183], v[208:215], v[104:107]
	v_mfma_f32_16x16x128_f8f6f4 v[100:103], v[0:7], v[216:223], v[100:103]
	v_mfma_f32_16x16x128_f8f6f4 v[96:99], v[176:183], v[216:223], v[96:99]
	s_barrier
	s_mov_b32 m0, s85
	v_lshl_add_u64 v[8:9], v[8:9], 0, s[10:11]
	s_add_u32 s44, s44, 0x20080
	ds_read_b128 v[192:195], v187 offset:49152
	ds_read_b128 v[196:199], v187 offset:50176
	ds_read_b128 v[200:203], v187 offset:51200
	ds_read_b128 v[204:207], v187 offset:52224
	ds_read_b128 v[208:211], v187 offset:53248
	ds_read_b128 v[212:215], v187 offset:54272
	ds_read_b128 v[216:219], v187 offset:55296
	ds_read_b128 v[220:223], v187 offset:56320
	global_load_lds_dwordx4 v[8:9], off
	v_lshl_add_u64 v[8:9], v[10:11], 0, s[10:11]
	s_mov_b32 m0, s86
	s_addc_u32 s45, s45, 0
	global_load_lds_dwordx4 v[8:9], off
	v_lshl_add_u64 v[8:9], s[44:45], 0, v[164:165]
	s_mov_b32 m0, s87
	s_nop 0
	global_load_lds_dwordx4 v[8:9], off
	v_lshl_add_u64 v[8:9], s[44:45], 0, v[160:161]
	s_mov_b32 m0, s88
	s_nop 0
	global_load_lds_dwordx4 v[8:9], off
	v_lshl_add_u64 v[8:9], v[12:13], 0, s[10:11]
	s_mov_b32 m0, s54
	s_nop 0
	global_load_lds_dwordx4 v[8:9], off
	v_lshl_add_u64 v[8:9], v[14:15], 0, s[10:11]
	s_mov_b32 m0, s55
	s_nop 0
	global_load_lds_dwordx4 v[8:9], off
	s_waitcnt vmcnt(8)
	s_waitcnt lgkmcnt(0)
	s_barrier
	s_waitcnt lgkmcnt(0)
	v_mfma_f32_16x16x128_f8f6f4 v[92:95], v[16:23], v[192:199], v[92:95]
	v_mfma_f32_16x16x128_f8f6f4 v[88:91], v[24:31], v[192:199], v[88:91]
	v_mfma_f32_16x16x128_f8f6f4 v[84:87], v[16:23], v[200:207], v[84:87]
	v_mfma_f32_16x16x128_f8f6f4 v[80:83], v[24:31], v[200:207], v[80:83]
	v_mfma_f32_16x16x128_f8f6f4 v[76:79], v[16:23], v[208:215], v[76:79]
	v_mfma_f32_16x16x128_f8f6f4 v[72:75], v[24:31], v[208:215], v[72:75]
	v_mfma_f32_16x16x128_f8f6f4 v[68:71], v[16:23], v[216:223], v[68:71]
	v_mfma_f32_16x16x128_f8f6f4 v[64:67], v[24:31], v[216:223], v[64:67]
	v_mfma_f32_16x16x128_f8f6f4 v[60:63], v[0:7], v[192:199], v[60:63]
	v_mfma_f32_16x16x128_f8f6f4 v[56:59], v[176:183], v[192:199], v[56:59]
	v_mfma_f32_16x16x128_f8f6f4 v[52:55], v[0:7], v[200:207], v[52:55]
	v_mfma_f32_16x16x128_f8f6f4 v[48:51], v[176:183], v[200:207], v[48:51]
	v_mfma_f32_16x16x128_f8f6f4 v[44:47], v[0:7], v[208:215], v[44:47]
	v_mfma_f32_16x16x128_f8f6f4 v[40:43], v[176:183], v[208:215], v[40:43]
	v_mfma_f32_16x16x128_f8f6f4 v[36:39], v[0:7], v[216:223], v[36:39]
	v_mfma_f32_16x16x128_f8f6f4 v[32:35], v[176:183], v[216:223], v[32:35]
	s_barrier
	s_add_i32 s91, s91, 2
	s_add_u32 s46, s46, 0x100
	s_addc_u32 s47, s47, 0
	s_add_u32 s89, s89, 0x100
	s_addc_u32 s90, s90, 0
	s_cmp_gt_u32 s91, 5
	s_cbranch_scc0 .LBB0_867
	s_and_b64 vcc, exec, s[6:7]
	s_cbranch_vccz .LBB0_870
	s_barrier

; #define PG8_STAGE(bufoff, gbase, voff) do { _Pragma("unroll") for (int _i = 0; _i < 2; ++_i) \
;         __builtin_amdgcn_global_load_lds((const unsigned*)((const char*)(gbase) + (voff)[_i]), (PG8_LAS unsigned*)(lds + (bufoff) + ldsw + _i * 8192), 16, 0, 0); } while (0)
; #define PG8_WAIT_V(n) asm volatile("s_waitcnt vmcnt(" #n ")" ::: "memory")
; #define PG8_WAIT_L(n) asm volatile("s_waitcnt lgkmcnt(" #n ")" ::: "memory")
; #define PG8_BAR __builtin_amdgcn_s_barrier()
; #define PG8_SCHED __builtin_amdgcn_sched_barrier(0)
; template <class Epi, class Sched, bool ALIGN_EPI = false, bool SP2 = false, bool FP8 = false, bool PEEL = false>
; __device__ __forceinline__ void gemm_phase(PG8_LAS unsigned char* lds, const Gemm g, const Sched& S, const Epi& E, const int wid) {
;     ...
;         for (int t = 0; t < nt; t += 2) {
;             const bool last = (t == nt - 2);
;             const char* a1 = cA + (size_t)(t + 1) * kstep;
;             const char* a2 = last ? nA : cA + (size_t)(t + 2) * kstep; const char* b2 = last ? nB : cB + (size_t)(t + 2) * kstep;
;             const char* a3 = a2 + kstep; const char* b3 = b2 + kstep;
;             if (last && has_next) S.a_ready(nxt);
;             PG8_LDB(B0, 0, 0); PG8_LDB(B1, 0, 1); PG8_SCHED; PG8_LDA(At, 0, 0); PG8_STAGE(PG8_SA(1, 1), a1 + hstep, voffA);
;             PG8_WAIT_V(8); PG8_WAIT_L(0); PG8_BAR; PG8_MMA(0, 0, At, B0); PG8_MMA(0, 1, At, B1); PG8_BAR; PG8_SCHED;
;             PG8_LDA(At, 0, 1); PG8_STAGE(PG8_SB(0, 0), b2, voffB); PG8_STAGE(PG8_SB(0, 1), b2 + hstep, voffB); PG8_STAGE(PG8_SA(0, 0), a2, voffA);
;             PG8_WAIT_V(8); PG8_WAIT_L(0); PG8_BAR; PG8_MMA(1, 0, At, B0); PG8_MMA(1, 1, At, B1); PG8_BAR; PG8_SCHED;
.LBB0_976:
	v_add_u32_e32 v12, s50, v180
	v_add_u32_e32 v172, s51, v180
	s_add_u32 s26, s6, s24
	ds_read_b128 v[0:3], v12
	ds_read_b128 v[4:7], v12 offset:1024
	ds_read_b128 v[8:11], v12 offset:2048
	ds_read_b128 v[12:15], v12 offset:3072
	ds_read_b128 v[16:19], v172
	ds_read_b128 v[20:23], v172 offset:1024
	ds_read_b128 v[182:185], v172 offset:2048
	ds_read_b128 v[186:189], v172 offset:3072
	s_addc_u32 s27, s7, s25
	s_add_u32 s26, s26, 0x100
	s_addc_u32 s27, s27, 0
	s_add_u32 s59, s56, s24
	s_addc_u32 s60, s57, s25
	s_cmpk_eq_i32 s24, 0xd00
	s_cselect_b32 s31, s17, s27
	s_cselect_b32 s30, s16, s26
	s_cselect_b32 s27, s13, s60
	s_cselect_b32 s26, s12, s59
	v_lshl_add_u64 v[198:199], v[168:169], 0, s[24:25]
	s_add_i32 m0, s43, 0xc000
	ds_read_b128 v[172:175], v181
	ds_read_b128 v[176:179], v181 offset:1024
	ds_read_b128 v[190:193], v181 offset:2048
	ds_read_b128 v[194:197], v181 offset:3072
	ds_read_b128 v[206:209], v181 offset:4096
	ds_read_b128 v[210:213], v181 offset:5120
	ds_read_b128 v[214:217], v181 offset:6144
	ds_read_b128 v[218:221], v181 offset:7168
	global_load_lds_dwordx4 v[198:199], off
	v_lshl_add_u64 v[198:199], v[170:171], 0, s[24:25]
	s_add_i32 m0, s43, 0xe000
	s_nop 0
	global_load_lds_dwordx4 v[198:199], off
	s_waitcnt vmcnt(8)
	s_waitcnt lgkmcnt(0)
	s_barrier
	s_waitcnt lgkmcnt(0)
	v_mfma_f32_16x16x128_f8f6f4 v[148:151], v[0:7], v[172:179], v[148:151]
	v_mfma_f32_16x16x128_f8f6f4 v[144:147], v[8:15], v[172:179], v[144:147]
	v_mfma_f32_16x16x128_f8f6f4 v[136:139], v[0:7], v[190:197], v[136:139]
	v_mfma_f32_16x16x128_f8f6f4 v[128:131], v[8:15], v[190:197], v[128:131]
	v_mfma_f32_16x16x128_f8f6f4 v[120:123], v[0:7], v[206:213], v[120:123]
	v_mfma_f32_16x16x128_f8f6f4 v[112:115], v[8:15], v[206:213], v[112:115]
	v_mfma_f32_16x16x128_f8f6f4 v[104:107], v[0:7], v[214:221], v[104:107]
	v_mfma_f32_16x16x128_f8f6f4 v[96:99], v[8:15], v[214:221], v[96:99]
	v_mfma_f32_16x16x128_f8f6f4 v[140:143], v[16:23], v[172:179], v[140:143]
	v_mfma_f32_16x16x128_f8f6f4 v[132:135], v[182:189], v[172:179], v[132:135]
	v_mfma_f32_16x16x128_f8f6f4 v[124:127], v[16:23], v[190:197], v[124:127]
	v_mfma_f32_16x16x128_f8f6f4 v[116:119], v[182:189], v[190:197], v[116:119]
	v_mfma_f32_16x16x128_f8f6f4 v[108:111], v[16:23], v[206:213], v[108:111]
	v_mfma_f32_16x16x128_f8f6f4 v[100:103], v[182:189], v[206:213], v[100:103]
	v_mfma_f32_16x16x128_f8f6f4 v[92:95], v[16:23], v[214:221], v[92:95]
	v_mfma_f32_16x16x128_f8f6f4 v[88:91], v[182:189], v[214:221], v[88:91]
	s_barrier
	s_add_i32 s59, s50, s40
	v_lshl_add_u64 v[172:173], s[26:27], 0, v[156:157]
	s_mov_b32 m0, s59
	ds_read_b128 v[190:193], v181 offset:16384
	ds_read_b128 v[194:197], v181 offset:17408
	ds_read_b128 v[206:209], v181 offset:18432
	ds_read_b128 v[210:213], v181 offset:19456
	ds_read_b128 v[214:217], v181 offset:20480
	ds_read_b128 v[218:221], v181 offset:21504
	ds_read_b128 v[222:225], v181 offset:22528
	ds_read_b128 v[226:229], v181 offset:23552
	global_load_lds_dwordx4 v[172:173], off
	s_add_i32 m0, s59, 0x2000
	s_add_u32 s60, s26, 0x70000
	v_lshl_add_u64 v[174:175], s[26:27], 0, v[152:153]
	s_addc_u32 s61, s27, 0
	s_add_i32 s59, s51, s40
	global_load_lds_dwordx4 v[174:175], off
	v_lshl_add_u64 v[176:177], s[60:61], 0, v[156:157]
	s_mov_b32 m0, s59
	v_lshl_add_u64 v[178:179], s[30:31], 0, v[154:155]
	global_load_lds_dwordx4 v[176:177], off
	v_lshl_add_u64 v[176:177], s[60:61], 0, v[152:153]
	s_add_i32 m0, s59, 0x2000
	s_nop 0
	global_load_lds_dwordx4 v[176:177], off
	v_lshl_add_u64 v[176:177], s[30:31], 0, v[158:159]
	s_mov_b32 m0, s43
	s_nop 0
	global_load_lds_dwordx4 v[176:177], off
	s_mov_b32 m0, s44
	s_nop 0
	global_load_lds_dwordx4 v[178:179], off
	s_waitcnt vmcnt(8)
	s_waitcnt lgkmcnt(0)
	s_barrier
	s_waitcnt lgkmcnt(0)
	v_mfma_f32_16x16x128_f8f6f4 v[84:87], v[0:7], v[190:197], v[84:87]
	v_mfma_f32_16x16x128_f8f6f4 v[80:83], v[8:15], v[190:197], v[80:83]
	v_mfma_f32_16x16x128_f8f6f4 v[72:75], v[0:7], v[206:213], v[72:75]
	v_mfma_f32_16x16x128_f8f6f4 v[64:67], v[8:15], v[206:213], v[64:67]
	v_mfma_f32_16x16x128_f8f6f4 v[56:59], v[0:7], v[214:221], v[56:59]
	v_mfma_f32_16x16x128_f8f6f4 v[48:51], v[8:15], v[214:221], v[48:51]
	v_mfma_f32_16x16x128_f8f6f4 v[40:43], v[0:7], v[222:229], v[40:43]
	v_mfma_f32_16x16x128_f8f6f4 v[32:35], v[8:15], v[222:229], v[32:35]
	v_mfma_f32_16x16x128_f8f6f4 v[76:79], v[16:23], v[190:197], v[76:79]
	v_mfma_f32_16x16x128_f8f6f4 v[68:71], v[182:189], v[190:197], v[68:71]
	v_mfma_f32_16x16x128_f8f6f4 v[60:63], v[16:23], v[206:213], v[60:63]
	v_mfma_f32_16x16x128_f8f6f4 v[52:55], v[182:189], v[206:213], v[52:55]
	v_mfma_f32_16x16x128_f8f6f4 v[44:47], v[16:23], v[214:221], v[44:47]
	v_mfma_f32_16x16x128_f8f6f4 v[36:39], v[182:189], v[214:221], v[36:39]
	v_mfma_f32_16x16x128_f8f6f4 v[28:31], v[16:23], v[222:229], v[28:31]
	v_mfma_f32_16x16x128_f8f6f4 v[24:27], v[182:189], v[222:229], v[24:27]
	s_barrier
	s_add_i32 s59, 0, 0x18000
	s_add_i32 s60, 0, 0x1c000
	v_add_u32_e32 v0, s59, v180
	v_add_u32_e32 v20, s60, v180
	ds_read_b128 v[8:11], v0
	ds_read_b128 v[12:15], v0 offset:1024
	ds_read_b128 v[182:185], v0 offset:2048
	ds_read_b128 v[186:189], v0 offset:3072
	ds_read_b128 v[0:3], v20
	ds_read_b128 v[4:7], v20 offset:1024
	ds_read_b128 v[16:19], v20 offset:2048
	ds_read_b128 v[20:23], v20 offset:3072
	s_add_u32 s30, s30, 0x70000
	s_addc_u32 s31, s31, 0
	s_mov_b32 m0, s45
	v_lshl_add_u64 v[198:199], s[30:31], 0, v[158:159]
	ds_read_b128 v[190:193], v181 offset:32768
	ds_read_b128 v[194:197], v181 offset:33792
	ds_read_b128 v[206:209], v181 offset:34816
	ds_read_b128 v[210:213], v181 offset:35840
	ds_read_b128 v[214:217], v181 offset:36864
	ds_read_b128 v[218:221], v181 offset:37888
	ds_read_b128 v[222:225], v181 offset:38912
	ds_read_b128 v[226:229], v181 offset:39936
	global_load_lds_dwordx4 v[198:199], off
	v_lshl_add_u64 v[198:199], s[30:31], 0, v[154:155]
	s_mov_b32 m0, s46
	s_nop 0
	global_load_lds_dwordx4 v[198:199], off
	s_waitcnt vmcnt(8)
	s_waitcnt lgkmcnt(0)
	s_barrier
; #define PG8_STAGE(bufoff, gbase, voff) do { _Pragma("unroll") for (int _i = 0; _i < 2; ++_i) \
;         __builtin_amdgcn_global_load_lds((const unsigned*)((const char*)(gbase) + (voff)[_i]), (PG8_LAS unsigned*)(lds + (bufoff) + ldsw + _i * 8192), 16, 0, 0); } while (0)
; #define PG8_WAIT_V(n) asm volatile("s_waitcnt vmcnt(" #n ")" ::: "memory")
; #define PG8_WAIT_L(n) asm volatile("s_waitcnt lgkmcnt(" #n ")" ::: "memory")
; #define PG8_BAR __builtin_amdgcn_s_barrier()
; #define PG8_SCHED __builtin_amdgcn_sched_barrier(0)
; template <class Epi, class Sched, bool ALIGN_EPI = false, bool SP2 = false, bool FP8 = false, bool PEEL = false>
; __device__ __forceinline__ void gemm_phase(PG8_LAS unsigned char* lds, const Gemm g, const Sched& S, const Epi& E, const int wid) {
;     ...
;             PG8_LDB(B0, 1, 0); PG8_LDB(B1, 1, 1); PG8_SCHED; PG8_LDA(At, 1, 0); PG8_STAGE(PG8_SA(0, 1), a2 + hstep, voffA);
;             PG8_WAIT_V(8); PG8_WAIT_L(0); PG8_BAR; PG8_MMA(0, 0, At, B0); PG8_MMA(0, 1, At, B1); PG8_BAR; PG8_SCHED;
;             PG8_LDA(At, 1, 1); PG8_STAGE(PG8_SB(1, 0), b3, voffB); PG8_STAGE(PG8_SB(1, 1), b3 + hstep, voffB); PG8_STAGE(PG8_SA(1, 0), a3, voffA);
;             PG8_WAIT_V(8); PG8_WAIT_L(0); PG8_BAR; PG8_MMA(1, 0, At, B0); PG8_MMA(1, 1, At, B1); PG8_BAR; PG8_SCHED;
	s_waitcnt lgkmcnt(0)
	v_mfma_f32_16x16x128_f8f6f4 v[148:151], v[8:15], v[190:197], v[148:151]
	v_mfma_f32_16x16x128_f8f6f4 v[144:147], v[182:189], v[190:197], v[144:147]
	v_mfma_f32_16x16x128_f8f6f4 v[136:139], v[8:15], v[206:213], v[136:139]
	v_mfma_f32_16x16x128_f8f6f4 v[128:131], v[182:189], v[206:213], v[128:131]
	v_mfma_f32_16x16x128_f8f6f4 v[120:123], v[8:15], v[214:221], v[120:123]
	v_mfma_f32_16x16x128_f8f6f4 v[112:115], v[182:189], v[214:221], v[112:115]
	v_mfma_f32_16x16x128_f8f6f4 v[104:107], v[8:15], v[222:229], v[104:107]
	v_mfma_f32_16x16x128_f8f6f4 v[96:99], v[182:189], v[222:229], v[96:99]
	v_mfma_f32_16x16x128_f8f6f4 v[140:143], v[0:7], v[190:197], v[140:143]
	v_mfma_f32_16x16x128_f8f6f4 v[132:135], v[16:23], v[190:197], v[132:135]
	v_mfma_f32_16x16x128_f8f6f4 v[124:127], v[0:7], v[206:213], v[124:127]
	v_mfma_f32_16x16x128_f8f6f4 v[116:119], v[16:23], v[206:213], v[116:119]
	v_mfma_f32_16x16x128_f8f6f4 v[108:111], v[0:7], v[214:221], v[108:111]
	v_mfma_f32_16x16x128_f8f6f4 v[100:103], v[16:23], v[214:221], v[100:103]
	v_mfma_f32_16x16x128_f8f6f4 v[92:95], v[0:7], v[222:229], v[92:95]
	v_mfma_f32_16x16x128_f8f6f4 v[88:91], v[16:23], v[222:229], v[88:91]
	s_barrier
	s_add_i32 s30, s59, s40
	v_lshl_add_u64 v[172:173], v[172:173], 0, s[14:15]
	s_mov_b32 m0, s30
	ds_read_b128 v[190:193], v181 offset:49152
	ds_read_b128 v[194:197], v181 offset:50176
	ds_read_b128 v[206:209], v181 offset:51200
	ds_read_b128 v[210:213], v181 offset:52224
	ds_read_b128 v[214:217], v181 offset:53248
	ds_read_b128 v[218:221], v181 offset:54272
	ds_read_b128 v[222:225], v181 offset:55296
	ds_read_b128 v[226:229], v181 offset:56320
	global_load_lds_dwordx4 v[172:173], off
	s_add_i32 m0, s30, 0x2000
	s_add_u32 s26, s26, 0x70080
	v_lshl_add_u64 v[172:173], v[174:175], 0, s[14:15]
	s_addc_u32 s27, s27, 0
	s_add_i32 s30, s60, s40
	global_load_lds_dwordx4 v[172:173], off
	v_lshl_add_u64 v[172:173], s[26:27], 0, v[156:157]
	s_mov_b32 m0, s30
	s_nop 0
	global_load_lds_dwordx4 v[172:173], off
	v_lshl_add_u64 v[172:173], s[26:27], 0, v[152:153]
	s_add_i32 m0, s30, 0x2000
	s_nop 0
	global_load_lds_dwordx4 v[172:173], off
	v_lshl_add_u64 v[172:173], v[176:177], 0, s[14:15]
	s_mov_b32 m0, s47
	s_nop 0
	global_load_lds_dwordx4 v[172:173], off
	v_lshl_add_u64 v[172:173], v[178:179], 0, s[14:15]
	s_mov_b32 m0, s48
	s_nop 0
	global_load_lds_dwordx4 v[172:173], off
	s_waitcnt vmcnt(8)
	s_waitcnt lgkmcnt(0)
	s_barrier
	s_waitcnt lgkmcnt(0)
	v_mfma_f32_16x16x128_f8f6f4 v[84:87], v[8:15], v[190:197], v[84:87]
	v_mfma_f32_16x16x128_f8f6f4 v[80:83], v[182:189], v[190:197], v[80:83]
	v_mfma_f32_16x16x128_f8f6f4 v[72:75], v[8:15], v[206:213], v[72:75]
	v_mfma_f32_16x16x128_f8f6f4 v[64:67], v[182:189], v[206:213], v[64:67]
	v_mfma_f32_16x16x128_f8f6f4 v[56:59], v[8:15], v[214:221], v[56:59]
	v_mfma_f32_16x16x128_f8f6f4 v[48:51], v[182:189], v[214:221], v[48:51]
	v_mfma_f32_16x16x128_f8f6f4 v[40:43], v[8:15], v[222:229], v[40:43]
	v_mfma_f32_16x16x128_f8f6f4 v[32:35], v[182:189], v[222:229], v[32:35]
	v_mfma_f32_16x16x128_f8f6f4 v[76:79], v[0:7], v[190:197], v[76:79]
	v_mfma_f32_16x16x128_f8f6f4 v[68:71], v[16:23], v[190:197], v[68:71]
	v_mfma_f32_16x16x128_f8f6f4 v[60:63], v[0:7], v[206:213], v[60:63]
	v_mfma_f32_16x16x128_f8f6f4 v[52:55], v[16:23], v[206:213], v[52:55]
	v_mfma_f32_16x16x128_f8f6f4 v[44:47], v[0:7], v[214:221], v[44:47]
	v_mfma_f32_16x16x128_f8f6f4 v[36:39], v[16:23], v[214:221], v[36:39]
	v_mfma_f32_16x16x128_f8f6f4 v[28:31], v[0:7], v[222:229], v[28:31]
	v_mfma_f32_16x16x128_f8f6f4 v[24:27], v[16:23], v[222:229], v[24:27]
	s_barrier
; template <class Epi, class Sched, bool ALIGN_EPI = false, bool SP2 = false, bool FP8 = false, bool PEEL = false>
; __device__ __forceinline__ void gemm_phase(PG8_LAS unsigned char* lds, const Gemm g, const Sched& S, const Epi& E, const int wid) {
;     ...
;         if constexpr (FP8) asm volatile("s_nop 15\n\ts_nop 15" ::: "memory");
;         if constexpr (!Epi::AFTER_DRAIN) { E(acc, cur, wr, wc, fr, fq); S.done(cur); }
;         if (!has_next) break;
;         if constexpr (!PEEL) {
; #pragma unroll
;         for (int a = 0; a < 2; ++a)
; #pragma unroll
;             for (int b = 0; b < 2; ++b)
; #pragma unroll
;                 for (int m = 0; m < 4; ++m)
; #pragma unroll
;                     for (int n = 0; n < 2; ++n) acc[a][b][m][n] = (f32x4){0.f, 0.f, 0.f, 0.f};
;         }
;         cur = nxt; cA = nA; cB = nB; ++ui;
	s_add_i32 s58, s58, 2
	s_add_u32 s24, s24, 0x100
	s_addc_u32 s25, s25, 0
	s_cmp_gt_u32 s58, 25
	s_cbranch_scc0 .LBB0_976
	s_nop 15
	s_nop 15
	s_add_u32 s24, s56, 0xffffff00
	s_addc_u32 s25, s57, -1
	s_and_b64 vcc, exec, s[10:11]
	s_cbranch_vccnz .LBB0_979
	v_mov_b32_e32 v24, 0
	s_mov_b32 s4, s52
	s_mov_b32 s3, s53
	s_mov_b64 s[6:7], s[16:17]
	s_mov_b32 s49, s55
	v_mov_b32_e32 v25, v24
	v_mov_b32_e32 v26, v24
	v_mov_b32_e32 v27, v24
	v_mov_b32_e32 v28, v24
	v_mov_b32_e32 v29, v24
	v_mov_b32_e32 v30, v24
	v_mov_b32_e32 v31, v24
	v_mov_b32_e32 v36, v24
	v_mov_b32_e32 v37, v24
	v_mov_b32_e32 v38, v24
	v_mov_b32_e32 v39, v24
	v_mov_b32_e32 v44, v24
	v_mov_b32_e32 v45, v24
	v_mov_b32_e32 v46, v24
	v_mov_b32_e32 v47, v24
	v_mov_b32_e32 v52, v24
	v_mov_b32_e32 v53, v24
	v_mov_b32_e32 v54, v24
	v_mov_b32_e32 v55, v24
	v_mov_b32_e32 v60, v24
	v_mov_b32_e32 v61, v24
	v_mov_b32_e32 v62, v24
	v_mov_b32_e32 v63, v24
	v_mov_b32_e32 v68, v24
	v_mov_b32_e32 v69, v24
	v_mov_b32_e32 v70, v24
	v_mov_b32_e32 v71, v24
	v_mov_b32_e32 v76, v24
	v_mov_b32_e32 v77, v24
	v_mov_b32_e32 v78, v24
	v_mov_b32_e32 v79, v24
	v_mov_b32_e32 v32, v24
	v_mov_b32_e32 v33, v24
	v_mov_b32_e32 v34, v24
	v_mov_b32_e32 v35, v24
	v_mov_b32_e32 v40, v24
	v_mov_b32_e32 v41, v24
	v_mov_b32_e32 v42, v24
	v_mov_b32_e32 v43, v24
	v_mov_b32_e32 v48, v24
	v_mov_b32_e32 v49, v24
	v_mov_b32_e32 v50, v24
	v_mov_b32_e32 v51, v24
	v_mov_b32_e32 v56, v24
	v_mov_b32_e32 v57, v24
	v_mov_b32_e32 v58, v24
	v_mov_b32_e32 v59, v24
	v_mov_b32_e32 v64, v24
	v_mov_b32_e32 v65, v24
	v_mov_b32_e32 v66, v24
	v_mov_b32_e32 v67, v24
	v_mov_b32_e32 v72, v24
	v_mov_b32_e32 v73, v24
	v_mov_b32_e32 v74, v24
	v_mov_b32_e32 v75, v24
	v_mov_b32_e32 v80, v24
	v_mov_b32_e32 v81, v24
	v_mov_b32_e32 v82, v24
	v_mov_b32_e32 v83, v24
	v_mov_b32_e32 v84, v24
	v_mov_b32_e32 v85, v24
	v_mov_b32_e32 v86, v24
	v_mov_b32_e32 v87, v24
	v_mov_b32_e32 v88, v24
	v_mov_b32_e32 v89, v24
	v_mov_b32_e32 v90, v24
	v_mov_b32_e32 v91, v24
	v_mov_b32_e32 v92, v24
	v_mov_b32_e32 v93, v24
	v_mov_b32_e32 v94, v24
	v_mov_b32_e32 v95, v24
	v_mov_b32_e32 v100, v24
	v_mov_b32_e32 v101, v24
	v_mov_b32_e32 v102, v24
	v_mov_b32_e32 v103, v24
	v_mov_b32_e32 v108, v24
	v_mov_b32_e32 v109, v24
	v_mov_b32_e32 v110, v24
	v_mov_b32_e32 v111, v24
	v_mov_b32_e32 v116, v24
	v_mov_b32_e32 v117, v24
	v_mov_b32_e32 v118, v24
	v_mov_b32_e32 v119, v24
	v_mov_b32_e32 v124, v24
	v_mov_b32_e32 v125, v24
	v_mov_b32_e32 v126, v24
	v_mov_b32_e32 v127, v24
	v_mov_b32_e32 v132, v24
	v_mov_b32_e32 v133, v24
	v_mov_b32_e32 v134, v24
	v_mov_b32_e32 v135, v24
	v_mov_b32_e32 v140, v24
	v_mov_b32_e32 v141, v24
	v_mov_b32_e32 v142, v24
	v_mov_b32_e32 v143, v24
	v_mov_b32_e32 v96, v24
	v_mov_b32_e32 v97, v24
	v_mov_b32_e32 v98, v24
	v_mov_b32_e32 v99, v24
	v_mov_b32_e32 v104, v24
	v_mov_b32_e32 v105, v24
	v_mov_b32_e32 v106, v24
	v_mov_b32_e32 v107, v24
	v_mov_b32_e32 v112, v24
	v_mov_b32_e32 v113, v24
	v_mov_b32_e32 v114, v24
	v_mov_b32_e32 v115, v24
	v_mov_b32_e32 v120, v24
	v_mov_b32_e32 v121, v24
	v_mov_b32_e32 v122, v24
	v_mov_b32_e32 v123, v24
	v_mov_b32_e32 v128, v24
	v_mov_b32_e32 v129, v24
	v_mov_b32_e32 v130, v24
	v_mov_b32_e32 v131, v24
	v_mov_b32_e32 v136, v24
	v_mov_b32_e32 v137, v24
	v_mov_b32_e32 v138, v24
	v_mov_b32_e32 v139, v24
	v_mov_b32_e32 v144, v24
	v_mov_b32_e32 v145, v24
	v_mov_b32_e32 v146, v24
	v_mov_b32_e32 v147, v24
	v_mov_b32_e32 v148, v24
	v_mov_b32_e32 v149, v24
	v_mov_b32_e32 v150, v24
	v_mov_b32_e32 v151, v24
	s_andn2_b64 vcc, exec, s[8:9]
	s_cbranch_vccnz .LBB0_980
	s_branch .LBB0_981

; #define PG8_STAGE(bufoff, gbase, voff) do { _Pragma("unroll") for (int _i = 0; _i < 2; ++_i) \
;         __builtin_amdgcn_global_load_lds((const unsigned*)((const char*)(gbase) + (voff)[_i]), (PG8_LAS unsigned*)(lds + (bufoff) + ldsw + _i * 8192), 16, 0, 0); } while (0)
; #define PG8_WAIT_V(n) asm volatile("s_waitcnt vmcnt(" #n ")" ::: "memory")
; #define PG8_WAIT_L(n) asm volatile("s_waitcnt lgkmcnt(" #n ")" ::: "memory")
; #define PG8_BAR __builtin_amdgcn_s_barrier()
; #define PG8_SCHED __builtin_amdgcn_sched_barrier(0)
; template <class Epi, class Sched, bool ALIGN_EPI = false, bool SP2 = false, bool FP8 = false, bool PEEL = false>
; __device__ __forceinline__ void gemm_phase(PG8_LAS unsigned char* lds, const Gemm g, const Sched& S, const Epi& E, const int wid) {
;     ...
;         for (int t = 0; t < nt; t += 2) {
;             const bool last = (t == nt - 2);
;             const char* a1 = cA + (size_t)(t + 1) * kstep;
;             const char* a2 = last ? nA : cA + (size_t)(t + 2) * kstep; const char* b2 = last ? nB : cB + (size_t)(t + 2) * kstep;
;             const char* a3 = a2 + kstep; const char* b3 = b2 + kstep;
;             if (last && has_next) S.a_ready(nxt);
;             PG8_LDB(B0, 0, 0); PG8_LDB(B1, 0, 1); PG8_SCHED; PG8_LDA(At, 0, 0); PG8_STAGE(PG8_SA(1, 1), a1 + hstep, voffA);
;             PG8_WAIT_V(8); PG8_WAIT_L(0); PG8_BAR; PG8_MMA(0, 0, At, B0); PG8_MMA(0, 1, At, B1); PG8_BAR; PG8_SCHED;
;             PG8_LDA(At, 0, 1); PG8_STAGE(PG8_SB(0, 0), b2, voffB); PG8_STAGE(PG8_SB(0, 1), b2 + hstep, voffB); PG8_STAGE(PG8_SA(0, 0), a2, voffA);
;             PG8_WAIT_V(8); PG8_WAIT_L(0); PG8_BAR; PG8_MMA(1, 0, At, B0); PG8_MMA(1, 1, At, B1); PG8_BAR; PG8_SCHED;
;             PG8_LDB(B0, 1, 0); PG8_LDB(B1, 1, 1); PG8_SCHED; PG8_LDA(At, 1, 0); PG8_STAGE(PG8_SA(0, 1), a2 + hstep, voffA);
;             PG8_WAIT_V(8); PG8_WAIT_L(0); PG8_BAR; PG8_MMA(0, 0, At, B0); PG8_MMA(0, 1, At, B1); PG8_BAR; PG8_SCHED;
;             PG8_LDA(At, 1, 1); PG8_STAGE(PG8_SB(1, 0), b3, voffB); PG8_STAGE(PG8_SB(1, 1), b3 + hstep, voffB); PG8_STAGE(PG8_SA(1, 0), a3, voffA);
;             PG8_WAIT_V(8); PG8_WAIT_L(0); PG8_BAR; PG8_MMA(1, 0, At, B0); PG8_MMA(1, 1, At, B1); PG8_BAR; PG8_SCHED;
;         }
.LBB0_1120:
	ds_read_b128 v[146:149], v152
	ds_read_b128 v[156:159], v152 offset:1024
	ds_read_b128 v[160:163], v152 offset:2048
	ds_read_b128 v[164:167], v152 offset:3072
	ds_read_b128 v[168:171], v153
	ds_read_b128 v[172:175], v153 offset:1024
	ds_read_b128 v[176:179], v153 offset:2048
	ds_read_b128 v[180:183], v153 offset:3072
	s_add_u32 s44, s36, 0xfffc0080
	s_addc_u32 s45, s37, -1
	s_cmp_eq_u32 s61, 12
	s_cselect_b32 s47, s10, s45
	s_cselect_b32 s46, s25, s44
	s_cselect_b32 s45, s17, s60
	s_cselect_b32 s44, s58, s59
	v_lshl_add_u64 v[216:217], s[36:37], 0, v[136:137]
	s_add_i32 m0, s41, 0xc000
	ds_read_b128 v[184:187], v154
	ds_read_b128 v[188:191], v154 offset:1024
	ds_read_b128 v[192:195], v154 offset:2048
	ds_read_b128 v[196:199], v154 offset:3072
	ds_read_b128 v[200:203], v154 offset:4096
	ds_read_b128 v[204:207], v154 offset:5120
	ds_read_b128 v[208:211], v154 offset:6144
	ds_read_b128 v[212:215], v154 offset:7168
	global_load_lds_dwordx4 v[216:217], off
	v_lshl_add_u64 v[216:217], s[36:37], 0, v[138:139]
	s_add_i32 m0, s41, 0xe000
	s_nop 0
	global_load_lds_dwordx4 v[216:217], off
	s_waitcnt vmcnt(8)
	s_waitcnt lgkmcnt(0)
	s_barrier
	s_waitcnt lgkmcnt(0)
	v_mfma_f32_16x16x32_bf16 v[124:127], v[146:149], v[184:187], v[124:127]
	v_mfma_f32_16x16x32_bf16 v[120:123], v[160:163], v[184:187], v[120:123]
	v_mfma_f32_16x16x32_bf16 v[112:115], v[146:149], v[192:195], v[112:115]
	v_mfma_f32_16x16x32_bf16 v[104:107], v[160:163], v[192:195], v[104:107]
	v_mfma_f32_16x16x32_bf16 v[96:99], v[146:149], v[200:203], v[96:99]
	v_mfma_f32_16x16x32_bf16 v[88:91], v[160:163], v[200:203], v[88:91]
	v_mfma_f32_16x16x32_bf16 v[80:83], v[146:149], v[208:211], v[80:83]
	v_mfma_f32_16x16x32_bf16 v[72:75], v[160:163], v[208:211], v[72:75]
	v_mfma_f32_16x16x32_bf16 v[124:127], v[156:159], v[188:191], v[124:127]
	v_mfma_f32_16x16x32_bf16 v[120:123], v[164:167], v[188:191], v[120:123]
	v_mfma_f32_16x16x32_bf16 v[112:115], v[156:159], v[196:199], v[112:115]
	v_mfma_f32_16x16x32_bf16 v[104:107], v[164:167], v[196:199], v[104:107]
	v_mfma_f32_16x16x32_bf16 v[96:99], v[156:159], v[204:207], v[96:99]
	v_mfma_f32_16x16x32_bf16 v[88:91], v[164:167], v[204:207], v[88:91]
	v_mfma_f32_16x16x32_bf16 v[80:83], v[156:159], v[212:215], v[80:83]
	v_mfma_f32_16x16x32_bf16 v[72:75], v[164:167], v[212:215], v[72:75]
	v_mfma_f32_16x16x32_bf16 v[116:119], v[168:171], v[184:187], v[116:119]
	v_mfma_f32_16x16x32_bf16 v[108:111], v[176:179], v[184:187], v[108:111]
	v_mfma_f32_16x16x32_bf16 v[100:103], v[168:171], v[192:195], v[100:103]
	v_mfma_f32_16x16x32_bf16 v[92:95], v[176:179], v[192:195], v[92:95]
	v_mfma_f32_16x16x32_bf16 v[84:87], v[168:171], v[200:203], v[84:87]
	v_mfma_f32_16x16x32_bf16 v[76:79], v[176:179], v[200:203], v[76:79]
	v_mfma_f32_16x16x32_bf16 v[68:71], v[168:171], v[208:211], v[68:71]
	v_mfma_f32_16x16x32_bf16 v[64:67], v[176:179], v[208:211], v[64:67]
	v_mfma_f32_16x16x32_bf16 v[116:119], v[172:175], v[188:191], v[116:119]
	v_mfma_f32_16x16x32_bf16 v[108:111], v[180:183], v[188:191], v[108:111]
	v_mfma_f32_16x16x32_bf16 v[100:103], v[172:175], v[196:199], v[100:103]
	v_mfma_f32_16x16x32_bf16 v[92:95], v[180:183], v[196:199], v[92:95]
	v_mfma_f32_16x16x32_bf16 v[84:87], v[172:175], v[204:207], v[84:87]
	v_mfma_f32_16x16x32_bf16 v[76:79], v[180:183], v[204:207], v[76:79]
	v_mfma_f32_16x16x32_bf16 v[68:71], v[172:175], v[212:215], v[68:71]
	v_mfma_f32_16x16x32_bf16 v[64:67], v[180:183], v[212:215], v[64:67]
	s_barrier
	s_add_i32 s62, s52, s3
	v_lshl_add_u64 v[216:217], s[44:45], 0, v[132:133]
	s_mov_b32 m0, s62
	ds_read_b128 v[184:187], v154 offset:16384
	ds_read_b128 v[188:191], v154 offset:17408
	ds_read_b128 v[192:195], v154 offset:18432
	ds_read_b128 v[196:199], v154 offset:19456
	ds_read_b128 v[200:203], v154 offset:20480
	ds_read_b128 v[204:207], v154 offset:21504
	ds_read_b128 v[208:211], v154 offset:22528
	ds_read_b128 v[212:215], v154 offset:23552
	global_load_lds_dwordx4 v[216:217], off
	s_add_i32 m0, s62, 0x2000
	s_add_u32 s62, s44, 0x40000
	v_lshl_add_u64 v[218:219], s[44:45], 0, v[128:129]
	s_addc_u32 s63, s45, 0
	s_add_i32 s64, s53, s3
	global_load_lds_dwordx4 v[218:219], off
	v_lshl_add_u64 v[220:221], s[62:63], 0, v[132:133]
	s_mov_b32 m0, s64
	v_lshl_add_u64 v[222:223], s[46:47], 0, v[130:131]
	global_load_lds_dwordx4 v[220:221], off
	v_lshl_add_u64 v[220:221], s[62:63], 0, v[128:129]
	s_add_i32 m0, s64, 0x2000
	s_nop 0
	global_load_lds_dwordx4 v[220:221], off
	v_lshl_add_u64 v[220:221], s[46:47], 0, v[134:135]
	s_mov_b32 m0, s41
	s_nop 0
	global_load_lds_dwordx4 v[220:221], off
	s_mov_b32 m0, s42
	s_nop 0
	global_load_lds_dwordx4 v[222:223], off
	s_waitcnt vmcnt(8)
	s_waitcnt lgkmcnt(0)
	s_barrier
; #define PG8_STAGE(bufoff, gbase, voff) do { _Pragma("unroll") for (int _i = 0; _i < 2; ++_i) \
;         __builtin_amdgcn_global_load_lds((const unsigned*)((const char*)(gbase) + (voff)[_i]), (PG8_LAS unsigned*)(lds + (bufoff) + ldsw + _i * 8192), 16, 0, 0); } while (0)
; #define PG8_WAIT_V(n) asm volatile("s_waitcnt vmcnt(" #n ")" ::: "memory")
; #define PG8_WAIT_L(n) asm volatile("s_waitcnt lgkmcnt(" #n ")" ::: "memory")
; #define PG8_BAR __builtin_amdgcn_s_barrier()
; #define PG8_SCHED __builtin_amdgcn_sched_barrier(0)
; template <class Epi, class Sched, bool ALIGN_EPI = false, bool SP2 = false, bool FP8 = false, bool PEEL = false>
; __device__ __forceinline__ void gemm_phase(PG8_LAS unsigned char* lds, const Gemm g, const Sched& S, const Epi& E, const int wid) {
;     ...
;         for (int t = 0; t < nt; t += 2) {
;             const bool last = (t == nt - 2);
;             const char* a1 = cA + (size_t)(t + 1) * kstep;
;             const char* a2 = last ? nA : cA + (size_t)(t + 2) * kstep; const char* b2 = last ? nB : cB + (size_t)(t + 2) * kstep;
;             const char* a3 = a2 + kstep; const char* b3 = b2 + kstep;
;             if (last && has_next) S.a_ready(nxt);
;             PG8_LDB(B0, 0, 0); PG8_LDB(B1, 0, 1); PG8_SCHED; PG8_LDA(At, 0, 0); PG8_STAGE(PG8_SA(1, 1), a1 + hstep, voffA);
;             PG8_WAIT_V(8); PG8_WAIT_L(0); PG8_BAR; PG8_MMA(0, 0, At, B0); PG8_MMA(0, 1, At, B1); PG8_BAR; PG8_SCHED;
;             PG8_LDA(At, 0, 1); PG8_STAGE(PG8_SB(0, 0), b2, voffB); PG8_STAGE(PG8_SB(0, 1), b2 + hstep, voffB); PG8_STAGE(PG8_SA(0, 0), a2, voffA);
;             PG8_WAIT_V(8); PG8_WAIT_L(0); PG8_BAR; PG8_MMA(1, 0, At, B0); PG8_MMA(1, 1, At, B1); PG8_BAR; PG8_SCHED;
;             PG8_LDB(B0, 1, 0); PG8_LDB(B1, 1, 1); PG8_SCHED; PG8_LDA(At, 1, 0); PG8_STAGE(PG8_SA(0, 1), a2 + hstep, voffA);
;             PG8_WAIT_V(8); PG8_WAIT_L(0); PG8_BAR; PG8_MMA(0, 0, At, B0); PG8_MMA(0, 1, At, B1); PG8_BAR; PG8_SCHED;
;             PG8_LDA(At, 1, 1); PG8_STAGE(PG8_SB(1, 0), b3, voffB); PG8_STAGE(PG8_SB(1, 1), b3 + hstep, voffB); PG8_STAGE(PG8_SA(1, 0), a3, voffA);
;             PG8_WAIT_V(8); PG8_WAIT_L(0); PG8_BAR; PG8_MMA(1, 0, At, B0); PG8_MMA(1, 1, At, B1); PG8_BAR; PG8_SCHED;
;         }
	s_waitcnt lgkmcnt(0)
	v_mfma_f32_16x16x32_bf16 v[60:63], v[146:149], v[184:187], v[60:63]
	v_mfma_f32_16x16x32_bf16 v[56:59], v[160:163], v[184:187], v[56:59]
	v_mfma_f32_16x16x32_bf16 v[48:51], v[146:149], v[192:195], v[48:51]
	v_mfma_f32_16x16x32_bf16 v[40:43], v[160:163], v[192:195], v[40:43]
	v_mfma_f32_16x16x32_bf16 v[32:35], v[146:149], v[200:203], v[32:35]
	v_mfma_f32_16x16x32_bf16 v[24:27], v[160:163], v[200:203], v[24:27]
	v_mfma_f32_16x16x32_bf16 v[16:19], v[146:149], v[208:211], v[16:19]
	v_mfma_f32_16x16x32_bf16 v[8:11], v[160:163], v[208:211], v[8:11]
	v_mfma_f32_16x16x32_bf16 v[60:63], v[156:159], v[188:191], v[60:63]
	v_mfma_f32_16x16x32_bf16 v[56:59], v[164:167], v[188:191], v[56:59]
	v_mfma_f32_16x16x32_bf16 v[48:51], v[156:159], v[196:199], v[48:51]
	v_mfma_f32_16x16x32_bf16 v[40:43], v[164:167], v[196:199], v[40:43]
	v_mfma_f32_16x16x32_bf16 v[32:35], v[156:159], v[204:207], v[32:35]
	v_mfma_f32_16x16x32_bf16 v[24:27], v[164:167], v[204:207], v[24:27]
	v_mfma_f32_16x16x32_bf16 v[16:19], v[156:159], v[212:215], v[16:19]
	v_mfma_f32_16x16x32_bf16 v[8:11], v[164:167], v[212:215], v[8:11]
	v_mfma_f32_16x16x32_bf16 v[52:55], v[168:171], v[184:187], v[52:55]
	v_mfma_f32_16x16x32_bf16 v[44:47], v[176:179], v[184:187], v[44:47]
	v_mfma_f32_16x16x32_bf16 v[36:39], v[168:171], v[192:195], v[36:39]
	v_mfma_f32_16x16x32_bf16 v[28:31], v[176:179], v[192:195], v[28:31]
	v_mfma_f32_16x16x32_bf16 v[20:23], v[168:171], v[200:203], v[20:23]
	v_mfma_f32_16x16x32_bf16 v[12:15], v[176:179], v[200:203], v[12:15]
	v_mfma_f32_16x16x32_bf16 v[4:7], v[168:171], v[208:211], v[4:7]
	v_mfma_f32_16x16x32_bf16 v[0:3], v[176:179], v[208:211], v[0:3]
	v_mfma_f32_16x16x32_bf16 v[52:55], v[172:175], v[188:191], v[52:55]
	v_mfma_f32_16x16x32_bf16 v[44:47], v[180:183], v[188:191], v[44:47]
	v_mfma_f32_16x16x32_bf16 v[36:39], v[172:175], v[196:199], v[36:39]
	v_mfma_f32_16x16x32_bf16 v[28:31], v[180:183], v[196:199], v[28:31]
	v_mfma_f32_16x16x32_bf16 v[20:23], v[172:175], v[204:207], v[20:23]
	v_mfma_f32_16x16x32_bf16 v[12:15], v[180:183], v[204:207], v[12:15]
	v_mfma_f32_16x16x32_bf16 v[4:7], v[172:175], v[212:215], v[4:7]
	v_mfma_f32_16x16x32_bf16 v[0:3], v[180:183], v[212:215], v[0:3]
	s_barrier
	s_add_i32 s62, 0, 0x18000
	v_add_u32_e32 v144, s62, v150
	s_add_i32 s63, 0, 0x1c000
	ds_read_b128 v[146:149], v144
	ds_read_b128 v[156:159], v144 offset:1024
	ds_read_b128 v[160:163], v144 offset:2048
	ds_read_b128 v[164:167], v144 offset:3072
	v_add_u32_e32 v144, s63, v150
	ds_read_b128 v[168:171], v144
	ds_read_b128 v[172:175], v144 offset:1024
	ds_read_b128 v[176:179], v144 offset:2048
	ds_read_b128 v[180:183], v144 offset:3072
	s_add_u32 s46, s46, 0x40000
	s_addc_u32 s47, s47, 0
	s_mov_b32 m0, s43
	v_lshl_add_u64 v[224:225], s[46:47], 0, v[134:135]
	ds_read_b128 v[184:187], v154 offset:32768
	ds_read_b128 v[188:191], v154 offset:33792
	ds_read_b128 v[192:195], v154 offset:34816
	ds_read_b128 v[196:199], v154 offset:35840
	ds_read_b128 v[200:203], v154 offset:36864
	ds_read_b128 v[204:207], v154 offset:37888
	ds_read_b128 v[208:211], v154 offset:38912
	ds_read_b128 v[212:215], v154 offset:39936
	global_load_lds_dwordx4 v[224:225], off
	v_lshl_add_u64 v[224:225], s[46:47], 0, v[130:131]
	s_mov_b32 m0, s48
	s_nop 0
	global_load_lds_dwordx4 v[224:225], off
	s_waitcnt vmcnt(8)
	s_waitcnt lgkmcnt(0)
	s_barrier
	s_waitcnt lgkmcnt(0)
	v_mfma_f32_16x16x32_bf16 v[124:127], v[146:149], v[184:187], v[124:127]
	v_mfma_f32_16x16x32_bf16 v[120:123], v[160:163], v[184:187], v[120:123]
	v_mfma_f32_16x16x32_bf16 v[112:115], v[146:149], v[192:195], v[112:115]
	v_mfma_f32_16x16x32_bf16 v[104:107], v[160:163], v[192:195], v[104:107]
	v_mfma_f32_16x16x32_bf16 v[96:99], v[146:149], v[200:203], v[96:99]
	v_mfma_f32_16x16x32_bf16 v[88:91], v[160:163], v[200:203], v[88:91]
	v_mfma_f32_16x16x32_bf16 v[80:83], v[146:149], v[208:211], v[80:83]
	v_mfma_f32_16x16x32_bf16 v[72:75], v[160:163], v[208:211], v[72:75]
	v_mfma_f32_16x16x32_bf16 v[124:127], v[156:159], v[188:191], v[124:127]
	v_mfma_f32_16x16x32_bf16 v[120:123], v[164:167], v[188:191], v[120:123]
	v_mfma_f32_16x16x32_bf16 v[112:115], v[156:159], v[196:199], v[112:115]
	v_mfma_f32_16x16x32_bf16 v[104:107], v[164:167], v[196:199], v[104:107]
	v_mfma_f32_16x16x32_bf16 v[96:99], v[156:159], v[204:207], v[96:99]
	v_mfma_f32_16x16x32_bf16 v[88:91], v[164:167], v[204:207], v[88:91]
	v_mfma_f32_16x16x32_bf16 v[80:83], v[156:159], v[212:215], v[80:83]
	v_mfma_f32_16x16x32_bf16 v[72:75], v[164:167], v[212:215], v[72:75]
	v_mfma_f32_16x16x32_bf16 v[116:119], v[168:171], v[184:187], v[116:119]
	v_mfma_f32_16x16x32_bf16 v[108:111], v[176:179], v[184:187], v[108:111]
	v_mfma_f32_16x16x32_bf16 v[100:103], v[168:171], v[192:195], v[100:103]
	v_mfma_f32_16x16x32_bf16 v[92:95], v[176:179], v[192:195], v[92:95]
	v_mfma_f32_16x16x32_bf16 v[84:87], v[168:171], v[200:203], v[84:87]
	v_mfma_f32_16x16x32_bf16 v[76:79], v[176:179], v[200:203], v[76:79]
	v_mfma_f32_16x16x32_bf16 v[68:71], v[168:171], v[208:211], v[68:71]
	v_mfma_f32_16x16x32_bf16 v[64:67], v[176:179], v[208:211], v[64:67]
	v_mfma_f32_16x16x32_bf16 v[116:119], v[172:175], v[188:191], v[116:119]
	v_mfma_f32_16x16x32_bf16 v[108:111], v[180:183], v[188:191], v[108:111]
	v_mfma_f32_16x16x32_bf16 v[100:103], v[172:175], v[196:199], v[100:103]
	v_mfma_f32_16x16x32_bf16 v[92:95], v[180:183], v[196:199], v[92:95]
	v_mfma_f32_16x16x32_bf16 v[84:87], v[172:175], v[204:207], v[84:87]
	v_mfma_f32_16x16x32_bf16 v[76:79], v[180:183], v[204:207], v[76:79]
	v_mfma_f32_16x16x32_bf16 v[68:71], v[172:175], v[212:215], v[68:71]
	v_mfma_f32_16x16x32_bf16 v[64:67], v[180:183], v[212:215], v[64:67]
	s_barrier
; #define PG8_STAGE(bufoff, gbase, voff) do { _Pragma("unroll") for (int _i = 0; _i < 2; ++_i) \
;         __builtin_amdgcn_global_load_lds((const unsigned*)((const char*)(gbase) + (voff)[_i]), (PG8_LAS unsigned*)(lds + (bufoff) + ldsw + _i * 8192), 16, 0, 0); } while (0)
; #define PG8_WAIT_V(n) asm volatile("s_waitcnt vmcnt(" #n ")" ::: "memory")
; #define PG8_WAIT_L(n) asm volatile("s_waitcnt lgkmcnt(" #n ")" ::: "memory")
; #define PG8_BAR __builtin_amdgcn_s_barrier()
; #define PG8_SCHED __builtin_amdgcn_sched_barrier(0)
; template <class Epi, class Sched, bool ALIGN_EPI = false, bool SP2 = false, bool FP8 = false, bool PEEL = false>
; __device__ __forceinline__ void gemm_phase(PG8_LAS unsigned char* lds, const Gemm g, const Sched& S, const Epi& E, const int wid) {
;     ...
;             PG8_WAIT_V(8); PG8_WAIT_L(0); PG8_BAR; PG8_MMA(1, 0, At, B0); PG8_MMA(1, 1, At, B1); PG8_BAR; PG8_SCHED;
;             PG8_LDB(B0, 1, 0); PG8_LDB(B1, 1, 1); PG8_SCHED; PG8_LDA(At, 1, 0); PG8_STAGE(PG8_SA(0, 1), a2 + hstep, voffA);
;             PG8_WAIT_V(8); PG8_WAIT_L(0); PG8_BAR; PG8_MMA(0, 0, At, B0); PG8_MMA(0, 1, At, B1); PG8_BAR; PG8_SCHED;
;             PG8_LDA(At, 1, 1); PG8_STAGE(PG8_SB(1, 0), b3, voffB); PG8_STAGE(PG8_SB(1, 1), b3 + hstep, voffB); PG8_STAGE(PG8_SA(1, 0), a3, voffA);
;             PG8_WAIT_V(8); PG8_WAIT_L(0); PG8_BAR; PG8_MMA(1, 0, At, B0); PG8_MMA(1, 1, At, B1); PG8_BAR; PG8_SCHED;
;         }
;     ...
;         if constexpr (ALIGN_EPI) { if (wr == 0) PG8_BAR; }
	s_add_i32 s46, s62, s3
	v_lshl_add_u64 v[216:217], v[216:217], 0, s[14:15]
	s_mov_b32 m0, s46
	ds_read_b128 v[184:187], v154 offset:49152
	ds_read_b128 v[188:191], v154 offset:50176
	ds_read_b128 v[192:195], v154 offset:51200
	ds_read_b128 v[196:199], v154 offset:52224
	ds_read_b128 v[200:203], v154 offset:53248
	ds_read_b128 v[204:207], v154 offset:54272
	ds_read_b128 v[208:211], v154 offset:55296
	ds_read_b128 v[212:215], v154 offset:56320
	global_load_lds_dwordx4 v[216:217], off
	s_add_i32 m0, s46, 0x2000
	s_add_u32 s44, s44, 0x40080
	v_lshl_add_u64 v[216:217], v[218:219], 0, s[14:15]
	s_addc_u32 s45, s45, 0
	s_add_i32 s46, s63, s3
	global_load_lds_dwordx4 v[216:217], off
	v_lshl_add_u64 v[216:217], s[44:45], 0, v[132:133]
	s_mov_b32 m0, s46
	s_nop 0
	global_load_lds_dwordx4 v[216:217], off
	v_lshl_add_u64 v[216:217], s[44:45], 0, v[128:129]
	s_add_i32 m0, s46, 0x2000
	s_nop 0
	global_load_lds_dwordx4 v[216:217], off
	v_lshl_add_u64 v[216:217], v[220:221], 0, s[14:15]
	s_mov_b32 m0, s50
	s_nop 0
	global_load_lds_dwordx4 v[216:217], off
	v_lshl_add_u64 v[216:217], v[222:223], 0, s[14:15]
	s_mov_b32 m0, s51
	s_nop 0
	global_load_lds_dwordx4 v[216:217], off
	s_waitcnt vmcnt(8)
	s_waitcnt lgkmcnt(0)
	s_barrier
	s_waitcnt lgkmcnt(0)
	v_mfma_f32_16x16x32_bf16 v[60:63], v[146:149], v[184:187], v[60:63]
	v_mfma_f32_16x16x32_bf16 v[56:59], v[160:163], v[184:187], v[56:59]
	v_mfma_f32_16x16x32_bf16 v[48:51], v[146:149], v[192:195], v[48:51]
	v_mfma_f32_16x16x32_bf16 v[40:43], v[160:163], v[192:195], v[40:43]
	v_mfma_f32_16x16x32_bf16 v[32:35], v[146:149], v[200:203], v[32:35]
	v_mfma_f32_16x16x32_bf16 v[24:27], v[160:163], v[200:203], v[24:27]
	v_mfma_f32_16x16x32_bf16 v[16:19], v[146:149], v[208:211], v[16:19]
	v_mfma_f32_16x16x32_bf16 v[8:11], v[160:163], v[208:211], v[8:11]
	v_mfma_f32_16x16x32_bf16 v[60:63], v[156:159], v[188:191], v[60:63]
	v_mfma_f32_16x16x32_bf16 v[56:59], v[164:167], v[188:191], v[56:59]
	v_mfma_f32_16x16x32_bf16 v[48:51], v[156:159], v[196:199], v[48:51]
	v_mfma_f32_16x16x32_bf16 v[40:43], v[164:167], v[196:199], v[40:43]
	v_mfma_f32_16x16x32_bf16 v[32:35], v[156:159], v[204:207], v[32:35]
	v_mfma_f32_16x16x32_bf16 v[24:27], v[164:167], v[204:207], v[24:27]
	v_mfma_f32_16x16x32_bf16 v[16:19], v[156:159], v[212:215], v[16:19]
	v_mfma_f32_16x16x32_bf16 v[8:11], v[164:167], v[212:215], v[8:11]
	v_mfma_f32_16x16x32_bf16 v[52:55], v[168:171], v[184:187], v[52:55]
	v_mfma_f32_16x16x32_bf16 v[44:47], v[176:179], v[184:187], v[44:47]
	v_mfma_f32_16x16x32_bf16 v[36:39], v[168:171], v[192:195], v[36:39]
	v_mfma_f32_16x16x32_bf16 v[28:31], v[176:179], v[192:195], v[28:31]
	v_mfma_f32_16x16x32_bf16 v[20:23], v[168:171], v[200:203], v[20:23]
	v_mfma_f32_16x16x32_bf16 v[12:15], v[176:179], v[200:203], v[12:15]
	v_mfma_f32_16x16x32_bf16 v[4:7], v[168:171], v[208:211], v[4:7]
	v_mfma_f32_16x16x32_bf16 v[0:3], v[176:179], v[208:211], v[0:3]
	v_mfma_f32_16x16x32_bf16 v[52:55], v[172:175], v[188:191], v[52:55]
	v_mfma_f32_16x16x32_bf16 v[44:47], v[180:183], v[188:191], v[44:47]
	v_mfma_f32_16x16x32_bf16 v[36:39], v[172:175], v[196:199], v[36:39]
	v_mfma_f32_16x16x32_bf16 v[28:31], v[180:183], v[196:199], v[28:31]
	v_mfma_f32_16x16x32_bf16 v[20:23], v[172:175], v[204:207], v[20:23]
	v_mfma_f32_16x16x32_bf16 v[12:15], v[180:183], v[204:207], v[12:15]
	v_mfma_f32_16x16x32_bf16 v[4:7], v[172:175], v[212:215], v[4:7]
	v_mfma_f32_16x16x32_bf16 v[0:3], v[180:183], v[212:215], v[0:3]
	s_barrier
	s_add_i32 s61, s61, 2
	s_add_u32 s36, s36, 0x100
	s_addc_u32 s37, s37, 0
	s_add_u32 s59, s59, 0x100
	s_addc_u32 s60, s60, 0
	s_cmp_gt_u32 s61, 13
	s_cbranch_scc0 .LBB0_1120
	s_and_b64 vcc, exec, s[12:13]
	s_cbranch_vccz .LBB0_1123
	s_barrier

; #define PG8_STAGE(bufoff, gbase, voff) do { _Pragma("unroll") for (int _i = 0; _i < 2; ++_i) \
;         __builtin_amdgcn_global_load_lds((const unsigned*)((const char*)(gbase) + (voff)[_i]), (PG8_LAS unsigned*)(lds + (bufoff) + ldsw + _i * 8192), 16, 0, 0); } while (0)
; #define PG8_WAIT_V(n) asm volatile("s_waitcnt vmcnt(" #n ")" ::: "memory")
; #define PG8_WAIT_L(n) asm volatile("s_waitcnt lgkmcnt(" #n ")" ::: "memory")
; #define PG8_BAR __builtin_amdgcn_s_barrier()
; #define PG8_SCHED __builtin_amdgcn_sched_barrier(0)
; template <class Epi, class Sched, bool ALIGN_EPI = false, bool SP2 = false, bool FP8 = false, bool PEEL = false>
; __device__ __forceinline__ void gemm_phase(PG8_LAS unsigned char* lds, const Gemm g, const Sched& S, const Epi& E, const int wid) {
;     ...
;         for (int t = 0; t < nt; t += 2) {
;             const bool last = (t == nt - 2);
;             const char* a1 = cA + (size_t)(t + 1) * kstep;
;             const char* a2 = last ? nA : cA + (size_t)(t + 2) * kstep; const char* b2 = last ? nB : cB + (size_t)(t + 2) * kstep;
;             const char* a3 = a2 + kstep; const char* b3 = b2 + kstep;
;             if (last && has_next) S.a_ready(nxt);
;             PG8_LDB(B0, 0, 0); PG8_LDB(B1, 0, 1); PG8_SCHED; PG8_LDA(At, 0, 0); PG8_STAGE(PG8_SA(1, 1), a1 + hstep, voffA);
;             PG8_WAIT_V(8); PG8_WAIT_L(0); PG8_BAR; PG8_MMA(0, 0, At, B0); PG8_MMA(0, 1, At, B1); PG8_BAR; PG8_SCHED;
;             PG8_LDA(At, 0, 1); PG8_STAGE(PG8_SB(0, 0), b2, voffB); PG8_STAGE(PG8_SB(0, 1), b2 + hstep, voffB); PG8_STAGE(PG8_SA(0, 0), a2, voffA);
;             PG8_WAIT_V(8); PG8_WAIT_L(0); PG8_BAR; PG8_MMA(1, 0, At, B0); PG8_MMA(1, 1, At, B1); PG8_BAR; PG8_SCHED;
;             PG8_LDB(B0, 1, 0); PG8_LDB(B1, 1, 1); PG8_SCHED; PG8_LDA(At, 1, 0); PG8_STAGE(PG8_SA(0, 1), a2 + hstep, voffA);
;             PG8_WAIT_V(8); PG8_WAIT_L(0); PG8_BAR; PG8_MMA(0, 0, At, B0); PG8_MMA(0, 1, At, B1); PG8_BAR; PG8_SCHED;
;             PG8_LDA(At, 1, 1); PG8_STAGE(PG8_SB(1, 0), b3, voffB); PG8_STAGE(PG8_SB(1, 1), b3 + hstep, voffB); PG8_STAGE(PG8_SA(1, 0), a3, voffA);
;             PG8_WAIT_V(8); PG8_WAIT_L(0); PG8_BAR; PG8_MMA(1, 0, At, B0); PG8_MMA(1, 1, At, B1); PG8_BAR; PG8_SCHED;
;         }
.LBB0_1535:
	ds_read_b128 v[128:131], v209
	ds_read_b128 v[132:135], v209 offset:1024
	ds_read_b128 v[136:139], v209 offset:2048
	ds_read_b128 v[140:143], v209 offset:3072
	ds_read_b128 v[144:147], v210
	ds_read_b128 v[148:151], v210 offset:1024
	ds_read_b128 v[152:155], v210 offset:2048
	ds_read_b128 v[156:159], v210 offset:3072
	s_add_u32 s30, s26, 0xfffc0080
	s_addc_u32 s31, s27, -1
	s_cmp_eq_u32 s67, 12
	s_cselect_b32 s37, s15, s31
	s_cselect_b32 s36, s63, s30
	s_cselect_b32 s31, s13, s66
	s_cselect_b32 s30, s64, s65
	v_lshl_add_u64 v[204:205], s[26:27], 0, v[196:197]
	s_add_i32 m0, s41, 0xc000
	ds_read_b128 v[160:163], v211
	ds_read_b128 v[164:167], v211 offset:1024
	ds_read_b128 v[168:171], v211 offset:2048
	ds_read_b128 v[172:175], v211 offset:3072
	ds_read_b128 v[176:179], v211 offset:4096
	ds_read_b128 v[180:183], v211 offset:5120
	ds_read_b128 v[184:187], v211 offset:6144
	ds_read_b128 v[212:215], v211 offset:7168
	global_load_lds_dwordx4 v[204:205], off
	v_lshl_add_u64 v[204:205], s[26:27], 0, v[198:199]
	s_add_i32 m0, s41, 0xe000
	s_nop 0
	global_load_lds_dwordx4 v[204:205], off
	s_waitcnt vmcnt(8)
	s_waitcnt lgkmcnt(0)
	s_barrier
	s_waitcnt lgkmcnt(0)
	v_mfma_f32_16x16x32_bf16 v[124:127], v[128:131], v[160:163], v[124:127]
	v_mfma_f32_16x16x32_bf16 v[120:123], v[136:139], v[160:163], v[120:123]
	v_mfma_f32_16x16x32_bf16 v[108:111], v[128:131], v[168:171], v[108:111]
	v_mfma_f32_16x16x32_bf16 v[104:107], v[136:139], v[168:171], v[104:107]
	v_mfma_f32_16x16x32_bf16 v[92:95], v[128:131], v[176:179], v[92:95]
	v_mfma_f32_16x16x32_bf16 v[88:91], v[136:139], v[176:179], v[88:91]
	v_mfma_f32_16x16x32_bf16 v[76:79], v[128:131], v[184:187], v[76:79]
	v_mfma_f32_16x16x32_bf16 v[72:75], v[136:139], v[184:187], v[72:75]
	v_mfma_f32_16x16x32_bf16 v[124:127], v[132:135], v[164:167], v[124:127]
	v_mfma_f32_16x16x32_bf16 v[120:123], v[140:143], v[164:167], v[120:123]
	v_mfma_f32_16x16x32_bf16 v[108:111], v[132:135], v[172:175], v[108:111]
	v_mfma_f32_16x16x32_bf16 v[104:107], v[140:143], v[172:175], v[104:107]
	v_mfma_f32_16x16x32_bf16 v[92:95], v[132:135], v[180:183], v[92:95]
	v_mfma_f32_16x16x32_bf16 v[88:91], v[140:143], v[180:183], v[88:91]
	v_mfma_f32_16x16x32_bf16 v[76:79], v[132:135], v[212:215], v[76:79]
	v_mfma_f32_16x16x32_bf16 v[72:75], v[140:143], v[212:215], v[72:75]
	v_mfma_f32_16x16x32_bf16 v[116:119], v[144:147], v[160:163], v[116:119]
	v_mfma_f32_16x16x32_bf16 v[112:115], v[152:155], v[160:163], v[112:115]
	v_mfma_f32_16x16x32_bf16 v[100:103], v[144:147], v[168:171], v[100:103]
	v_mfma_f32_16x16x32_bf16 v[96:99], v[152:155], v[168:171], v[96:99]
	v_mfma_f32_16x16x32_bf16 v[84:87], v[144:147], v[176:179], v[84:87]
	v_mfma_f32_16x16x32_bf16 v[80:83], v[152:155], v[176:179], v[80:83]
	v_mfma_f32_16x16x32_bf16 v[68:71], v[144:147], v[184:187], v[68:71]
	v_mfma_f32_16x16x32_bf16 v[64:67], v[152:155], v[184:187], v[64:67]
	v_mfma_f32_16x16x32_bf16 v[116:119], v[148:151], v[164:167], v[116:119]
	v_mfma_f32_16x16x32_bf16 v[112:115], v[156:159], v[164:167], v[112:115]
	v_mfma_f32_16x16x32_bf16 v[100:103], v[148:151], v[172:175], v[100:103]
	v_mfma_f32_16x16x32_bf16 v[96:99], v[156:159], v[172:175], v[96:99]
	v_mfma_f32_16x16x32_bf16 v[84:87], v[148:151], v[180:183], v[84:87]
	v_mfma_f32_16x16x32_bf16 v[80:83], v[156:159], v[180:183], v[80:83]
	v_mfma_f32_16x16x32_bf16 v[68:71], v[148:151], v[212:215], v[68:71]
	v_mfma_f32_16x16x32_bf16 v[64:67], v[156:159], v[212:215], v[64:67]
	s_barrier
	s_add_i32 s75, s54, s39
	v_lshl_add_u64 v[204:205], s[30:31], 0, v[192:193]
	s_mov_b32 m0, s75
	ds_read_b128 v[160:163], v211 offset:16384
	ds_read_b128 v[164:167], v211 offset:17408
	ds_read_b128 v[168:171], v211 offset:18432
	ds_read_b128 v[172:175], v211 offset:19456
	ds_read_b128 v[176:179], v211 offset:20480
	ds_read_b128 v[180:183], v211 offset:21504
	ds_read_b128 v[184:187], v211 offset:22528
	ds_read_b128 v[212:215], v211 offset:23552
	global_load_lds_dwordx4 v[204:205], off
	s_add_i32 m0, s75, 0x2000
	s_add_u32 s80, s30, 0x40000
	v_lshl_add_u64 v[216:217], s[30:31], 0, v[188:189]
	s_addc_u32 s81, s31, 0
	s_add_i32 s75, s55, s39
	global_load_lds_dwordx4 v[216:217], off
	v_lshl_add_u64 v[218:219], s[80:81], 0, v[192:193]
	s_mov_b32 m0, s75
	v_lshl_add_u64 v[220:221], s[36:37], 0, v[190:191]
	global_load_lds_dwordx4 v[218:219], off
	v_lshl_add_u64 v[218:219], s[80:81], 0, v[188:189]
	s_add_i32 m0, s75, 0x2000
	s_nop 0
	global_load_lds_dwordx4 v[218:219], off
	v_lshl_add_u64 v[218:219], s[36:37], 0, v[194:195]
	s_mov_b32 m0, s41
	s_nop 0
	global_load_lds_dwordx4 v[218:219], off
	s_mov_b32 m0, s42
	s_nop 0
	global_load_lds_dwordx4 v[220:221], off
	s_waitcnt vmcnt(8)
	s_waitcnt lgkmcnt(0)
	s_barrier
; #define PG8_STAGE(bufoff, gbase, voff) do { _Pragma("unroll") for (int _i = 0; _i < 2; ++_i) \
;         __builtin_amdgcn_global_load_lds((const unsigned*)((const char*)(gbase) + (voff)[_i]), (PG8_LAS unsigned*)(lds + (bufoff) + ldsw + _i * 8192), 16, 0, 0); } while (0)
; #define PG8_WAIT_V(n) asm volatile("s_waitcnt vmcnt(" #n ")" ::: "memory")
; #define PG8_WAIT_L(n) asm volatile("s_waitcnt lgkmcnt(" #n ")" ::: "memory")
; #define PG8_BAR __builtin_amdgcn_s_barrier()
; #define PG8_SCHED __builtin_amdgcn_sched_barrier(0)
; template <class Epi, class Sched, bool ALIGN_EPI = false, bool SP2 = false, bool FP8 = false, bool PEEL = false>
; __device__ __forceinline__ void gemm_phase(PG8_LAS unsigned char* lds, const Gemm g, const Sched& S, const Epi& E, const int wid) {
;     ...
;         for (int t = 0; t < nt; t += 2) {
;             const bool last = (t == nt - 2);
;             const char* a1 = cA + (size_t)(t + 1) * kstep;
;             const char* a2 = last ? nA : cA + (size_t)(t + 2) * kstep; const char* b2 = last ? nB : cB + (size_t)(t + 2) * kstep;
;             const char* a3 = a2 + kstep; const char* b3 = b2 + kstep;
;             if (last && has_next) S.a_ready(nxt);
;             PG8_LDB(B0, 0, 0); PG8_LDB(B1, 0, 1); PG8_SCHED; PG8_LDA(At, 0, 0); PG8_STAGE(PG8_SA(1, 1), a1 + hstep, voffA);
;             PG8_WAIT_V(8); PG8_WAIT_L(0); PG8_BAR; PG8_MMA(0, 0, At, B0); PG8_MMA(0, 1, At, B1); PG8_BAR; PG8_SCHED;
;             PG8_LDA(At, 0, 1); PG8_STAGE(PG8_SB(0, 0), b2, voffB); PG8_STAGE(PG8_SB(0, 1), b2 + hstep, voffB); PG8_STAGE(PG8_SA(0, 0), a2, voffA);
;             PG8_WAIT_V(8); PG8_WAIT_L(0); PG8_BAR; PG8_MMA(1, 0, At, B0); PG8_MMA(1, 1, At, B1); PG8_BAR; PG8_SCHED;
;             PG8_LDB(B0, 1, 0); PG8_LDB(B1, 1, 1); PG8_SCHED; PG8_LDA(At, 1, 0); PG8_STAGE(PG8_SA(0, 1), a2 + hstep, voffA);
;             PG8_WAIT_V(8); PG8_WAIT_L(0); PG8_BAR; PG8_MMA(0, 0, At, B0); PG8_MMA(0, 1, At, B1); PG8_BAR; PG8_SCHED;
;             PG8_LDA(At, 1, 1); PG8_STAGE(PG8_SB(1, 0), b3, voffB); PG8_STAGE(PG8_SB(1, 1), b3 + hstep, voffB); PG8_STAGE(PG8_SA(1, 0), a3, voffA);
;             PG8_WAIT_V(8); PG8_WAIT_L(0); PG8_BAR; PG8_MMA(1, 0, At, B0); PG8_MMA(1, 1, At, B1); PG8_BAR; PG8_SCHED;
;         }
	s_waitcnt lgkmcnt(0)
	v_mfma_f32_16x16x32_bf16 v[60:63], v[128:131], v[160:163], v[60:63]
	v_mfma_f32_16x16x32_bf16 v[56:59], v[136:139], v[160:163], v[56:59]
	v_mfma_f32_16x16x32_bf16 v[44:47], v[128:131], v[168:171], v[44:47]
	v_mfma_f32_16x16x32_bf16 v[40:43], v[136:139], v[168:171], v[40:43]
	v_mfma_f32_16x16x32_bf16 v[28:31], v[128:131], v[176:179], v[28:31]
	v_mfma_f32_16x16x32_bf16 v[24:27], v[136:139], v[176:179], v[24:27]
	v_mfma_f32_16x16x32_bf16 v[12:15], v[128:131], v[184:187], v[12:15]
	v_mfma_f32_16x16x32_bf16 v[8:11], v[136:139], v[184:187], v[8:11]
	v_mfma_f32_16x16x32_bf16 v[60:63], v[132:135], v[164:167], v[60:63]
	v_mfma_f32_16x16x32_bf16 v[56:59], v[140:143], v[164:167], v[56:59]
	v_mfma_f32_16x16x32_bf16 v[44:47], v[132:135], v[172:175], v[44:47]
	v_mfma_f32_16x16x32_bf16 v[40:43], v[140:143], v[172:175], v[40:43]
	v_mfma_f32_16x16x32_bf16 v[28:31], v[132:135], v[180:183], v[28:31]
	v_mfma_f32_16x16x32_bf16 v[24:27], v[140:143], v[180:183], v[24:27]
	v_mfma_f32_16x16x32_bf16 v[12:15], v[132:135], v[212:215], v[12:15]
	v_mfma_f32_16x16x32_bf16 v[8:11], v[140:143], v[212:215], v[8:11]
	v_mfma_f32_16x16x32_bf16 v[52:55], v[144:147], v[160:163], v[52:55]
	v_mfma_f32_16x16x32_bf16 v[48:51], v[152:155], v[160:163], v[48:51]
	v_mfma_f32_16x16x32_bf16 v[36:39], v[144:147], v[168:171], v[36:39]
	v_mfma_f32_16x16x32_bf16 v[32:35], v[152:155], v[168:171], v[32:35]
	v_mfma_f32_16x16x32_bf16 v[20:23], v[144:147], v[176:179], v[20:23]
	v_mfma_f32_16x16x32_bf16 v[16:19], v[152:155], v[176:179], v[16:19]
	v_mfma_f32_16x16x32_bf16 v[4:7], v[144:147], v[184:187], v[4:7]
	v_mfma_f32_16x16x32_bf16 v[0:3], v[152:155], v[184:187], v[0:3]
	v_mfma_f32_16x16x32_bf16 v[52:55], v[148:151], v[164:167], v[52:55]
	v_mfma_f32_16x16x32_bf16 v[48:51], v[156:159], v[164:167], v[48:51]
	v_mfma_f32_16x16x32_bf16 v[36:39], v[148:151], v[172:175], v[36:39]
	v_mfma_f32_16x16x32_bf16 v[32:35], v[156:159], v[172:175], v[32:35]
	v_mfma_f32_16x16x32_bf16 v[20:23], v[148:151], v[180:183], v[20:23]
	v_mfma_f32_16x16x32_bf16 v[16:19], v[156:159], v[180:183], v[16:19]
	v_mfma_f32_16x16x32_bf16 v[4:7], v[148:151], v[212:215], v[4:7]
	v_mfma_f32_16x16x32_bf16 v[0:3], v[156:159], v[212:215], v[0:3]
	s_barrier
	s_add_i32 s75, 0, 0x18000
	s_add_i32 s80, 0, 0x1c000
	v_add_u32_e32 v140, s75, v207
	v_add_u32_e32 v156, s80, v207
	ds_read_b128 v[128:131], v140
	ds_read_b128 v[132:135], v140 offset:1024
	ds_read_b128 v[136:139], v140 offset:2048
	ds_read_b128 v[140:143], v140 offset:3072
	ds_read_b128 v[144:147], v156
	ds_read_b128 v[148:151], v156 offset:1024
	ds_read_b128 v[152:155], v156 offset:2048
	ds_read_b128 v[156:159], v156 offset:3072
	s_add_u32 s36, s36, 0x40000
	s_addc_u32 s37, s37, 0
	s_mov_b32 m0, s43
	v_lshl_add_u64 v[222:223], s[36:37], 0, v[194:195]
	ds_read_b128 v[160:163], v211 offset:32768
	ds_read_b128 v[164:167], v211 offset:33792
	ds_read_b128 v[168:171], v211 offset:34816
	ds_read_b128 v[172:175], v211 offset:35840
	ds_read_b128 v[176:179], v211 offset:36864
	ds_read_b128 v[180:183], v211 offset:37888
	ds_read_b128 v[184:187], v211 offset:38912
	ds_read_b128 v[212:215], v211 offset:39936
	global_load_lds_dwordx4 v[222:223], off
	v_lshl_add_u64 v[222:223], s[36:37], 0, v[190:191]
	s_mov_b32 m0, s44
	s_nop 0
	global_load_lds_dwordx4 v[222:223], off
	s_waitcnt vmcnt(8)
	s_waitcnt lgkmcnt(0)
	s_barrier
	s_waitcnt lgkmcnt(0)
	v_mfma_f32_16x16x32_bf16 v[124:127], v[128:131], v[160:163], v[124:127]
	v_mfma_f32_16x16x32_bf16 v[120:123], v[136:139], v[160:163], v[120:123]
	v_mfma_f32_16x16x32_bf16 v[108:111], v[128:131], v[168:171], v[108:111]
	v_mfma_f32_16x16x32_bf16 v[104:107], v[136:139], v[168:171], v[104:107]
	v_mfma_f32_16x16x32_bf16 v[92:95], v[128:131], v[176:179], v[92:95]
	v_mfma_f32_16x16x32_bf16 v[88:91], v[136:139], v[176:179], v[88:91]
	v_mfma_f32_16x16x32_bf16 v[76:79], v[128:131], v[184:187], v[76:79]
	v_mfma_f32_16x16x32_bf16 v[72:75], v[136:139], v[184:187], v[72:75]
	v_mfma_f32_16x16x32_bf16 v[124:127], v[132:135], v[164:167], v[124:127]
	v_mfma_f32_16x16x32_bf16 v[120:123], v[140:143], v[164:167], v[120:123]
	v_mfma_f32_16x16x32_bf16 v[108:111], v[132:135], v[172:175], v[108:111]
	v_mfma_f32_16x16x32_bf16 v[104:107], v[140:143], v[172:175], v[104:107]
	v_mfma_f32_16x16x32_bf16 v[92:95], v[132:135], v[180:183], v[92:95]
	v_mfma_f32_16x16x32_bf16 v[88:91], v[140:143], v[180:183], v[88:91]
	v_mfma_f32_16x16x32_bf16 v[76:79], v[132:135], v[212:215], v[76:79]
	v_mfma_f32_16x16x32_bf16 v[72:75], v[140:143], v[212:215], v[72:75]
	v_mfma_f32_16x16x32_bf16 v[116:119], v[144:147], v[160:163], v[116:119]
	v_mfma_f32_16x16x32_bf16 v[112:115], v[152:155], v[160:163], v[112:115]
	v_mfma_f32_16x16x32_bf16 v[100:103], v[144:147], v[168:171], v[100:103]
	v_mfma_f32_16x16x32_bf16 v[96:99], v[152:155], v[168:171], v[96:99]
	v_mfma_f32_16x16x32_bf16 v[84:87], v[144:147], v[176:179], v[84:87]
	v_mfma_f32_16x16x32_bf16 v[80:83], v[152:155], v[176:179], v[80:83]
	v_mfma_f32_16x16x32_bf16 v[68:71], v[144:147], v[184:187], v[68:71]
	v_mfma_f32_16x16x32_bf16 v[64:67], v[152:155], v[184:187], v[64:67]
	v_mfma_f32_16x16x32_bf16 v[116:119], v[148:151], v[164:167], v[116:119]
	v_mfma_f32_16x16x32_bf16 v[112:115], v[156:159], v[164:167], v[112:115]
	v_mfma_f32_16x16x32_bf16 v[100:103], v[148:151], v[172:175], v[100:103]
	v_mfma_f32_16x16x32_bf16 v[96:99], v[156:159], v[172:175], v[96:99]
	v_mfma_f32_16x16x32_bf16 v[84:87], v[148:151], v[180:183], v[84:87]
	v_mfma_f32_16x16x32_bf16 v[80:83], v[156:159], v[180:183], v[80:83]
	v_mfma_f32_16x16x32_bf16 v[68:71], v[148:151], v[212:215], v[68:71]
	v_mfma_f32_16x16x32_bf16 v[64:67], v[156:159], v[212:215], v[64:67]
	s_barrier
; #define PG8_STAGE(bufoff, gbase, voff) do { _Pragma("unroll") for (int _i = 0; _i < 2; ++_i) \
;         __builtin_amdgcn_global_load_lds((const unsigned*)((const char*)(gbase) + (voff)[_i]), (PG8_LAS unsigned*)(lds + (bufoff) + ldsw + _i * 8192), 16, 0, 0); } while (0)
; #define PG8_WAIT_V(n) asm volatile("s_waitcnt vmcnt(" #n ")" ::: "memory")
; #define PG8_WAIT_L(n) asm volatile("s_waitcnt lgkmcnt(" #n ")" ::: "memory")
; #define PG8_BAR __builtin_amdgcn_s_barrier()
; #define PG8_SCHED __builtin_amdgcn_sched_barrier(0)
; template <class Epi, class Sched, bool ALIGN_EPI = false, bool SP2 = false, bool FP8 = false, bool PEEL = false>
; __device__ __forceinline__ void gemm_phase(PG8_LAS unsigned char* lds, const Gemm g, const Sched& S, const Epi& E, const int wid) {
;     ...
;             PG8_WAIT_V(8); PG8_WAIT_L(0); PG8_BAR; PG8_MMA(1, 0, At, B0); PG8_MMA(1, 1, At, B1); PG8_BAR; PG8_SCHED;
;             PG8_LDB(B0, 1, 0); PG8_LDB(B1, 1, 1); PG8_SCHED; PG8_LDA(At, 1, 0); PG8_STAGE(PG8_SA(0, 1), a2 + hstep, voffA);
;             PG8_WAIT_V(8); PG8_WAIT_L(0); PG8_BAR; PG8_MMA(0, 0, At, B0); PG8_MMA(0, 1, At, B1); PG8_BAR; PG8_SCHED;
;             PG8_LDA(At, 1, 1); PG8_STAGE(PG8_SB(1, 0), b3, voffB); PG8_STAGE(PG8_SB(1, 1), b3 + hstep, voffB); PG8_STAGE(PG8_SA(1, 0), a3, voffA);
;             PG8_WAIT_V(8); PG8_WAIT_L(0); PG8_BAR; PG8_MMA(1, 0, At, B0); PG8_MMA(1, 1, At, B1); PG8_BAR; PG8_SCHED;
;         }
;     ...
;         if constexpr (ALIGN_EPI) { if (wr == 0) PG8_BAR; }
	s_add_i32 s36, s75, s39
	v_lshl_add_u64 v[204:205], v[204:205], 0, s[10:11]
	s_mov_b32 m0, s36
	ds_read_b128 v[160:163], v211 offset:49152
	ds_read_b128 v[164:167], v211 offset:50176
	ds_read_b128 v[168:171], v211 offset:51200
	ds_read_b128 v[172:175], v211 offset:52224
	ds_read_b128 v[176:179], v211 offset:53248
	ds_read_b128 v[180:183], v211 offset:54272
	ds_read_b128 v[184:187], v211 offset:55296
	ds_read_b128 v[212:215], v211 offset:56320
	global_load_lds_dwordx4 v[204:205], off
	s_add_i32 m0, s36, 0x2000
	s_add_u32 s30, s30, 0x40080
	v_lshl_add_u64 v[204:205], v[216:217], 0, s[10:11]
	s_addc_u32 s31, s31, 0
	s_add_i32 s36, s80, s39
	global_load_lds_dwordx4 v[204:205], off
	v_lshl_add_u64 v[204:205], s[30:31], 0, v[192:193]
	s_mov_b32 m0, s36
	s_nop 0
	global_load_lds_dwordx4 v[204:205], off
	v_lshl_add_u64 v[204:205], s[30:31], 0, v[188:189]
	s_add_i32 m0, s36, 0x2000
	s_nop 0
	global_load_lds_dwordx4 v[204:205], off
	v_lshl_add_u64 v[204:205], v[218:219], 0, s[10:11]
	s_mov_b32 m0, s50
	s_nop 0
	global_load_lds_dwordx4 v[204:205], off
	v_lshl_add_u64 v[204:205], v[220:221], 0, s[10:11]
	s_mov_b32 m0, s51
	s_nop 0
	global_load_lds_dwordx4 v[204:205], off
	s_waitcnt vmcnt(8)
	s_waitcnt lgkmcnt(0)
	s_barrier
	s_waitcnt lgkmcnt(0)
	v_mfma_f32_16x16x32_bf16 v[60:63], v[128:131], v[160:163], v[60:63]
	v_mfma_f32_16x16x32_bf16 v[56:59], v[136:139], v[160:163], v[56:59]
	v_mfma_f32_16x16x32_bf16 v[44:47], v[128:131], v[168:171], v[44:47]
	v_mfma_f32_16x16x32_bf16 v[40:43], v[136:139], v[168:171], v[40:43]
	v_mfma_f32_16x16x32_bf16 v[28:31], v[128:131], v[176:179], v[28:31]
	v_mfma_f32_16x16x32_bf16 v[24:27], v[136:139], v[176:179], v[24:27]
	v_mfma_f32_16x16x32_bf16 v[12:15], v[128:131], v[184:187], v[12:15]
	v_mfma_f32_16x16x32_bf16 v[8:11], v[136:139], v[184:187], v[8:11]
	v_mfma_f32_16x16x32_bf16 v[60:63], v[132:135], v[164:167], v[60:63]
	v_mfma_f32_16x16x32_bf16 v[56:59], v[140:143], v[164:167], v[56:59]
	v_mfma_f32_16x16x32_bf16 v[44:47], v[132:135], v[172:175], v[44:47]
	v_mfma_f32_16x16x32_bf16 v[40:43], v[140:143], v[172:175], v[40:43]
	v_mfma_f32_16x16x32_bf16 v[28:31], v[132:135], v[180:183], v[28:31]
	v_mfma_f32_16x16x32_bf16 v[24:27], v[140:143], v[180:183], v[24:27]
	v_mfma_f32_16x16x32_bf16 v[12:15], v[132:135], v[212:215], v[12:15]
	v_mfma_f32_16x16x32_bf16 v[8:11], v[140:143], v[212:215], v[8:11]
	v_mfma_f32_16x16x32_bf16 v[52:55], v[144:147], v[160:163], v[52:55]
	v_mfma_f32_16x16x32_bf16 v[48:51], v[152:155], v[160:163], v[48:51]
	v_mfma_f32_16x16x32_bf16 v[36:39], v[144:147], v[168:171], v[36:39]
	v_mfma_f32_16x16x32_bf16 v[32:35], v[152:155], v[168:171], v[32:35]
	v_mfma_f32_16x16x32_bf16 v[20:23], v[144:147], v[176:179], v[20:23]
	v_mfma_f32_16x16x32_bf16 v[16:19], v[152:155], v[176:179], v[16:19]
	v_mfma_f32_16x16x32_bf16 v[4:7], v[144:147], v[184:187], v[4:7]
	v_mfma_f32_16x16x32_bf16 v[0:3], v[152:155], v[184:187], v[0:3]
	v_mfma_f32_16x16x32_bf16 v[52:55], v[148:151], v[164:167], v[52:55]
	v_mfma_f32_16x16x32_bf16 v[48:51], v[156:159], v[164:167], v[48:51]
	v_mfma_f32_16x16x32_bf16 v[36:39], v[148:151], v[172:175], v[36:39]
	v_mfma_f32_16x16x32_bf16 v[32:35], v[156:159], v[172:175], v[32:35]
	v_mfma_f32_16x16x32_bf16 v[20:23], v[148:151], v[180:183], v[20:23]
	v_mfma_f32_16x16x32_bf16 v[16:19], v[156:159], v[180:183], v[16:19]
	v_mfma_f32_16x16x32_bf16 v[4:7], v[148:151], v[212:215], v[4:7]
	v_mfma_f32_16x16x32_bf16 v[0:3], v[156:159], v[212:215], v[0:3]
	s_barrier
	s_add_i32 s67, s67, 2
	s_add_u32 s26, s26, 0x100
	s_addc_u32 s27, s27, 0
	s_add_u32 s65, s65, 0x100
	s_addc_u32 s66, s66, 0
	s_cmp_gt_u32 s67, 13
	s_cbranch_scc0 .LBB0_1535
	s_and_b64 vcc, exec, s[8:9]
	s_cbranch_vccz .LBB0_1538
	s_barrier

; #define PG8_STAGE(bufoff, gbase, voff) do { _Pragma("unroll") for (int _i = 0; _i < 2; ++_i) \
;         __builtin_amdgcn_global_load_lds((const unsigned*)((const char*)(gbase) + (voff)[_i]), (PG8_LAS unsigned*)(lds + (bufoff) + ldsw + _i * 8192), 16, 0, 0); } while (0)
; #define PG8_WAIT_V(n) asm volatile("s_waitcnt vmcnt(" #n ")" ::: "memory")
; #define PG8_WAIT_L(n) asm volatile("s_waitcnt lgkmcnt(" #n ")" ::: "memory")
; #define PG8_BAR __builtin_amdgcn_s_barrier()
; #define PG8_SCHED __builtin_amdgcn_sched_barrier(0)
; template <class Epi, class Sched, bool ALIGN_EPI = false, bool SP2 = false, bool FP8 = false, bool PEEL = false>
; __device__ __forceinline__ void gemm_phase(PG8_LAS unsigned char* lds, const Gemm g, const Sched& S, const Epi& E, const int wid) {
;     ...
;         {
;             const int t = 0;
;             const bool last = (t == nt - 2);
;             const char* a1 = cA + (size_t)(t + 1) * kstep;
;             const char* a2 = last ? nA : cA + (size_t)(t + 2) * kstep; const char* b2 = last ? nB : cB + (size_t)(t + 2) * kstep;
;             const char* a3 = a2 + kstep; const char* b3 = b2 + kstep;
;             if (last && has_next) S.a_ready(nxt);
;             PG8_LDB(B0, 0, 0); PG8_LDB(B1, 0, 1); PG8_SCHED; PG8_LDA(At, 0, 0); PG8_STAGE(PG8_SA(1, 1), a1 + hstep, voffA);
;             PG8_WAIT_V(8); PG8_WAIT_L(0); PG8_BAR; PG8_MMAZ(0, 0, At, B0); PG8_MMAZ(0, 1, At, B1); PG8_BAR; PG8_SCHED;
;             PG8_LDA(At, 0, 1); PG8_STAGE(PG8_SB(0, 0), b2, voffB); PG8_STAGE(PG8_SB(0, 1), b2 + hstep, voffB); PG8_STAGE(PG8_SA(0, 0), a2, voffA);
;             PG8_WAIT_V(8); PG8_WAIT_L(0); PG8_BAR; PG8_MMAZ(1, 0, At, B0); PG8_MMAZ(1, 1, At, B1); PG8_BAR; PG8_SCHED;
;             PG8_LDB(B0, 1, 0); PG8_LDB(B1, 1, 1); PG8_SCHED; PG8_LDA(At, 1, 0); PG8_STAGE(PG8_SA(0, 1), a2 + hstep, voffA);
.LBB0_1760:
	s_ashr_i32 s25, s24, 31
	s_lshl_b64 s[30:31], s[24:25], 18
	v_add_u32_e32 v186, s62, v183
	v_add_u32_e32 v187, s63, v183
	s_add_u32 s30, s34, s30
	ds_read_b128 v[16:19], v186
	ds_read_b128 v[20:23], v186 offset:1024
	ds_read_b128 v[24:27], v186 offset:2048
	ds_read_b128 v[28:31], v186 offset:3072
	ds_read_b128 v[0:3], v187
	ds_read_b128 v[4:7], v187 offset:1024
	ds_read_b128 v[8:11], v187 offset:2048
	ds_read_b128 v[12:15], v187 offset:3072
	s_addc_u32 s31, s35, s31
	s_ashr_i32 s27, s26, 31
	s_lshl_b64 s[36:37], s[26:27], 18
	s_add_u32 s36, s47, s36
	s_addc_u32 s37, s48, s37
	s_and_b64 s[42:43], s[4:5], exec
	s_cselect_b32 s25, s31, s41
	s_cselect_b32 s27, s30, s40
	s_cselect_b32 s75, s37, s39
	s_cselect_b32 s76, s36, s38
	s_add_u32 s42, s40, 0x20080
	s_addc_u32 s43, s41, 0
	s_add_i32 s77, s54, 0xc000
	v_lshl_add_u64 v[212:213], s[42:43], 0, v[160:161]
	s_mov_b32 m0, s77
	s_add_i32 s78, s54, 0xe000
	ds_read_b128 v[174:177], v185
	ds_read_b128 v[178:181], v185 offset:1024
	ds_read_b128 v[188:191], v185 offset:2048
	ds_read_b128 v[192:195], v185 offset:3072
	ds_read_b128 v[196:199], v185 offset:4096
	ds_read_b128 v[200:203], v185 offset:5120
	ds_read_b128 v[204:207], v185 offset:6144
	ds_read_b128 v[208:211], v185 offset:7168
	global_load_lds_dwordx4 v[212:213], off
	v_lshl_add_u64 v[212:213], s[42:43], 0, v[164:165]
	s_mov_b32 m0, s78
	s_nop 0
	global_load_lds_dwordx4 v[212:213], off
	s_waitcnt vmcnt(8)
	s_waitcnt lgkmcnt(0)
	s_barrier
	s_waitcnt lgkmcnt(0)
	v_mfma_f32_16x16x128_f8f6f4 v[156:159], v[16:23], v[174:181], 0
	v_mfma_f32_16x16x128_f8f6f4 v[152:155], v[24:31], v[174:181], 0
	v_mfma_f32_16x16x128_f8f6f4 v[148:151], v[16:23], v[188:195], 0
	v_mfma_f32_16x16x128_f8f6f4 v[144:147], v[24:31], v[188:195], 0
	v_mfma_f32_16x16x128_f8f6f4 v[140:143], v[16:23], v[196:203], 0
	v_mfma_f32_16x16x128_f8f6f4 v[136:139], v[24:31], v[196:203], 0
	v_mfma_f32_16x16x128_f8f6f4 v[132:135], v[16:23], v[204:211], 0
	v_mfma_f32_16x16x128_f8f6f4 v[128:131], v[24:31], v[204:211], 0
	v_mfma_f32_16x16x128_f8f6f4 v[124:127], v[0:7], v[174:181], 0
	v_mfma_f32_16x16x128_f8f6f4 v[120:123], v[8:15], v[174:181], 0
	v_mfma_f32_16x16x128_f8f6f4 v[116:119], v[0:7], v[188:195], 0
	v_mfma_f32_16x16x128_f8f6f4 v[112:115], v[8:15], v[188:195], 0
	v_mfma_f32_16x16x128_f8f6f4 v[108:111], v[0:7], v[196:203], 0
	v_mfma_f32_16x16x128_f8f6f4 v[104:107], v[8:15], v[196:203], 0
	v_mfma_f32_16x16x128_f8f6f4 v[100:103], v[0:7], v[204:211], 0
	v_mfma_f32_16x16x128_f8f6f4 v[96:99], v[8:15], v[204:211], 0
	s_barrier
	v_lshl_add_u64 v[174:175], s[38:39], 0, v[162:163]
	s_add_i32 s79, s62, s49
	v_lshl_add_u64 v[176:177], v[174:175], 0, s[12:13]
	s_mov_b32 m0, s79
	s_add_i32 s80, s79, 0x2000
	ds_read_b128 v[188:191], v185 offset:16384
	ds_read_b128 v[192:195], v185 offset:17408
	ds_read_b128 v[196:199], v185 offset:18432
	ds_read_b128 v[200:203], v185 offset:19456
	ds_read_b128 v[204:207], v185 offset:20480
	ds_read_b128 v[208:211], v185 offset:21504
	ds_read_b128 v[212:215], v185 offset:22528
	ds_read_b128 v[216:219], v185 offset:23552
	global_load_lds_dwordx4 v[176:177], off
	v_lshl_add_u64 v[176:177], s[38:39], 0, v[166:167]
	s_add_u32 s42, s38, 0x20100
	v_lshl_add_u64 v[178:179], v[176:177], 0, s[12:13]
	s_mov_b32 m0, s80
	s_addc_u32 s43, s39, 0
	s_add_i32 s81, s63, s49
	global_load_lds_dwordx4 v[178:179], off
	v_lshl_add_u64 v[178:179], s[42:43], 0, v[162:163]
	s_mov_b32 m0, s81
	s_add_i32 s82, s81, 0x2000
	global_load_lds_dwordx4 v[178:179], off
	v_lshl_add_u64 v[178:179], s[42:43], 0, v[166:167]
	s_mov_b32 m0, s82
	s_nop 0
	global_load_lds_dwordx4 v[178:179], off
	v_lshl_add_u64 v[178:179], s[40:41], 0, v[160:161]
	v_lshl_add_u64 v[180:181], v[178:179], 0, s[12:13]
	s_mov_b32 m0, s54
	s_nop 0
	global_load_lds_dwordx4 v[180:181], off
	v_lshl_add_u64 v[180:181], s[40:41], 0, v[164:165]
	v_lshl_add_u64 v[220:221], v[180:181], 0, s[12:13]
	s_mov_b32 m0, s55
	s_nop 0
	global_load_lds_dwordx4 v[220:221], off
	s_waitcnt vmcnt(8)
	s_waitcnt lgkmcnt(0)
	s_barrier
	s_waitcnt lgkmcnt(0)
	v_mfma_f32_16x16x128_f8f6f4 v[92:95], v[16:23], v[188:195], 0
	v_mfma_f32_16x16x128_f8f6f4 v[88:91], v[24:31], v[188:195], 0
	v_mfma_f32_16x16x128_f8f6f4 v[84:87], v[16:23], v[196:203], 0
	v_mfma_f32_16x16x128_f8f6f4 v[80:83], v[24:31], v[196:203], 0
	v_mfma_f32_16x16x128_f8f6f4 v[76:79], v[16:23], v[204:211], 0
	v_mfma_f32_16x16x128_f8f6f4 v[72:75], v[24:31], v[204:211], 0
	v_mfma_f32_16x16x128_f8f6f4 v[68:71], v[16:23], v[212:219], 0
	v_mfma_f32_16x16x128_f8f6f4 v[64:67], v[24:31], v[212:219], 0
	v_mfma_f32_16x16x128_f8f6f4 v[60:63], v[0:7], v[188:195], 0
	v_mfma_f32_16x16x128_f8f6f4 v[56:59], v[8:15], v[188:195], 0
	v_mfma_f32_16x16x128_f8f6f4 v[52:55], v[0:7], v[196:203], 0
	v_mfma_f32_16x16x128_f8f6f4 v[48:51], v[8:15], v[196:203], 0
	v_mfma_f32_16x16x128_f8f6f4 v[44:47], v[0:7], v[204:211], 0
	v_mfma_f32_16x16x128_f8f6f4 v[40:43], v[8:15], v[204:211], 0
	v_mfma_f32_16x16x128_f8f6f4 v[36:39], v[0:7], v[212:219], 0
	v_mfma_f32_16x16x128_f8f6f4 v[32:35], v[8:15], v[212:219], 0
	s_barrier
	s_add_i32 s83, 0, 0x18000
	s_add_i32 s85, 0, 0x1c000
	v_add_u32_e32 v188, s83, v183
	v_add_u32_e32 v189, s85, v183
	ds_read_b128 v[16:19], v188
	ds_read_b128 v[20:23], v188 offset:1024
	ds_read_b128 v[24:27], v188 offset:2048
	ds_read_b128 v[28:31], v188 offset:3072
	ds_read_b128 v[0:3], v189
	ds_read_b128 v[4:7], v189 offset:1024
	ds_read_b128 v[8:11], v189 offset:2048
	ds_read_b128 v[12:15], v189 offset:3072
	s_add_u32 s42, s40, 0x20100
	s_addc_u32 s43, s41, 0
	s_mov_b32 m0, s56
	v_lshl_add_u64 v[222:223], s[42:43], 0, v[160:161]
	ds_read_b128 v[190:193], v185 offset:32768
	ds_read_b128 v[194:197], v185 offset:33792
	ds_read_b128 v[198:201], v185 offset:34816
	ds_read_b128 v[202:205], v185 offset:35840
	ds_read_b128 v[206:209], v185 offset:36864
	ds_read_b128 v[210:213], v185 offset:37888
	ds_read_b128 v[214:217], v185 offset:38912
	ds_read_b128 v[218:221], v185 offset:39936
	global_load_lds_dwordx4 v[222:223], off
	v_lshl_add_u64 v[222:223], s[42:43], 0, v[164:165]
	s_mov_b32 m0, s57
	s_nop 0
	global_load_lds_dwordx4 v[222:223], off
	s_waitcnt vmcnt(8)
	s_waitcnt lgkmcnt(0)
	s_barrier
; #define PG8_STAGE(bufoff, gbase, voff) do { _Pragma("unroll") for (int _i = 0; _i < 2; ++_i) \
;         __builtin_amdgcn_global_load_lds((const unsigned*)((const char*)(gbase) + (voff)[_i]), (PG8_LAS unsigned*)(lds + (bufoff) + ldsw + _i * 8192), 16, 0, 0); } while (0)
; #define PG8_WAIT_V(n) asm volatile("s_waitcnt vmcnt(" #n ")" ::: "memory")
; #define PG8_WAIT_L(n) asm volatile("s_waitcnt lgkmcnt(" #n ")" ::: "memory")
; #define PG8_BAR __builtin_amdgcn_s_barrier()
; #define PG8_SCHED __builtin_amdgcn_sched_barrier(0)
; template <class Epi, class Sched, bool ALIGN_EPI = false, bool SP2 = false, bool FP8 = false, bool PEEL = false>
; __device__ __forceinline__ void gemm_phase(PG8_LAS unsigned char* lds, const Gemm g, const Sched& S, const Epi& E, const int wid) {
;     ...
;             PG8_WAIT_V(8); PG8_WAIT_L(0); PG8_BAR; PG8_MMA(0, 0, At, B0); PG8_MMA(0, 1, At, B1); PG8_BAR; PG8_SCHED;
;             PG8_LDA(At, 1, 1); PG8_STAGE(PG8_SB(1, 0), b3, voffB); PG8_STAGE(PG8_SB(1, 1), b3 + hstep, voffB); PG8_STAGE(PG8_SA(1, 0), a3, voffA);
;             PG8_WAIT_V(8); PG8_WAIT_L(0); PG8_BAR; PG8_MMA(1, 0, At, B0); PG8_MMA(1, 1, At, B1); PG8_BAR; PG8_SCHED;
;         }
; #pragma unroll 1
;         for (int t = 2; t < nt; t += 2) {
;             const bool last = (t == nt - 2);
;             const char* a1 = cA + (size_t)(t + 1) * kstep;
;             const char* a2 = last ? nA : cA + (size_t)(t + 2) * kstep; const char* b2 = last ? nB : cB + (size_t)(t + 2) * kstep;
;             const char* a3 = a2 + kstep; const char* b3 = b2 + kstep;
;             if (last && has_next) S.a_ready(nxt);
;             PG8_LDB(B0, 0, 0); PG8_LDB(B1, 0, 1); PG8_SCHED; PG8_LDA(At, 0, 0); PG8_STAGE(PG8_SA(1, 1), a1 + hstep, voffA);
;             PG8_WAIT_V(8); PG8_WAIT_L(0); PG8_BAR; PG8_MMA(0, 0, At, B0); PG8_MMA(0, 1, At, B1); PG8_BAR; PG8_SCHED;
	s_waitcnt lgkmcnt(0)
	v_mfma_f32_16x16x128_f8f6f4 v[156:159], v[16:23], v[190:197], v[156:159]
	v_mfma_f32_16x16x128_f8f6f4 v[152:155], v[24:31], v[190:197], v[152:155]
	v_mfma_f32_16x16x128_f8f6f4 v[148:151], v[16:23], v[198:205], v[148:151]
	v_mfma_f32_16x16x128_f8f6f4 v[144:147], v[24:31], v[198:205], v[144:147]
	v_mfma_f32_16x16x128_f8f6f4 v[140:143], v[16:23], v[206:213], v[140:143]
	v_mfma_f32_16x16x128_f8f6f4 v[136:139], v[24:31], v[206:213], v[136:139]
	v_mfma_f32_16x16x128_f8f6f4 v[132:135], v[16:23], v[214:221], v[132:135]
	v_mfma_f32_16x16x128_f8f6f4 v[128:131], v[24:31], v[214:221], v[128:131]
	v_mfma_f32_16x16x128_f8f6f4 v[124:127], v[0:7], v[190:197], v[124:127]
	v_mfma_f32_16x16x128_f8f6f4 v[120:123], v[8:15], v[190:197], v[120:123]
	v_mfma_f32_16x16x128_f8f6f4 v[116:119], v[0:7], v[198:205], v[116:119]
	v_mfma_f32_16x16x128_f8f6f4 v[112:115], v[8:15], v[198:205], v[112:115]
	v_mfma_f32_16x16x128_f8f6f4 v[108:111], v[0:7], v[206:213], v[108:111]
	v_mfma_f32_16x16x128_f8f6f4 v[104:107], v[8:15], v[206:213], v[104:107]
	v_mfma_f32_16x16x128_f8f6f4 v[100:103], v[0:7], v[214:221], v[100:103]
	v_mfma_f32_16x16x128_f8f6f4 v[96:99], v[8:15], v[214:221], v[96:99]
	s_barrier
	s_add_i32 s83, s83, s49
	s_add_i32 s84, s83, 0x2000
	v_lshl_add_u64 v[174:175], v[174:175], 0, s[14:15]
	s_mov_b32 m0, s83
	s_add_u32 s42, s38, 0x20180
	ds_read_b128 v[190:193], v185 offset:49152
	ds_read_b128 v[194:197], v185 offset:50176
	ds_read_b128 v[198:201], v185 offset:51200
	ds_read_b128 v[202:205], v185 offset:52224
	ds_read_b128 v[206:209], v185 offset:53248
	ds_read_b128 v[210:213], v185 offset:54272
	ds_read_b128 v[214:217], v185 offset:55296
	ds_read_b128 v[218:221], v185 offset:56320
	global_load_lds_dwordx4 v[174:175], off
	v_lshl_add_u64 v[174:175], v[176:177], 0, s[14:15]
	s_mov_b32 m0, s84
	s_addc_u32 s43, s39, 0
	s_add_i32 s85, s85, s49
	global_load_lds_dwordx4 v[174:175], off
	v_lshl_add_u64 v[174:175], s[42:43], 0, v[162:163]
	s_mov_b32 m0, s85
	s_add_i32 s86, s85, 0x2000
	global_load_lds_dwordx4 v[174:175], off
	v_lshl_add_u64 v[174:175], s[42:43], 0, v[166:167]
	s_mov_b32 m0, s86
	s_nop 0
	global_load_lds_dwordx4 v[174:175], off
	v_lshl_add_u64 v[174:175], v[178:179], 0, s[14:15]
	s_mov_b32 m0, s60
	s_nop 0
	global_load_lds_dwordx4 v[174:175], off
	v_lshl_add_u64 v[174:175], v[180:181], 0, s[14:15]
	s_mov_b32 m0, s61
	s_nop 0
	global_load_lds_dwordx4 v[174:175], off
	s_waitcnt vmcnt(8)
	s_waitcnt lgkmcnt(0)
	s_barrier
	s_waitcnt lgkmcnt(0)
	v_mfma_f32_16x16x128_f8f6f4 v[92:95], v[16:23], v[190:197], v[92:95]
	v_mfma_f32_16x16x128_f8f6f4 v[88:91], v[24:31], v[190:197], v[88:91]
	v_mfma_f32_16x16x128_f8f6f4 v[84:87], v[16:23], v[198:205], v[84:87]
	v_mfma_f32_16x16x128_f8f6f4 v[80:83], v[24:31], v[198:205], v[80:83]
	v_mfma_f32_16x16x128_f8f6f4 v[76:79], v[16:23], v[206:213], v[76:79]
	v_mfma_f32_16x16x128_f8f6f4 v[72:75], v[24:31], v[206:213], v[72:75]
	v_mfma_f32_16x16x128_f8f6f4 v[68:71], v[16:23], v[214:221], v[68:71]
	v_mfma_f32_16x16x128_f8f6f4 v[64:67], v[24:31], v[214:221], v[64:67]
	v_mfma_f32_16x16x128_f8f6f4 v[60:63], v[0:7], v[190:197], v[60:63]
	v_mfma_f32_16x16x128_f8f6f4 v[56:59], v[8:15], v[190:197], v[56:59]
	v_mfma_f32_16x16x128_f8f6f4 v[52:55], v[0:7], v[198:205], v[52:55]
	v_mfma_f32_16x16x128_f8f6f4 v[48:51], v[8:15], v[198:205], v[48:51]
	v_mfma_f32_16x16x128_f8f6f4 v[44:47], v[0:7], v[206:213], v[44:47]
	v_mfma_f32_16x16x128_f8f6f4 v[40:43], v[8:15], v[206:213], v[40:43]
	v_mfma_f32_16x16x128_f8f6f4 v[36:39], v[0:7], v[214:221], v[36:39]
	v_mfma_f32_16x16x128_f8f6f4 v[32:35], v[8:15], v[214:221], v[32:35]
	s_barrier
	s_add_u32 s40, s40, 0x20180
	s_addc_u32 s41, s41, 0
	s_add_u32 s87, s38, 0x200
	s_addc_u32 s88, s39, 0
	s_mov_b32 s89, 0
.LBB0_1761:
	ds_read_b128 v[0:3], v186
	ds_read_b128 v[4:7], v186 offset:1024
	ds_read_b128 v[16:19], v186 offset:2048
	ds_read_b128 v[20:23], v186 offset:3072
	ds_read_b128 v[24:27], v187
	ds_read_b128 v[28:31], v187 offset:1024
	ds_read_b128 v[174:177], v187 offset:2048
	ds_read_b128 v[178:181], v187 offset:3072
	s_add_u32 s38, s40, 0xfffe0080
	s_addc_u32 s39, s41, -1
	s_cmp_eq_u32 s89, 4
	s_cselect_b32 s43, s25, s39
	s_cselect_b32 s42, s27, s38
	s_cselect_b32 s39, s75, s88
	s_cselect_b32 s38, s76, s87
	s_mov_b32 m0, s77
	v_lshl_add_u64 v[214:215], s[40:41], 0, v[168:169]
	ds_read_b128 v[8:11], v185
	ds_read_b128 v[12:15], v185 offset:1024
	ds_read_b128 v[190:193], v185 offset:2048
	ds_read_b128 v[194:197], v185 offset:3072
	ds_read_b128 v[198:201], v185 offset:4096
	ds_read_b128 v[202:205], v185 offset:5120
	ds_read_b128 v[206:209], v185 offset:6144
	ds_read_b128 v[210:213], v185 offset:7168
	global_load_lds_dwordx4 v[214:215], off
	v_lshl_add_u64 v[214:215], s[40:41], 0, v[170:171]
	s_mov_b32 m0, s78
	s_nop 0
	global_load_lds_dwordx4 v[214:215], off
	s_waitcnt vmcnt(8)
	s_waitcnt lgkmcnt(0)
	s_barrier
	s_waitcnt lgkmcnt(0)
	v_mfma_f32_16x16x128_f8f6f4 v[156:159], v[0:7], v[8:15], v[156:159]
	v_mfma_f32_16x16x128_f8f6f4 v[152:155], v[16:23], v[8:15], v[152:155]
	v_mfma_f32_16x16x128_f8f6f4 v[148:151], v[0:7], v[190:197], v[148:151]
	v_mfma_f32_16x16x128_f8f6f4 v[144:147], v[16:23], v[190:197], v[144:147]
	v_mfma_f32_16x16x128_f8f6f4 v[140:143], v[0:7], v[198:205], v[140:143]
	v_mfma_f32_16x16x128_f8f6f4 v[136:139], v[16:23], v[198:205], v[136:139]
	v_mfma_f32_16x16x128_f8f6f4 v[132:135], v[0:7], v[206:213], v[132:135]
	v_mfma_f32_16x16x128_f8f6f4 v[128:131], v[16:23], v[206:213], v[128:131]
	v_mfma_f32_16x16x128_f8f6f4 v[124:127], v[24:31], v[8:15], v[124:127]
	v_mfma_f32_16x16x128_f8f6f4 v[120:123], v[174:181], v[8:15], v[120:123]
	v_mfma_f32_16x16x128_f8f6f4 v[116:119], v[24:31], v[190:197], v[116:119]
	v_mfma_f32_16x16x128_f8f6f4 v[112:115], v[174:181], v[190:197], v[112:115]
	v_mfma_f32_16x16x128_f8f6f4 v[108:111], v[24:31], v[198:205], v[108:111]
	v_mfma_f32_16x16x128_f8f6f4 v[104:107], v[174:181], v[198:205], v[104:107]
	v_mfma_f32_16x16x128_f8f6f4 v[100:103], v[24:31], v[206:213], v[100:103]
	v_mfma_f32_16x16x128_f8f6f4 v[96:99], v[174:181], v[206:213], v[96:99]
	s_barrier
; #define PG8_STAGE(bufoff, gbase, voff) do { _Pragma("unroll") for (int _i = 0; _i < 2; ++_i) \
;         __builtin_amdgcn_global_load_lds((const unsigned*)((const char*)(gbase) + (voff)[_i]), (PG8_LAS unsigned*)(lds + (bufoff) + ldsw + _i * 8192), 16, 0, 0); } while (0)
; #define PG8_WAIT_V(n) asm volatile("s_waitcnt vmcnt(" #n ")" ::: "memory")
; #define PG8_WAIT_L(n) asm volatile("s_waitcnt lgkmcnt(" #n ")" ::: "memory")
; #define PG8_BAR __builtin_amdgcn_s_barrier()
; #define PG8_SCHED __builtin_amdgcn_sched_barrier(0)
; template <class Epi, class Sched, bool ALIGN_EPI = false, bool SP2 = false, bool FP8 = false, bool PEEL = false>
; __device__ __forceinline__ void gemm_phase(PG8_LAS unsigned char* lds, const Gemm g, const Sched& S, const Epi& E, const int wid) {
;     ...
;             PG8_LDA(At, 0, 1); PG8_STAGE(PG8_SB(0, 0), b2, voffB); PG8_STAGE(PG8_SB(0, 1), b2 + hstep, voffB); PG8_STAGE(PG8_SA(0, 0), a2, voffA);
;             PG8_WAIT_V(8); PG8_WAIT_L(0); PG8_BAR; PG8_MMA(1, 0, At, B0); PG8_MMA(1, 1, At, B1); PG8_BAR; PG8_SCHED;
;             PG8_LDB(B0, 1, 0); PG8_LDB(B1, 1, 1); PG8_SCHED; PG8_LDA(At, 1, 0); PG8_STAGE(PG8_SA(0, 1), a2 + hstep, voffA);
;             PG8_WAIT_V(8); PG8_WAIT_L(0); PG8_BAR; PG8_MMA(0, 0, At, B0); PG8_MMA(0, 1, At, B1); PG8_BAR; PG8_SCHED;
	s_mov_b32 m0, s79
	v_lshl_add_u64 v[8:9], s[38:39], 0, v[162:163]
	s_add_u32 s90, s38, 0x20000
	ds_read_b128 v[190:193], v185 offset:16384
	ds_read_b128 v[194:197], v185 offset:17408
	ds_read_b128 v[198:201], v185 offset:18432
	ds_read_b128 v[202:205], v185 offset:19456
	ds_read_b128 v[206:209], v185 offset:20480
	ds_read_b128 v[210:213], v185 offset:21504
	ds_read_b128 v[214:217], v185 offset:22528
	ds_read_b128 v[218:221], v185 offset:23552
	global_load_lds_dwordx4 v[8:9], off
	v_lshl_add_u64 v[10:11], s[38:39], 0, v[166:167]
	s_mov_b32 m0, s80
	s_addc_u32 s91, s39, 0
	global_load_lds_dwordx4 v[10:11], off
	v_lshl_add_u64 v[12:13], s[90:91], 0, v[162:163]
	s_mov_b32 m0, s81
	v_lshl_add_u64 v[14:15], s[42:43], 0, v[164:165]
	global_load_lds_dwordx4 v[12:13], off
	v_lshl_add_u64 v[12:13], s[90:91], 0, v[166:167]
	s_mov_b32 m0, s82
	s_nop 0
	global_load_lds_dwordx4 v[12:13], off
	v_lshl_add_u64 v[12:13], s[42:43], 0, v[160:161]
	s_mov_b32 m0, s54
	s_nop 0
	global_load_lds_dwordx4 v[12:13], off
	s_mov_b32 m0, s55
	s_nop 0
	global_load_lds_dwordx4 v[14:15], off
	s_waitcnt vmcnt(8)
	s_waitcnt lgkmcnt(0)
	s_barrier
	s_waitcnt lgkmcnt(0)
	v_mfma_f32_16x16x128_f8f6f4 v[92:95], v[0:7], v[190:197], v[92:95]
	v_mfma_f32_16x16x128_f8f6f4 v[88:91], v[16:23], v[190:197], v[88:91]
	v_mfma_f32_16x16x128_f8f6f4 v[84:87], v[0:7], v[198:205], v[84:87]
	v_mfma_f32_16x16x128_f8f6f4 v[80:83], v[16:23], v[198:205], v[80:83]
	v_mfma_f32_16x16x128_f8f6f4 v[76:79], v[0:7], v[206:213], v[76:79]
	v_mfma_f32_16x16x128_f8f6f4 v[72:75], v[16:23], v[206:213], v[72:75]
	v_mfma_f32_16x16x128_f8f6f4 v[68:71], v[0:7], v[214:221], v[68:71]
	v_mfma_f32_16x16x128_f8f6f4 v[64:67], v[16:23], v[214:221], v[64:67]
	v_mfma_f32_16x16x128_f8f6f4 v[60:63], v[24:31], v[190:197], v[60:63]
	v_mfma_f32_16x16x128_f8f6f4 v[56:59], v[174:181], v[190:197], v[56:59]
	v_mfma_f32_16x16x128_f8f6f4 v[52:55], v[24:31], v[198:205], v[52:55]
	v_mfma_f32_16x16x128_f8f6f4 v[48:51], v[174:181], v[198:205], v[48:51]
	v_mfma_f32_16x16x128_f8f6f4 v[44:47], v[24:31], v[206:213], v[44:47]
	v_mfma_f32_16x16x128_f8f6f4 v[40:43], v[174:181], v[206:213], v[40:43]
	v_mfma_f32_16x16x128_f8f6f4 v[36:39], v[24:31], v[214:221], v[36:39]
	v_mfma_f32_16x16x128_f8f6f4 v[32:35], v[174:181], v[214:221], v[32:35]
	s_barrier
	ds_read_b128 v[16:19], v188
	ds_read_b128 v[20:23], v188 offset:1024
	ds_read_b128 v[24:27], v188 offset:2048
	ds_read_b128 v[28:31], v188 offset:3072
	ds_read_b128 v[0:3], v189
	ds_read_b128 v[4:7], v189 offset:1024
	ds_read_b128 v[174:177], v189 offset:2048
	ds_read_b128 v[178:181], v189 offset:3072
	s_add_u32 s42, s42, 0x20000
	s_addc_u32 s43, s43, 0
	s_mov_b32 m0, s56
	v_lshl_add_u64 v[222:223], s[42:43], 0, v[160:161]
	ds_read_b128 v[190:193], v185 offset:32768
	ds_read_b128 v[194:197], v185 offset:33792
	ds_read_b128 v[198:201], v185 offset:34816
	ds_read_b128 v[202:205], v185 offset:35840
	ds_read_b128 v[206:209], v185 offset:36864
	ds_read_b128 v[210:213], v185 offset:37888
	ds_read_b128 v[214:217], v185 offset:38912
	ds_read_b128 v[218:221], v185 offset:39936
	global_load_lds_dwordx4 v[222:223], off
	v_lshl_add_u64 v[222:223], s[42:43], 0, v[164:165]
	s_mov_b32 m0, s57
	s_nop 0
	global_load_lds_dwordx4 v[222:223], off
	s_waitcnt vmcnt(8)
	s_waitcnt lgkmcnt(0)
	s_barrier
; #define PG8_STAGE(bufoff, gbase, voff) do { _Pragma("unroll") for (int _i = 0; _i < 2; ++_i) \
;         __builtin_amdgcn_global_load_lds((const unsigned*)((const char*)(gbase) + (voff)[_i]), (PG8_LAS unsigned*)(lds + (bufoff) + ldsw + _i * 8192), 16, 0, 0); } while (0)
; #define PG8_WAIT_V(n) asm volatile("s_waitcnt vmcnt(" #n ")" ::: "memory")
; #define PG8_WAIT_L(n) asm volatile("s_waitcnt lgkmcnt(" #n ")" ::: "memory")
; #define PG8_BAR __builtin_amdgcn_s_barrier()
; #define PG8_SCHED __builtin_amdgcn_sched_barrier(0)
; template <class Epi, class Sched, bool ALIGN_EPI = false, bool SP2 = false, bool FP8 = false, bool PEEL = false>
; __device__ __forceinline__ void gemm_phase(PG8_LAS unsigned char* lds, const Gemm g, const Sched& S, const Epi& E, const int wid) {
;     ...
;             PG8_WAIT_V(8); PG8_WAIT_L(0); PG8_BAR; PG8_MMA(0, 0, At, B0); PG8_MMA(0, 1, At, B1); PG8_BAR; PG8_SCHED;
;             PG8_LDA(At, 1, 1); PG8_STAGE(PG8_SB(1, 0), b3, voffB); PG8_STAGE(PG8_SB(1, 1), b3 + hstep, voffB); PG8_STAGE(PG8_SA(1, 0), a3, voffA);
;             PG8_WAIT_V(8); PG8_WAIT_L(0); PG8_BAR; PG8_MMA(1, 0, At, B0); PG8_MMA(1, 1, At, B1); PG8_BAR; PG8_SCHED;
;         }
	s_waitcnt lgkmcnt(0)
	v_mfma_f32_16x16x128_f8f6f4 v[156:159], v[16:23], v[190:197], v[156:159]
	v_mfma_f32_16x16x128_f8f6f4 v[152:155], v[24:31], v[190:197], v[152:155]
	v_mfma_f32_16x16x128_f8f6f4 v[148:151], v[16:23], v[198:205], v[148:151]
	v_mfma_f32_16x16x128_f8f6f4 v[144:147], v[24:31], v[198:205], v[144:147]
	v_mfma_f32_16x16x128_f8f6f4 v[140:143], v[16:23], v[206:213], v[140:143]
	v_mfma_f32_16x16x128_f8f6f4 v[136:139], v[24:31], v[206:213], v[136:139]
	v_mfma_f32_16x16x128_f8f6f4 v[132:135], v[16:23], v[214:221], v[132:135]
	v_mfma_f32_16x16x128_f8f6f4 v[128:131], v[24:31], v[214:221], v[128:131]
	v_mfma_f32_16x16x128_f8f6f4 v[124:127], v[0:7], v[190:197], v[124:127]
	v_mfma_f32_16x16x128_f8f6f4 v[120:123], v[174:181], v[190:197], v[120:123]
	v_mfma_f32_16x16x128_f8f6f4 v[116:119], v[0:7], v[198:205], v[116:119]
	v_mfma_f32_16x16x128_f8f6f4 v[112:115], v[174:181], v[198:205], v[112:115]
	v_mfma_f32_16x16x128_f8f6f4 v[108:111], v[0:7], v[206:213], v[108:111]
	v_mfma_f32_16x16x128_f8f6f4 v[104:107], v[174:181], v[206:213], v[104:107]
	v_mfma_f32_16x16x128_f8f6f4 v[100:103], v[0:7], v[214:221], v[100:103]
	v_mfma_f32_16x16x128_f8f6f4 v[96:99], v[174:181], v[214:221], v[96:99]
	s_barrier
	s_mov_b32 m0, s83
	v_lshl_add_u64 v[8:9], v[8:9], 0, s[10:11]
	s_add_u32 s38, s38, 0x20080
	ds_read_b128 v[190:193], v185 offset:49152
	ds_read_b128 v[194:197], v185 offset:50176
	ds_read_b128 v[198:201], v185 offset:51200
	ds_read_b128 v[202:205], v185 offset:52224
	ds_read_b128 v[206:209], v185 offset:53248
	ds_read_b128 v[210:213], v185 offset:54272
	ds_read_b128 v[214:217], v185 offset:55296
	ds_read_b128 v[218:221], v185 offset:56320
	global_load_lds_dwordx4 v[8:9], off
	v_lshl_add_u64 v[8:9], v[10:11], 0, s[10:11]
	s_mov_b32 m0, s84
	s_addc_u32 s39, s39, 0
	global_load_lds_dwordx4 v[8:9], off
	v_lshl_add_u64 v[8:9], s[38:39], 0, v[162:163]
	s_mov_b32 m0, s85
	s_nop 0
	global_load_lds_dwordx4 v[8:9], off
	v_lshl_add_u64 v[8:9], s[38:39], 0, v[166:167]
	s_mov_b32 m0, s86
	s_nop 0
	global_load_lds_dwordx4 v[8:9], off
	v_lshl_add_u64 v[8:9], v[12:13], 0, s[10:11]
	s_mov_b32 m0, s60
	s_nop 0
	global_load_lds_dwordx4 v[8:9], off
	v_lshl_add_u64 v[8:9], v[14:15], 0, s[10:11]
	s_mov_b32 m0, s61
	s_nop 0
	global_load_lds_dwordx4 v[8:9], off
	s_waitcnt vmcnt(8)
	s_waitcnt lgkmcnt(0)
	s_barrier
	s_waitcnt lgkmcnt(0)
	v_mfma_f32_16x16x128_f8f6f4 v[92:95], v[16:23], v[190:197], v[92:95]
	v_mfma_f32_16x16x128_f8f6f4 v[88:91], v[24:31], v[190:197], v[88:91]
	v_mfma_f32_16x16x128_f8f6f4 v[84:87], v[16:23], v[198:205], v[84:87]
	v_mfma_f32_16x16x128_f8f6f4 v[80:83], v[24:31], v[198:205], v[80:83]
	v_mfma_f32_16x16x128_f8f6f4 v[76:79], v[16:23], v[206:213], v[76:79]
	v_mfma_f32_16x16x128_f8f6f4 v[72:75], v[24:31], v[206:213], v[72:75]
	v_mfma_f32_16x16x128_f8f6f4 v[68:71], v[16:23], v[214:221], v[68:71]
	v_mfma_f32_16x16x128_f8f6f4 v[64:67], v[24:31], v[214:221], v[64:67]
	v_mfma_f32_16x16x128_f8f6f4 v[60:63], v[0:7], v[190:197], v[60:63]
	v_mfma_f32_16x16x128_f8f6f4 v[56:59], v[174:181], v[190:197], v[56:59]
	v_mfma_f32_16x16x128_f8f6f4 v[52:55], v[0:7], v[198:205], v[52:55]
	v_mfma_f32_16x16x128_f8f6f4 v[48:51], v[174:181], v[198:205], v[48:51]
	v_mfma_f32_16x16x128_f8f6f4 v[44:47], v[0:7], v[206:213], v[44:47]
	v_mfma_f32_16x16x128_f8f6f4 v[40:43], v[174:181], v[206:213], v[40:43]
	v_mfma_f32_16x16x128_f8f6f4 v[36:39], v[0:7], v[214:221], v[36:39]
	v_mfma_f32_16x16x128_f8f6f4 v[32:35], v[174:181], v[214:221], v[32:35]
	s_barrier
	s_add_i32 s89, s89, 2
	s_add_u32 s40, s40, 0x100
	s_addc_u32 s41, s41, 0
	s_add_u32 s87, s87, 0x100
	s_addc_u32 s88, s88, 0
	s_cmp_gt_u32 s89, 5
	s_cbranch_scc0 .LBB0_1761
	v_readlane_b32 s76, v254, 57
	s_and_b64 vcc, exec, s[8:9]
	v_readlane_b32 s77, v254, 58
	v_readlane_b32 s78, v254, 59
	v_readlane_b32 s79, v254, 60
	v_readlane_b32 s80, v254, 61
	v_readlane_b32 s81, v254, 62
	v_readlane_b32 s82, v254, 63
	v_readlane_b32 s83, v255, 0
	s_cbranch_vccz .LBB0_1764
	s_barrier

; #define PG8_STAGE(bufoff, gbase, voff) do { _Pragma("unroll") for (int _i = 0; _i < 2; ++_i) \
;         __builtin_amdgcn_global_load_lds((const unsigned*)((const char*)(gbase) + (voff)[_i]), (PG8_LAS unsigned*)(lds + (bufoff) + ldsw + _i * 8192), 16, 0, 0); } while (0)
; #define PG8_WAIT_V(n) asm volatile("s_waitcnt vmcnt(" #n ")" ::: "memory")
; #define PG8_WAIT_L(n) asm volatile("s_waitcnt lgkmcnt(" #n ")" ::: "memory")
; #define PG8_BAR __builtin_amdgcn_s_barrier()
; #define PG8_SCHED __builtin_amdgcn_sched_barrier(0)
; template <class Epi, class Sched, bool ALIGN_EPI = false, bool SP2 = false, bool FP8 = false, bool PEEL = false>
; __device__ __forceinline__ void gemm_phase(PG8_LAS unsigned char* lds, const Gemm g, const Sched& S, const Epi& E, const int wid) {
;     ...
;         {
;             const int t = 0;
;             const bool last = (t == nt - 2);
;             const char* a1 = cA + (size_t)(t + 1) * kstep;
;             const char* a2 = last ? nA : cA + (size_t)(t + 2) * kstep; const char* b2 = last ? nB : cB + (size_t)(t + 2) * kstep;
;             const char* a3 = a2 + kstep; const char* b3 = b2 + kstep;
;             if (last && has_next) S.a_ready(nxt);
;             PG8_LDB(B0, 0, 0); PG8_LDB(B1, 0, 1); PG8_SCHED; PG8_LDA(At, 0, 0); PG8_STAGE(PG8_SA(1, 1), a1 + hstep, voffA);
;             PG8_WAIT_V(8); PG8_WAIT_L(0); PG8_BAR; PG8_MMAZ(0, 0, At, B0); PG8_MMAZ(0, 1, At, B1); PG8_BAR; PG8_SCHED;
;             PG8_LDA(At, 0, 1); PG8_STAGE(PG8_SB(0, 0), b2, voffB); PG8_STAGE(PG8_SB(0, 1), b2 + hstep, voffB); PG8_STAGE(PG8_SA(0, 0), a2, voffA);
;             PG8_WAIT_V(8); PG8_WAIT_L(0); PG8_BAR; PG8_MMAZ(1, 0, At, B0); PG8_MMAZ(1, 1, At, B1); PG8_BAR; PG8_SCHED;
;             PG8_LDB(B0, 1, 0); PG8_LDB(B1, 1, 1); PG8_SCHED; PG8_LDA(At, 1, 0); PG8_STAGE(PG8_SA(0, 1), a2 + hstep, voffA);
.LBB0_1852:
	v_add_u32_e32 v187, s65, v185
	v_add_u32_e32 v188, s66, v185
	ds_read_b128 v[16:19], v187
	ds_read_b128 v[20:23], v187 offset:1024
	ds_read_b128 v[24:27], v187 offset:2048
	ds_read_b128 v[28:31], v187 offset:3072
	ds_read_b128 v[0:3], v188
	ds_read_b128 v[4:7], v188 offset:1024
	ds_read_b128 v[8:11], v188 offset:2048
	ds_read_b128 v[12:15], v188 offset:3072
	s_add_u32 s40, s36, 0x70080
	s_addc_u32 s41, s37, 0
	s_add_i32 s80, s59, 0xc000
	v_lshl_add_u64 v[214:215], s[40:41], 0, v[160:161]
	s_mov_b32 m0, s80
	s_add_i32 s81, s59, 0xe000
	ds_read_b128 v[176:179], v186
	ds_read_b128 v[180:183], v186 offset:1024
	ds_read_b128 v[190:193], v186 offset:2048
	ds_read_b128 v[194:197], v186 offset:3072
	ds_read_b128 v[198:201], v186 offset:4096
	ds_read_b128 v[202:205], v186 offset:5120
	ds_read_b128 v[206:209], v186 offset:6144
	ds_read_b128 v[210:213], v186 offset:7168
	global_load_lds_dwordx4 v[214:215], off
	v_lshl_add_u64 v[214:215], s[40:41], 0, v[164:165]
	s_mov_b32 m0, s81
	s_nop 0
	global_load_lds_dwordx4 v[214:215], off
	s_waitcnt vmcnt(8)
	s_waitcnt lgkmcnt(0)
	s_barrier
	s_waitcnt lgkmcnt(0)
	v_mfma_f32_16x16x128_f8f6f4 v[156:159], v[16:23], v[176:183], 0
	v_mfma_f32_16x16x128_f8f6f4 v[152:155], v[24:31], v[176:183], 0
	v_mfma_f32_16x16x128_f8f6f4 v[148:151], v[16:23], v[190:197], 0
	v_mfma_f32_16x16x128_f8f6f4 v[144:147], v[24:31], v[190:197], 0
	v_mfma_f32_16x16x128_f8f6f4 v[140:143], v[16:23], v[198:205], 0
	v_mfma_f32_16x16x128_f8f6f4 v[136:139], v[24:31], v[198:205], 0
	v_mfma_f32_16x16x128_f8f6f4 v[132:135], v[16:23], v[206:213], 0
	v_mfma_f32_16x16x128_f8f6f4 v[128:131], v[24:31], v[206:213], 0
	v_mfma_f32_16x16x128_f8f6f4 v[124:127], v[0:7], v[176:183], 0
	v_mfma_f32_16x16x128_f8f6f4 v[120:123], v[8:15], v[176:183], 0
	v_mfma_f32_16x16x128_f8f6f4 v[116:119], v[0:7], v[190:197], 0
	v_mfma_f32_16x16x128_f8f6f4 v[112:115], v[8:15], v[190:197], 0
	v_mfma_f32_16x16x128_f8f6f4 v[108:111], v[0:7], v[198:205], 0
	v_mfma_f32_16x16x128_f8f6f4 v[104:107], v[8:15], v[198:205], 0
	v_mfma_f32_16x16x128_f8f6f4 v[100:103], v[0:7], v[206:213], 0
	v_mfma_f32_16x16x128_f8f6f4 v[96:99], v[8:15], v[206:213], 0
	s_barrier
	v_lshl_add_u64 v[176:177], s[38:39], 0, v[162:163]
	s_add_i32 s82, s65, s54
	v_lshl_add_u64 v[178:179], v[176:177], 0, s[24:25]
	s_mov_b32 m0, s82
	s_add_i32 s83, s82, 0x2000
	ds_read_b128 v[190:193], v186 offset:16384
	ds_read_b128 v[194:197], v186 offset:17408
	ds_read_b128 v[198:201], v186 offset:18432
	ds_read_b128 v[202:205], v186 offset:19456
	ds_read_b128 v[206:209], v186 offset:20480
	ds_read_b128 v[210:213], v186 offset:21504
	ds_read_b128 v[214:217], v186 offset:22528
	ds_read_b128 v[218:221], v186 offset:23552
	global_load_lds_dwordx4 v[178:179], off
	v_lshl_add_u64 v[178:179], s[38:39], 0, v[166:167]
	s_add_u32 s40, s38, 0x70100
	v_lshl_add_u64 v[180:181], v[178:179], 0, s[24:25]
	s_mov_b32 m0, s83
	s_addc_u32 s41, s39, 0
	s_add_i32 s84, s66, s54
	global_load_lds_dwordx4 v[180:181], off
	v_lshl_add_u64 v[180:181], s[40:41], 0, v[162:163]
	s_mov_b32 m0, s84
	s_add_i32 s85, s84, 0x2000
	global_load_lds_dwordx4 v[180:181], off
	v_lshl_add_u64 v[180:181], s[40:41], 0, v[166:167]
	s_mov_b32 m0, s85
	s_nop 0
	global_load_lds_dwordx4 v[180:181], off
	v_lshl_add_u64 v[180:181], s[36:37], 0, v[160:161]
	v_lshl_add_u64 v[182:183], v[180:181], 0, s[24:25]
	s_mov_b32 m0, s59
	s_nop 0
	global_load_lds_dwordx4 v[182:183], off
	v_lshl_add_u64 v[182:183], s[36:37], 0, v[164:165]
	v_lshl_add_u64 v[222:223], v[182:183], 0, s[24:25]
	s_mov_b32 m0, s60
	s_nop 0
	global_load_lds_dwordx4 v[222:223], off
	s_waitcnt vmcnt(8)
	s_waitcnt lgkmcnt(0)
	s_barrier
	s_waitcnt lgkmcnt(0)
	v_mfma_f32_16x16x128_f8f6f4 v[92:95], v[16:23], v[190:197], 0
	v_mfma_f32_16x16x128_f8f6f4 v[88:91], v[24:31], v[190:197], 0
	v_mfma_f32_16x16x128_f8f6f4 v[84:87], v[16:23], v[198:205], 0
	v_mfma_f32_16x16x128_f8f6f4 v[80:83], v[24:31], v[198:205], 0
	v_mfma_f32_16x16x128_f8f6f4 v[76:79], v[16:23], v[206:213], 0
	v_mfma_f32_16x16x128_f8f6f4 v[72:75], v[24:31], v[206:213], 0
	v_mfma_f32_16x16x128_f8f6f4 v[68:71], v[16:23], v[214:221], 0
	v_mfma_f32_16x16x128_f8f6f4 v[64:67], v[24:31], v[214:221], 0
	v_mfma_f32_16x16x128_f8f6f4 v[60:63], v[0:7], v[190:197], 0
	v_mfma_f32_16x16x128_f8f6f4 v[56:59], v[8:15], v[190:197], 0
	v_mfma_f32_16x16x128_f8f6f4 v[52:55], v[0:7], v[198:205], 0
	v_mfma_f32_16x16x128_f8f6f4 v[48:51], v[8:15], v[198:205], 0
	v_mfma_f32_16x16x128_f8f6f4 v[44:47], v[0:7], v[206:213], 0
	v_mfma_f32_16x16x128_f8f6f4 v[40:43], v[8:15], v[206:213], 0
	v_mfma_f32_16x16x128_f8f6f4 v[36:39], v[0:7], v[214:221], 0
	v_mfma_f32_16x16x128_f8f6f4 v[32:35], v[8:15], v[214:221], 0
	s_barrier
	s_add_i32 s86, 0, 0x18000
	s_add_i32 s88, 0, 0x1c000
	v_add_u32_e32 v189, s86, v185
	v_add_u32_e32 v190, s88, v185
	ds_read_b128 v[16:19], v189
	ds_read_b128 v[20:23], v189 offset:1024
	ds_read_b128 v[24:27], v189 offset:2048
	ds_read_b128 v[28:31], v189 offset:3072
	ds_read_b128 v[0:3], v190
	ds_read_b128 v[4:7], v190 offset:1024
	ds_read_b128 v[8:11], v190 offset:2048
	ds_read_b128 v[12:15], v190 offset:3072
	s_add_u32 s40, s36, 0x70100
	s_addc_u32 s41, s37, 0
	s_mov_b32 m0, s61
	v_lshl_add_u64 v[224:225], s[40:41], 0, v[160:161]
	ds_read_b128 v[192:195], v186 offset:32768
	ds_read_b128 v[196:199], v186 offset:33792
	ds_read_b128 v[200:203], v186 offset:34816
	ds_read_b128 v[204:207], v186 offset:35840
	ds_read_b128 v[208:211], v186 offset:36864
	ds_read_b128 v[212:215], v186 offset:37888
	ds_read_b128 v[216:219], v186 offset:38912
	ds_read_b128 v[220:223], v186 offset:39936
	global_load_lds_dwordx4 v[224:225], off
	v_lshl_add_u64 v[224:225], s[40:41], 0, v[164:165]
	s_mov_b32 m0, s62
	s_nop 0
	global_load_lds_dwordx4 v[224:225], off
	s_waitcnt vmcnt(8)
	s_waitcnt lgkmcnt(0)
	s_barrier
; #define PG8_STAGE(bufoff, gbase, voff) do { _Pragma("unroll") for (int _i = 0; _i < 2; ++_i) \
;         __builtin_amdgcn_global_load_lds((const unsigned*)((const char*)(gbase) + (voff)[_i]), (PG8_LAS unsigned*)(lds + (bufoff) + ldsw + _i * 8192), 16, 0, 0); } while (0)
; #define PG8_WAIT_V(n) asm volatile("s_waitcnt vmcnt(" #n ")" ::: "memory")
; #define PG8_WAIT_L(n) asm volatile("s_waitcnt lgkmcnt(" #n ")" ::: "memory")
; #define PG8_BAR __builtin_amdgcn_s_barrier()
; #define PG8_SCHED __builtin_amdgcn_sched_barrier(0)
; template <class Epi, class Sched, bool ALIGN_EPI = false, bool SP2 = false, bool FP8 = false, bool PEEL = false>
; __device__ __forceinline__ void gemm_phase(PG8_LAS unsigned char* lds, const Gemm g, const Sched& S, const Epi& E, const int wid) {
;     ...
;             PG8_WAIT_V(8); PG8_WAIT_L(0); PG8_BAR; PG8_MMA(0, 0, At, B0); PG8_MMA(0, 1, At, B1); PG8_BAR; PG8_SCHED;
;             PG8_LDA(At, 1, 1); PG8_STAGE(PG8_SB(1, 0), b3, voffB); PG8_STAGE(PG8_SB(1, 1), b3 + hstep, voffB); PG8_STAGE(PG8_SA(1, 0), a3, voffA);
;             PG8_WAIT_V(8); PG8_WAIT_L(0); PG8_BAR; PG8_MMA(1, 0, At, B0); PG8_MMA(1, 1, At, B1); PG8_BAR; PG8_SCHED;
;         }
; #pragma unroll 1
;         for (int t = 2; t < nt; t += 2) {
;             const bool last = (t == nt - 2);
;             const char* a1 = cA + (size_t)(t + 1) * kstep;
;             const char* a2 = last ? nA : cA + (size_t)(t + 2) * kstep; const char* b2 = last ? nB : cB + (size_t)(t + 2) * kstep;
;             const char* a3 = a2 + kstep; const char* b3 = b2 + kstep;
;             if (last && has_next) S.a_ready(nxt);
;             PG8_LDB(B0, 0, 0); PG8_LDB(B1, 0, 1); PG8_SCHED; PG8_LDA(At, 0, 0); PG8_STAGE(PG8_SA(1, 1), a1 + hstep, voffA);
;             PG8_WAIT_V(8); PG8_WAIT_L(0); PG8_BAR; PG8_MMA(0, 0, At, B0); PG8_MMA(0, 1, At, B1); PG8_BAR; PG8_SCHED;
	s_waitcnt lgkmcnt(0)
	v_mfma_f32_16x16x128_f8f6f4 v[156:159], v[16:23], v[192:199], v[156:159]
	v_mfma_f32_16x16x128_f8f6f4 v[152:155], v[24:31], v[192:199], v[152:155]
	v_mfma_f32_16x16x128_f8f6f4 v[148:151], v[16:23], v[200:207], v[148:151]
	v_mfma_f32_16x16x128_f8f6f4 v[144:147], v[24:31], v[200:207], v[144:147]
	v_mfma_f32_16x16x128_f8f6f4 v[140:143], v[16:23], v[208:215], v[140:143]
	v_mfma_f32_16x16x128_f8f6f4 v[136:139], v[24:31], v[208:215], v[136:139]
	v_mfma_f32_16x16x128_f8f6f4 v[132:135], v[16:23], v[216:223], v[132:135]
	v_mfma_f32_16x16x128_f8f6f4 v[128:131], v[24:31], v[216:223], v[128:131]
	v_mfma_f32_16x16x128_f8f6f4 v[124:127], v[0:7], v[192:199], v[124:127]
	v_mfma_f32_16x16x128_f8f6f4 v[120:123], v[8:15], v[192:199], v[120:123]
	v_mfma_f32_16x16x128_f8f6f4 v[116:119], v[0:7], v[200:207], v[116:119]
	v_mfma_f32_16x16x128_f8f6f4 v[112:115], v[8:15], v[200:207], v[112:115]
	v_mfma_f32_16x16x128_f8f6f4 v[108:111], v[0:7], v[208:215], v[108:111]
	v_mfma_f32_16x16x128_f8f6f4 v[104:107], v[8:15], v[208:215], v[104:107]
	v_mfma_f32_16x16x128_f8f6f4 v[100:103], v[0:7], v[216:223], v[100:103]
	v_mfma_f32_16x16x128_f8f6f4 v[96:99], v[8:15], v[216:223], v[96:99]
	s_barrier
	s_add_i32 s86, s86, s54
	s_add_i32 s87, s86, 0x2000
	v_lshl_add_u64 v[176:177], v[176:177], 0, s[26:27]
	s_mov_b32 m0, s86
	s_add_u32 s40, s38, 0x70180
	ds_read_b128 v[192:195], v186 offset:49152
	ds_read_b128 v[196:199], v186 offset:50176
	ds_read_b128 v[200:203], v186 offset:51200
	ds_read_b128 v[204:207], v186 offset:52224
	ds_read_b128 v[208:211], v186 offset:53248
	ds_read_b128 v[212:215], v186 offset:54272
	ds_read_b128 v[216:219], v186 offset:55296
	ds_read_b128 v[220:223], v186 offset:56320
	global_load_lds_dwordx4 v[176:177], off
	v_lshl_add_u64 v[176:177], v[178:179], 0, s[26:27]
	s_mov_b32 m0, s87
	s_addc_u32 s41, s39, 0
	s_add_i32 s88, s88, s54
	global_load_lds_dwordx4 v[176:177], off
	v_lshl_add_u64 v[176:177], s[40:41], 0, v[162:163]
	s_mov_b32 m0, s88
	s_add_i32 s89, s88, 0x2000
	global_load_lds_dwordx4 v[176:177], off
	v_lshl_add_u64 v[176:177], s[40:41], 0, v[166:167]
	s_mov_b32 m0, s89
	s_nop 0
	global_load_lds_dwordx4 v[176:177], off
	v_lshl_add_u64 v[176:177], v[180:181], 0, s[26:27]
	s_mov_b32 m0, s63
	s_nop 0
	global_load_lds_dwordx4 v[176:177], off
	v_lshl_add_u64 v[176:177], v[182:183], 0, s[26:27]
	s_mov_b32 m0, s64
	s_nop 0
	global_load_lds_dwordx4 v[176:177], off
	s_waitcnt vmcnt(8)
	s_waitcnt lgkmcnt(0)
	s_barrier
	s_waitcnt lgkmcnt(0)
	v_mfma_f32_16x16x128_f8f6f4 v[92:95], v[16:23], v[192:199], v[92:95]
	v_mfma_f32_16x16x128_f8f6f4 v[88:91], v[24:31], v[192:199], v[88:91]
	v_mfma_f32_16x16x128_f8f6f4 v[84:87], v[16:23], v[200:207], v[84:87]
	v_mfma_f32_16x16x128_f8f6f4 v[80:83], v[24:31], v[200:207], v[80:83]
	v_mfma_f32_16x16x128_f8f6f4 v[76:79], v[16:23], v[208:215], v[76:79]
	v_mfma_f32_16x16x128_f8f6f4 v[72:75], v[24:31], v[208:215], v[72:75]
	v_mfma_f32_16x16x128_f8f6f4 v[68:71], v[16:23], v[216:223], v[68:71]
	v_mfma_f32_16x16x128_f8f6f4 v[64:67], v[24:31], v[216:223], v[64:67]
	v_mfma_f32_16x16x128_f8f6f4 v[60:63], v[0:7], v[192:199], v[60:63]
	v_mfma_f32_16x16x128_f8f6f4 v[56:59], v[8:15], v[192:199], v[56:59]
	v_mfma_f32_16x16x128_f8f6f4 v[52:55], v[0:7], v[200:207], v[52:55]
	v_mfma_f32_16x16x128_f8f6f4 v[48:51], v[8:15], v[200:207], v[48:51]
	v_mfma_f32_16x16x128_f8f6f4 v[44:47], v[0:7], v[208:215], v[44:47]
	v_mfma_f32_16x16x128_f8f6f4 v[40:43], v[8:15], v[208:215], v[40:43]
	v_mfma_f32_16x16x128_f8f6f4 v[36:39], v[0:7], v[216:223], v[36:39]
	v_mfma_f32_16x16x128_f8f6f4 v[32:35], v[8:15], v[216:223], v[32:35]
	s_barrier
	s_add_u32 s90, s38, 0x200
	s_addc_u32 s91, s39, 0
	s_mov_b32 s92, 0
.LBB0_1853:
	ds_read_b128 v[0:3], v187
	ds_read_b128 v[4:7], v187 offset:1024
	ds_read_b128 v[16:19], v187 offset:2048
	ds_read_b128 v[20:23], v187 offset:3072
	ds_read_b128 v[24:27], v188
	ds_read_b128 v[28:31], v188 offset:1024
	ds_read_b128 v[176:179], v188 offset:2048
	ds_read_b128 v[180:183], v188 offset:3072
	s_add_u32 s38, s36, 0x200
	s_addc_u32 s39, s37, 0
	s_cmp_eq_u32 s92, 24
	s_cselect_b32 s41, s9, s39
	s_cselect_b32 s40, s8, s38
	s_cselect_b32 s39, s35, s91
	s_cselect_b32 s38, s34, s90
	s_mov_b32 m0, s80
	v_lshl_add_u64 v[216:217], s[36:37], 0, v[170:171]
	ds_read_b128 v[8:11], v186
	ds_read_b128 v[12:15], v186 offset:1024
	ds_read_b128 v[192:195], v186 offset:2048
	ds_read_b128 v[196:199], v186 offset:3072
	ds_read_b128 v[200:203], v186 offset:4096
	ds_read_b128 v[204:207], v186 offset:5120
	ds_read_b128 v[208:211], v186 offset:6144
	ds_read_b128 v[212:215], v186 offset:7168
	global_load_lds_dwordx4 v[216:217], off
	v_lshl_add_u64 v[216:217], s[36:37], 0, v[172:173]
	s_mov_b32 m0, s81
	s_nop 0
	global_load_lds_dwordx4 v[216:217], off
	s_waitcnt vmcnt(8)
	s_waitcnt lgkmcnt(0)
	s_barrier
	s_waitcnt lgkmcnt(0)
	v_mfma_f32_16x16x128_f8f6f4 v[156:159], v[0:7], v[8:15], v[156:159]
	v_mfma_f32_16x16x128_f8f6f4 v[152:155], v[16:23], v[8:15], v[152:155]
	v_mfma_f32_16x16x128_f8f6f4 v[148:151], v[0:7], v[192:199], v[148:151]
	v_mfma_f32_16x16x128_f8f6f4 v[144:147], v[16:23], v[192:199], v[144:147]
	v_mfma_f32_16x16x128_f8f6f4 v[140:143], v[0:7], v[200:207], v[140:143]
	v_mfma_f32_16x16x128_f8f6f4 v[136:139], v[16:23], v[200:207], v[136:139]
	v_mfma_f32_16x16x128_f8f6f4 v[132:135], v[0:7], v[208:215], v[132:135]
	v_mfma_f32_16x16x128_f8f6f4 v[128:131], v[16:23], v[208:215], v[128:131]
	v_mfma_f32_16x16x128_f8f6f4 v[124:127], v[24:31], v[8:15], v[124:127]
	v_mfma_f32_16x16x128_f8f6f4 v[120:123], v[176:183], v[8:15], v[120:123]
	v_mfma_f32_16x16x128_f8f6f4 v[116:119], v[24:31], v[192:199], v[116:119]
	v_mfma_f32_16x16x128_f8f6f4 v[112:115], v[176:183], v[192:199], v[112:115]
	v_mfma_f32_16x16x128_f8f6f4 v[108:111], v[24:31], v[200:207], v[108:111]
	v_mfma_f32_16x16x128_f8f6f4 v[104:107], v[176:183], v[200:207], v[104:107]
	v_mfma_f32_16x16x128_f8f6f4 v[100:103], v[24:31], v[208:215], v[100:103]
	v_mfma_f32_16x16x128_f8f6f4 v[96:99], v[176:183], v[208:215], v[96:99]
	s_barrier
; #define PG8_STAGE(bufoff, gbase, voff) do { _Pragma("unroll") for (int _i = 0; _i < 2; ++_i) \
;         __builtin_amdgcn_global_load_lds((const unsigned*)((const char*)(gbase) + (voff)[_i]), (PG8_LAS unsigned*)(lds + (bufoff) + ldsw + _i * 8192), 16, 0, 0); } while (0)
; #define PG8_WAIT_V(n) asm volatile("s_waitcnt vmcnt(" #n ")" ::: "memory")
; #define PG8_WAIT_L(n) asm volatile("s_waitcnt lgkmcnt(" #n ")" ::: "memory")
; #define PG8_BAR __builtin_amdgcn_s_barrier()
; #define PG8_SCHED __builtin_amdgcn_sched_barrier(0)
; template <class Epi, class Sched, bool ALIGN_EPI = false, bool SP2 = false, bool FP8 = false, bool PEEL = false>
; __device__ __forceinline__ void gemm_phase(PG8_LAS unsigned char* lds, const Gemm g, const Sched& S, const Epi& E, const int wid) {
;     ...
;             PG8_LDA(At, 0, 1); PG8_STAGE(PG8_SB(0, 0), b2, voffB); PG8_STAGE(PG8_SB(0, 1), b2 + hstep, voffB); PG8_STAGE(PG8_SA(0, 0), a2, voffA);
;             PG8_WAIT_V(8); PG8_WAIT_L(0); PG8_BAR; PG8_MMA(1, 0, At, B0); PG8_MMA(1, 1, At, B1); PG8_BAR; PG8_SCHED;
;             PG8_LDB(B0, 1, 0); PG8_LDB(B1, 1, 1); PG8_SCHED; PG8_LDA(At, 1, 0); PG8_STAGE(PG8_SA(0, 1), a2 + hstep, voffA);
;             PG8_WAIT_V(8); PG8_WAIT_L(0); PG8_BAR; PG8_MMA(0, 0, At, B0); PG8_MMA(0, 1, At, B1); PG8_BAR; PG8_SCHED;
;             PG8_LDA(At, 1, 1); PG8_STAGE(PG8_SB(1, 0), b3, voffB); PG8_STAGE(PG8_SB(1, 1), b3 + hstep, voffB); PG8_STAGE(PG8_SA(1, 0), a3, voffA);
;             PG8_WAIT_V(8); PG8_WAIT_L(0); PG8_BAR; PG8_MMA(1, 0, At, B0); PG8_MMA(1, 1, At, B1); PG8_BAR; PG8_SCHED;
;         }
	s_mov_b32 m0, s82
	v_lshl_add_u64 v[8:9], s[38:39], 0, v[162:163]
	s_add_u32 s94, s38, 0x70000
	ds_read_b128 v[192:195], v186 offset:16384
	ds_read_b128 v[196:199], v186 offset:17408
	ds_read_b128 v[200:203], v186 offset:18432
	ds_read_b128 v[204:207], v186 offset:19456
	ds_read_b128 v[208:211], v186 offset:20480
	ds_read_b128 v[212:215], v186 offset:21504
	ds_read_b128 v[216:219], v186 offset:22528
	ds_read_b128 v[220:223], v186 offset:23552
	global_load_lds_dwordx4 v[8:9], off
	v_lshl_add_u64 v[10:11], s[38:39], 0, v[166:167]
	s_mov_b32 m0, s83
	s_addc_u32 s95, s39, 0
	global_load_lds_dwordx4 v[10:11], off
	v_lshl_add_u64 v[12:13], s[94:95], 0, v[162:163]
	s_mov_b32 m0, s84
	v_lshl_add_u64 v[14:15], s[40:41], 0, v[164:165]
	global_load_lds_dwordx4 v[12:13], off
	v_lshl_add_u64 v[12:13], s[94:95], 0, v[166:167]
	s_mov_b32 m0, s85
	s_nop 0
	global_load_lds_dwordx4 v[12:13], off
	v_lshl_add_u64 v[12:13], s[40:41], 0, v[160:161]
	s_mov_b32 m0, s59
	s_nop 0
	global_load_lds_dwordx4 v[12:13], off
	s_mov_b32 m0, s60
	s_nop 0
	global_load_lds_dwordx4 v[14:15], off
	s_waitcnt vmcnt(8)
	s_waitcnt lgkmcnt(0)
	s_barrier
	s_waitcnt lgkmcnt(0)
	v_mfma_f32_16x16x128_f8f6f4 v[92:95], v[0:7], v[192:199], v[92:95]
	v_mfma_f32_16x16x128_f8f6f4 v[88:91], v[16:23], v[192:199], v[88:91]
	v_mfma_f32_16x16x128_f8f6f4 v[84:87], v[0:7], v[200:207], v[84:87]
	v_mfma_f32_16x16x128_f8f6f4 v[80:83], v[16:23], v[200:207], v[80:83]
	v_mfma_f32_16x16x128_f8f6f4 v[76:79], v[0:7], v[208:215], v[76:79]
	v_mfma_f32_16x16x128_f8f6f4 v[72:75], v[16:23], v[208:215], v[72:75]
	v_mfma_f32_16x16x128_f8f6f4 v[68:71], v[0:7], v[216:223], v[68:71]
	v_mfma_f32_16x16x128_f8f6f4 v[64:67], v[16:23], v[216:223], v[64:67]
	v_mfma_f32_16x16x128_f8f6f4 v[60:63], v[24:31], v[192:199], v[60:63]
	v_mfma_f32_16x16x128_f8f6f4 v[56:59], v[176:183], v[192:199], v[56:59]
	v_mfma_f32_16x16x128_f8f6f4 v[52:55], v[24:31], v[200:207], v[52:55]
	v_mfma_f32_16x16x128_f8f6f4 v[48:51], v[176:183], v[200:207], v[48:51]
	v_mfma_f32_16x16x128_f8f6f4 v[44:47], v[24:31], v[208:215], v[44:47]
	v_mfma_f32_16x16x128_f8f6f4 v[40:43], v[176:183], v[208:215], v[40:43]
	v_mfma_f32_16x16x128_f8f6f4 v[36:39], v[24:31], v[216:223], v[36:39]
	v_mfma_f32_16x16x128_f8f6f4 v[32:35], v[176:183], v[216:223], v[32:35]
	s_barrier
	ds_read_b128 v[16:19], v189
	ds_read_b128 v[20:23], v189 offset:1024
	ds_read_b128 v[24:27], v189 offset:2048
	ds_read_b128 v[28:31], v189 offset:3072
	ds_read_b128 v[0:3], v190
	ds_read_b128 v[4:7], v190 offset:1024
	ds_read_b128 v[176:179], v190 offset:2048
	ds_read_b128 v[180:183], v190 offset:3072
	s_add_u32 s40, s40, 0x70000
	s_addc_u32 s41, s41, 0
	s_mov_b32 m0, s61
	v_lshl_add_u64 v[224:225], s[40:41], 0, v[160:161]
	ds_read_b128 v[192:195], v186 offset:32768
	ds_read_b128 v[196:199], v186 offset:33792
	ds_read_b128 v[200:203], v186 offset:34816
	ds_read_b128 v[204:207], v186 offset:35840
	ds_read_b128 v[208:211], v186 offset:36864
	ds_read_b128 v[212:215], v186 offset:37888
	ds_read_b128 v[216:219], v186 offset:38912
	ds_read_b128 v[220:223], v186 offset:39936
	global_load_lds_dwordx4 v[224:225], off
	v_lshl_add_u64 v[224:225], s[40:41], 0, v[164:165]
	s_mov_b32 m0, s62
	s_nop 0
	global_load_lds_dwordx4 v[224:225], off
	s_waitcnt vmcnt(8)
	s_waitcnt lgkmcnt(0)
	s_barrier
	s_waitcnt lgkmcnt(0)
	v_mfma_f32_16x16x128_f8f6f4 v[156:159], v[16:23], v[192:199], v[156:159]
	v_mfma_f32_16x16x128_f8f6f4 v[152:155], v[24:31], v[192:199], v[152:155]
	v_mfma_f32_16x16x128_f8f6f4 v[148:151], v[16:23], v[200:207], v[148:151]
	v_mfma_f32_16x16x128_f8f6f4 v[144:147], v[24:31], v[200:207], v[144:147]
	v_mfma_f32_16x16x128_f8f6f4 v[140:143], v[16:23], v[208:215], v[140:143]
	v_mfma_f32_16x16x128_f8f6f4 v[136:139], v[24:31], v[208:215], v[136:139]
	v_mfma_f32_16x16x128_f8f6f4 v[132:135], v[16:23], v[216:223], v[132:135]
	v_mfma_f32_16x16x128_f8f6f4 v[128:131], v[24:31], v[216:223], v[128:131]
	v_mfma_f32_16x16x128_f8f6f4 v[124:127], v[0:7], v[192:199], v[124:127]
	v_mfma_f32_16x16x128_f8f6f4 v[120:123], v[176:183], v[192:199], v[120:123]
	v_mfma_f32_16x16x128_f8f6f4 v[116:119], v[0:7], v[200:207], v[116:119]
	v_mfma_f32_16x16x128_f8f6f4 v[112:115], v[176:183], v[200:207], v[112:115]
	v_mfma_f32_16x16x128_f8f6f4 v[108:111], v[0:7], v[208:215], v[108:111]
	v_mfma_f32_16x16x128_f8f6f4 v[104:107], v[176:183], v[208:215], v[104:107]
	v_mfma_f32_16x16x128_f8f6f4 v[100:103], v[0:7], v[216:223], v[100:103]
	v_mfma_f32_16x16x128_f8f6f4 v[96:99], v[176:183], v[216:223], v[96:99]
	s_barrier
	s_mov_b32 m0, s86
	v_lshl_add_u64 v[8:9], v[8:9], 0, s[22:23]
	s_add_u32 s38, s38, 0x70080
	ds_read_b128 v[192:195], v186 offset:49152
	ds_read_b128 v[196:199], v186 offset:50176
	ds_read_b128 v[200:203], v186 offset:51200
	ds_read_b128 v[204:207], v186 offset:52224
	ds_read_b128 v[208:211], v186 offset:53248
	ds_read_b128 v[212:215], v186 offset:54272
	ds_read_b128 v[216:219], v186 offset:55296
	ds_read_b128 v[220:223], v186 offset:56320
	global_load_lds_dwordx4 v[8:9], off
	v_lshl_add_u64 v[8:9], v[10:11], 0, s[22:23]
	s_mov_b32 m0, s87
	s_addc_u32 s39, s39, 0
	global_load_lds_dwordx4 v[8:9], off
	v_lshl_add_u64 v[8:9], s[38:39], 0, v[162:163]
	s_mov_b32 m0, s88
	s_nop 0
	global_load_lds_dwordx4 v[8:9], off
	v_lshl_add_u64 v[8:9], s[38:39], 0, v[166:167]
	s_mov_b32 m0, s89
	s_nop 0
	global_load_lds_dwordx4 v[8:9], off
	v_lshl_add_u64 v[8:9], v[12:13], 0, s[22:23]
	s_mov_b32 m0, s63
	s_nop 0
	global_load_lds_dwordx4 v[8:9], off
	v_lshl_add_u64 v[8:9], v[14:15], 0, s[22:23]
	s_mov_b32 m0, s64
	s_nop 0
	global_load_lds_dwordx4 v[8:9], off
	s_waitcnt vmcnt(8)
	s_waitcnt lgkmcnt(0)
	s_barrier
	s_waitcnt lgkmcnt(0)
	v_mfma_f32_16x16x128_f8f6f4 v[92:95], v[16:23], v[192:199], v[92:95]
	v_mfma_f32_16x16x128_f8f6f4 v[88:91], v[24:31], v[192:199], v[88:91]
	v_mfma_f32_16x16x128_f8f6f4 v[84:87], v[16:23], v[200:207], v[84:87]
	v_mfma_f32_16x16x128_f8f6f4 v[80:83], v[24:31], v[200:207], v[80:83]
	v_mfma_f32_16x16x128_f8f6f4 v[76:79], v[16:23], v[208:215], v[76:79]
	v_mfma_f32_16x16x128_f8f6f4 v[72:75], v[24:31], v[208:215], v[72:75]
	v_mfma_f32_16x16x128_f8f6f4 v[68:71], v[16:23], v[216:223], v[68:71]
	v_mfma_f32_16x16x128_f8f6f4 v[64:67], v[24:31], v[216:223], v[64:67]
	v_mfma_f32_16x16x128_f8f6f4 v[60:63], v[0:7], v[192:199], v[60:63]
	v_mfma_f32_16x16x128_f8f6f4 v[56:59], v[176:183], v[192:199], v[56:59]
	v_mfma_f32_16x16x128_f8f6f4 v[52:55], v[0:7], v[200:207], v[52:55]
	v_mfma_f32_16x16x128_f8f6f4 v[48:51], v[176:183], v[200:207], v[48:51]
	v_mfma_f32_16x16x128_f8f6f4 v[44:47], v[0:7], v[208:215], v[44:47]
	v_mfma_f32_16x16x128_f8f6f4 v[40:43], v[176:183], v[208:215], v[40:43]
	v_mfma_f32_16x16x128_f8f6f4 v[36:39], v[0:7], v[216:223], v[36:39]
	v_mfma_f32_16x16x128_f8f6f4 v[32:35], v[176:183], v[216:223], v[32:35]
	s_barrier
	s_add_i32 s92, s92, 2
	s_add_u32 s36, s36, 0x100
	s_addc_u32 s37, s37, 0
	s_add_u32 s90, s90, 0x100
	s_addc_u32 s91, s91, 0
	s_cmp_gt_u32 s92, 25
	s_cbranch_scc0 .LBB0_1853
	s_and_b64 vcc, exec, s[12:13]
	s_cbranch_vccz .LBB0_1856
	s_barrier

; #define PG8_STAGE(bufoff, gbase, voff) do { _Pragma("unroll") for (int _i = 0; _i < 2; ++_i) \
;         __builtin_amdgcn_global_load_lds((const unsigned*)((const char*)(gbase) + (voff)[_i]), (PG8_LAS unsigned*)(lds + (bufoff) + ldsw + _i * 8192), 16, 0, 0); } while (0)
; #define PG8_WAIT_V(n) asm volatile("s_waitcnt vmcnt(" #n ")" ::: "memory")
; #define PG8_WAIT_L(n) asm volatile("s_waitcnt lgkmcnt(" #n ")" ::: "memory")
; #define PG8_BAR __builtin_amdgcn_s_barrier()
; #define PG8_SCHED __builtin_amdgcn_sched_barrier(0)
; template <class Epi, class Sched, bool ALIGN_EPI = false, bool SP2 = false, bool FP8 = false, bool PEEL = false>
; __device__ __forceinline__ void gemm_phase(PG8_LAS unsigned char* lds, const Gemm g, const Sched& S, const Epi& E, const int wid) {
;     ...
;         for (int t = 0; t < nt; t += 2) {
;             const bool last = (t == nt - 2);
;             const char* a1 = cA + (size_t)(t + 1) * kstep;
;             const char* a2 = last ? nA : cA + (size_t)(t + 2) * kstep; const char* b2 = last ? nB : cB + (size_t)(t + 2) * kstep;
;             const char* a3 = a2 + kstep; const char* b3 = b2 + kstep;
;             if (last && has_next) S.a_ready(nxt);
;             PG8_LDB(B0, 0, 0); PG8_LDB(B1, 0, 1); PG8_SCHED; PG8_LDA(At, 0, 0); PG8_STAGE(PG8_SA(1, 1), a1 + hstep, voffA);
;             PG8_WAIT_V(8); PG8_WAIT_L(0); PG8_BAR; PG8_MMA(0, 0, At, B0); PG8_MMA(0, 1, At, B1); PG8_BAR; PG8_SCHED;
;             PG8_LDA(At, 0, 1); PG8_STAGE(PG8_SB(0, 0), b2, voffB); PG8_STAGE(PG8_SB(0, 1), b2 + hstep, voffB); PG8_STAGE(PG8_SA(0, 0), a2, voffA);
;             PG8_WAIT_V(8); PG8_WAIT_L(0); PG8_BAR; PG8_MMA(1, 0, At, B0); PG8_MMA(1, 1, At, B1); PG8_BAR; PG8_SCHED;
;             PG8_LDB(B0, 1, 0); PG8_LDB(B1, 1, 1); PG8_SCHED; PG8_LDA(At, 1, 0); PG8_STAGE(PG8_SA(0, 1), a2 + hstep, voffA);
;             PG8_WAIT_V(8); PG8_WAIT_L(0); PG8_BAR; PG8_MMA(0, 0, At, B0); PG8_MMA(0, 1, At, B1); PG8_BAR; PG8_SCHED;
.LBB0_1873:
	s_add_u32 s25, s26, s42
	s_addc_u32 s37, s27, s43
	s_add_u32 s46, s25, 0x100
	s_addc_u32 s47, s37, 0
	s_and_b64 s[44:45], s[40:41], exec
	s_cselect_b32 s45, s9, s47
	s_cselect_b32 s44, s8, s46
	s_add_u32 s42, s34, s42
	s_addc_u32 s43, s35, s43
	s_add_u32 s42, s42, 0x100
	s_addc_u32 s43, s43, 0
	s_and_b64 s[40:41], s[40:41], exec
	s_cselect_b32 s47, s31, s43
	s_cselect_b32 s46, s30, s42
	s_add_u32 s50, s25, 0x70080
	ds_read_b128 v[16:19], v183
	ds_read_b128 v[20:23], v183 offset:1024
	ds_read_b128 v[24:27], v183 offset:2048
	ds_read_b128 v[28:31], v183 offset:3072
	ds_read_b128 v[0:3], v184
	ds_read_b128 v[4:7], v184 offset:1024
	ds_read_b128 v[8:11], v184 offset:2048
	ds_read_b128 v[12:15], v184 offset:3072
	s_addc_u32 s51, s37, 0
	s_add_i32 s92, s67, s54
	s_add_i32 m0, s59, 0xc000
	s_add_i32 s93, s59, 0xe000
	s_add_i32 s89, s92, 0x2000
	s_add_u32 s48, s46, 0x70000
	s_addc_u32 s49, s47, 0
	s_add_i32 s91, s74, s54
	s_add_i32 s90, s91, 0x2000
	s_add_i32 s88, 0, 0x18000
	s_add_i32 s87, 0, 0x1c000
	s_add_u32 s42, s44, 0x70000
	s_addc_u32 s43, s45, 0
	s_add_i32 s86, s88, s54
	s_add_i32 s37, s86, 0x2000
	s_add_u32 s40, s46, 0x70080
	s_addc_u32 s41, s47, 0
	s_add_i32 s85, s87, s54
	s_add_i32 s25, s85, 0x2000
	v_lshl_add_u64 v[210:211], s[50:51], 0, v[166:167]
	ds_read_b128 v[174:177], v185
	ds_read_b128 v[178:181], v185 offset:1024
	ds_read_b128 v[186:189], v185 offset:2048
	ds_read_b128 v[190:193], v185 offset:3072
	ds_read_b128 v[194:197], v185 offset:4096
	ds_read_b128 v[198:201], v185 offset:5120
	ds_read_b128 v[202:205], v185 offset:6144
	ds_read_b128 v[206:209], v185 offset:7168
	global_load_lds_dwordx4 v[210:211], off
	v_lshl_add_u64 v[210:211], s[50:51], 0, v[162:163]
	s_mov_b32 m0, s93
	s_nop 0
	global_load_lds_dwordx4 v[210:211], off
	s_waitcnt vmcnt(8)
	s_waitcnt lgkmcnt(0)
	s_barrier
	s_waitcnt lgkmcnt(0)
	v_mfma_f32_16x16x128_f8f6f4 v[156:159], v[16:23], v[174:181], v[156:159]
	v_mfma_f32_16x16x128_f8f6f4 v[152:155], v[24:31], v[174:181], v[152:155]
	v_mfma_f32_16x16x128_f8f6f4 v[148:151], v[16:23], v[186:193], v[148:151]
	v_mfma_f32_16x16x128_f8f6f4 v[140:143], v[24:31], v[186:193], v[140:143]
	v_mfma_f32_16x16x128_f8f6f4 v[132:135], v[16:23], v[194:201], v[132:135]
	v_mfma_f32_16x16x128_f8f6f4 v[124:127], v[24:31], v[194:201], v[124:127]
	v_mfma_f32_16x16x128_f8f6f4 v[116:119], v[16:23], v[202:209], v[116:119]
	v_mfma_f32_16x16x128_f8f6f4 v[108:111], v[24:31], v[202:209], v[108:111]
	v_mfma_f32_16x16x128_f8f6f4 v[144:147], v[0:7], v[174:181], v[144:147]
	v_mfma_f32_16x16x128_f8f6f4 v[136:139], v[8:15], v[174:181], v[136:139]
	v_mfma_f32_16x16x128_f8f6f4 v[128:131], v[0:7], v[186:193], v[128:131]
	v_mfma_f32_16x16x128_f8f6f4 v[120:123], v[8:15], v[186:193], v[120:123]
	v_mfma_f32_16x16x128_f8f6f4 v[112:115], v[0:7], v[194:201], v[112:115]
	v_mfma_f32_16x16x128_f8f6f4 v[104:107], v[8:15], v[194:201], v[104:107]
	v_mfma_f32_16x16x128_f8f6f4 v[100:103], v[0:7], v[202:209], v[100:103]
	v_mfma_f32_16x16x128_f8f6f4 v[96:99], v[8:15], v[202:209], v[96:99]
	s_barrier
	s_mov_b32 m0, s92
	v_lshl_add_u64 v[174:175], s[46:47], 0, v[164:165]
	ds_read_b128 v[186:189], v185 offset:16384
	ds_read_b128 v[190:193], v185 offset:17408
	ds_read_b128 v[194:197], v185 offset:18432
	ds_read_b128 v[198:201], v185 offset:19456
	ds_read_b128 v[202:205], v185 offset:20480
	ds_read_b128 v[206:209], v185 offset:21504
	ds_read_b128 v[210:213], v185 offset:22528
	ds_read_b128 v[214:217], v185 offset:23552
	global_load_lds_dwordx4 v[174:175], off
	v_lshl_add_u64 v[176:177], s[46:47], 0, v[160:161]
	s_mov_b32 m0, s89
	v_lshl_add_u64 v[178:179], s[48:49], 0, v[164:165]
	global_load_lds_dwordx4 v[176:177], off
	s_mov_b32 m0, s91
	v_lshl_add_u64 v[180:181], s[44:45], 0, v[162:163]
	global_load_lds_dwordx4 v[178:179], off
	v_lshl_add_u64 v[178:179], s[48:49], 0, v[160:161]
	s_mov_b32 m0, s90
	s_nop 0
	global_load_lds_dwordx4 v[178:179], off
	v_lshl_add_u64 v[178:179], s[44:45], 0, v[166:167]
	s_mov_b32 m0, s59
	s_nop 0
	global_load_lds_dwordx4 v[178:179], off
	s_mov_b32 m0, s60
	s_nop 0
	global_load_lds_dwordx4 v[180:181], off
	s_waitcnt vmcnt(8)
	s_waitcnt lgkmcnt(0)
	s_barrier
	s_waitcnt lgkmcnt(0)
	v_mfma_f32_16x16x128_f8f6f4 v[92:95], v[16:23], v[186:193], v[92:95]
	v_mfma_f32_16x16x128_f8f6f4 v[88:91], v[24:31], v[186:193], v[88:91]
	v_mfma_f32_16x16x128_f8f6f4 v[84:87], v[16:23], v[194:201], v[84:87]
	v_mfma_f32_16x16x128_f8f6f4 v[76:79], v[24:31], v[194:201], v[76:79]
	v_mfma_f32_16x16x128_f8f6f4 v[68:71], v[16:23], v[202:209], v[68:71]
	v_mfma_f32_16x16x128_f8f6f4 v[60:63], v[24:31], v[202:209], v[60:63]
	v_mfma_f32_16x16x128_f8f6f4 v[52:55], v[16:23], v[210:217], v[52:55]
	v_mfma_f32_16x16x128_f8f6f4 v[44:47], v[24:31], v[210:217], v[44:47]
	v_mfma_f32_16x16x128_f8f6f4 v[80:83], v[0:7], v[186:193], v[80:83]
	v_mfma_f32_16x16x128_f8f6f4 v[72:75], v[8:15], v[186:193], v[72:75]
	v_mfma_f32_16x16x128_f8f6f4 v[64:67], v[0:7], v[194:201], v[64:67]
	v_mfma_f32_16x16x128_f8f6f4 v[56:59], v[8:15], v[194:201], v[56:59]
	v_mfma_f32_16x16x128_f8f6f4 v[48:51], v[0:7], v[202:209], v[48:51]
	v_mfma_f32_16x16x128_f8f6f4 v[40:43], v[8:15], v[202:209], v[40:43]
	v_mfma_f32_16x16x128_f8f6f4 v[36:39], v[0:7], v[210:217], v[36:39]
	v_mfma_f32_16x16x128_f8f6f4 v[32:35], v[8:15], v[210:217], v[32:35]
	s_barrier
; #define PG8_STAGE(bufoff, gbase, voff) do { _Pragma("unroll") for (int _i = 0; _i < 2; ++_i) \
;         __builtin_amdgcn_global_load_lds((const unsigned*)((const char*)(gbase) + (voff)[_i]), (PG8_LAS unsigned*)(lds + (bufoff) + ldsw + _i * 8192), 16, 0, 0); } while (0)
; #define PG8_WAIT_V(n) asm volatile("s_waitcnt vmcnt(" #n ")" ::: "memory")
; #define PG8_WAIT_L(n) asm volatile("s_waitcnt lgkmcnt(" #n ")" ::: "memory")
; #define PG8_BAR __builtin_amdgcn_s_barrier()
; #define PG8_SCHED __builtin_amdgcn_sched_barrier(0)
; template <class Epi, class Sched, bool ALIGN_EPI = false, bool SP2 = false, bool FP8 = false, bool PEEL = false>
; __device__ __forceinline__ void gemm_phase(PG8_LAS unsigned char* lds, const Gemm g, const Sched& S, const Epi& E, const int wid) {
;     ...
;             PG8_LDB(B0, 1, 0); PG8_LDB(B1, 1, 1); PG8_SCHED; PG8_LDA(At, 1, 0); PG8_STAGE(PG8_SA(0, 1), a2 + hstep, voffA);
;             PG8_WAIT_V(8); PG8_WAIT_L(0); PG8_BAR; PG8_MMA(0, 0, At, B0); PG8_MMA(0, 1, At, B1); PG8_BAR; PG8_SCHED;
;             PG8_LDA(At, 1, 1); PG8_STAGE(PG8_SB(1, 0), b3, voffB); PG8_STAGE(PG8_SB(1, 1), b3 + hstep, voffB); PG8_STAGE(PG8_SA(1, 0), a3, voffA);
;             PG8_WAIT_V(8); PG8_WAIT_L(0); PG8_BAR; PG8_MMA(1, 0, At, B0); PG8_MMA(1, 1, At, B1); PG8_BAR; PG8_SCHED;
;         }
;     ...
;         if constexpr (ALIGN_EPI) { if (wr == 0) PG8_BAR; }
	v_add_u32_e32 v12, s88, v182
	v_add_u32_e32 v28, s87, v182
	ds_read_b128 v[0:3], v12
	ds_read_b128 v[4:7], v12 offset:1024
	ds_read_b128 v[8:11], v12 offset:2048
	ds_read_b128 v[12:15], v12 offset:3072
	ds_read_b128 v[16:19], v28
	ds_read_b128 v[20:23], v28 offset:1024
	ds_read_b128 v[24:27], v28 offset:2048
	ds_read_b128 v[28:31], v28 offset:3072
	s_mov_b32 m0, s61
	v_lshl_add_u64 v[218:219], s[42:43], 0, v[166:167]
	ds_read_b128 v[186:189], v185 offset:32768
	ds_read_b128 v[190:193], v185 offset:33792
	ds_read_b128 v[194:197], v185 offset:34816
	ds_read_b128 v[198:201], v185 offset:35840
	ds_read_b128 v[202:205], v185 offset:36864
	ds_read_b128 v[206:209], v185 offset:37888
	ds_read_b128 v[210:213], v185 offset:38912
	ds_read_b128 v[214:217], v185 offset:39936
	global_load_lds_dwordx4 v[218:219], off
	v_lshl_add_u64 v[218:219], s[42:43], 0, v[162:163]
	s_mov_b32 m0, s62
	s_nop 0
	global_load_lds_dwordx4 v[218:219], off
	s_waitcnt vmcnt(8)
	s_waitcnt lgkmcnt(0)
	s_barrier
	s_waitcnt lgkmcnt(0)
	v_mfma_f32_16x16x128_f8f6f4 v[156:159], v[0:7], v[186:193], v[156:159]
	v_mfma_f32_16x16x128_f8f6f4 v[152:155], v[8:15], v[186:193], v[152:155]
	v_mfma_f32_16x16x128_f8f6f4 v[148:151], v[0:7], v[194:201], v[148:151]
	v_mfma_f32_16x16x128_f8f6f4 v[140:143], v[8:15], v[194:201], v[140:143]
	v_mfma_f32_16x16x128_f8f6f4 v[132:135], v[0:7], v[202:209], v[132:135]
	v_mfma_f32_16x16x128_f8f6f4 v[124:127], v[8:15], v[202:209], v[124:127]
	v_mfma_f32_16x16x128_f8f6f4 v[116:119], v[0:7], v[210:217], v[116:119]
	v_mfma_f32_16x16x128_f8f6f4 v[108:111], v[8:15], v[210:217], v[108:111]
	v_mfma_f32_16x16x128_f8f6f4 v[144:147], v[16:23], v[186:193], v[144:147]
	v_mfma_f32_16x16x128_f8f6f4 v[136:139], v[24:31], v[186:193], v[136:139]
	v_mfma_f32_16x16x128_f8f6f4 v[128:131], v[16:23], v[194:201], v[128:131]
	v_mfma_f32_16x16x128_f8f6f4 v[120:123], v[24:31], v[194:201], v[120:123]
	v_mfma_f32_16x16x128_f8f6f4 v[112:115], v[16:23], v[202:209], v[112:115]
	v_mfma_f32_16x16x128_f8f6f4 v[104:107], v[24:31], v[202:209], v[104:107]
	v_mfma_f32_16x16x128_f8f6f4 v[100:103], v[16:23], v[210:217], v[100:103]
	v_mfma_f32_16x16x128_f8f6f4 v[96:99], v[24:31], v[210:217], v[96:99]
	s_barrier
	s_mov_b32 m0, s86
	v_lshl_add_u64 v[174:175], v[174:175], 0, s[14:15]
	ds_read_b128 v[186:189], v185 offset:49152
	ds_read_b128 v[190:193], v185 offset:50176
	ds_read_b128 v[194:197], v185 offset:51200
	ds_read_b128 v[198:201], v185 offset:52224
	ds_read_b128 v[202:205], v185 offset:53248
	ds_read_b128 v[206:209], v185 offset:54272
	ds_read_b128 v[210:213], v185 offset:55296
	ds_read_b128 v[214:217], v185 offset:56320
	global_load_lds_dwordx4 v[174:175], off
	v_lshl_add_u64 v[174:175], v[176:177], 0, s[14:15]
	s_mov_b32 m0, s37
	s_nop 0
	global_load_lds_dwordx4 v[174:175], off
	v_lshl_add_u64 v[174:175], s[40:41], 0, v[164:165]
	s_mov_b32 m0, s85
	s_nop 0
	global_load_lds_dwordx4 v[174:175], off
	v_lshl_add_u64 v[174:175], s[40:41], 0, v[160:161]
	s_mov_b32 m0, s25
	s_nop 0
	global_load_lds_dwordx4 v[174:175], off
	v_lshl_add_u64 v[174:175], v[178:179], 0, s[14:15]
	s_mov_b32 m0, s65
	s_nop 0
	global_load_lds_dwordx4 v[174:175], off
	v_lshl_add_u64 v[174:175], v[180:181], 0, s[14:15]
	s_mov_b32 m0, s66
	s_nop 0
	global_load_lds_dwordx4 v[174:175], off
	s_waitcnt vmcnt(8)
	s_waitcnt lgkmcnt(0)
	s_barrier
	s_waitcnt lgkmcnt(0)
	v_mfma_f32_16x16x128_f8f6f4 v[92:95], v[0:7], v[186:193], v[92:95]
	v_mfma_f32_16x16x128_f8f6f4 v[88:91], v[8:15], v[186:193], v[88:91]
	v_mfma_f32_16x16x128_f8f6f4 v[84:87], v[0:7], v[194:201], v[84:87]
	v_mfma_f32_16x16x128_f8f6f4 v[76:79], v[8:15], v[194:201], v[76:79]
	v_mfma_f32_16x16x128_f8f6f4 v[68:71], v[0:7], v[202:209], v[68:71]
	v_mfma_f32_16x16x128_f8f6f4 v[60:63], v[8:15], v[202:209], v[60:63]
	v_mfma_f32_16x16x128_f8f6f4 v[52:55], v[0:7], v[210:217], v[52:55]
	v_mfma_f32_16x16x128_f8f6f4 v[44:47], v[8:15], v[210:217], v[44:47]
	v_mfma_f32_16x16x128_f8f6f4 v[80:83], v[16:23], v[186:193], v[80:83]
	v_mfma_f32_16x16x128_f8f6f4 v[72:75], v[24:31], v[186:193], v[72:75]
	v_mfma_f32_16x16x128_f8f6f4 v[64:67], v[16:23], v[194:201], v[64:67]
	v_mfma_f32_16x16x128_f8f6f4 v[56:59], v[24:31], v[194:201], v[56:59]
	v_mfma_f32_16x16x128_f8f6f4 v[48:51], v[16:23], v[202:209], v[48:51]
	v_mfma_f32_16x16x128_f8f6f4 v[40:43], v[24:31], v[202:209], v[40:43]
	v_mfma_f32_16x16x128_f8f6f4 v[36:39], v[16:23], v[210:217], v[36:39]
	v_mfma_f32_16x16x128_f8f6f4 v[32:35], v[24:31], v[210:217], v[32:35]
	s_barrier
	s_andn2_b64 vcc, exec, s[38:39]
	s_mov_b64 s[40:41], -1
	s_mov_b64 s[38:39], 0
	s_mov_b64 s[42:43], 0x100
	s_cbranch_vccz .LBB0_1873
	s_and_b64 vcc, exec, s[12:13]
	s_cbranch_vccz .LBB0_1876
	s_barrier
